# GEMM: last row piece (k beyond 1432) clamps unneeded lanes onto the last needed 16 B so lines past the row end are not fetched
# speedup vs baseline: 1.0246x; 1.0058x over previous
_Z6k_gemmPKfPKDv8_DF16_S0_S0_PDF16_:
	s_load_dwordx2 s[8:9], s[0:1], 0x0
	s_load_dwordx2 s[10:11], s[0:1], 0x10
	s_load_dwordx2 s[12:13], s[0:1], 0x8
	s_load_dwordx4 s[4:7], s[0:1], 0x18
	s_mul_i32 s14, s2, 0xc4
	v_lshrrev_b32_e32 v1, 5, v0
	v_and_b32_e32 v89, 31, v0
	v_add_u32_e32 v2, s14, v1
	v_lshlrev_b32_e32 v154, 4, v89
	s_movk_i32 s15, 0x1664
	v_mad_u64_u32 v[150:151], s[0:1], v2, s15, v[154:155]
	s_lshl_b32 s16, s2, 2
	v_mul_u32_u24_e32 v245, 25, v1
	v_add_u32_e32 v245, s16, v245
	v_and_b32_e32 v245, 31, v245
	v_xor_b32_e32 v246, 16, v245
	v_lshlrev_b32_e32 v247, 2, v246
	v_sub_u32_e32 v244, v150, v247
	v_lshlrev_b32_e32 v247, 2, v245
	v_sub_u32_e32 v150, v150, v247
	v_add_u32_e32 v247, 24, v245
	v_lshrrev_b32_e32 v247, 2, v247
	v_sub_u32_e32 v247, v89, v247
	v_max_i32_e32 v247, 0, v247
	v_lshlrev_b32_e32 v247, 4, v247
	v_sub_u32_e32 v250, v150, v247
	v_add_u32_e32 v247, 24, v246
	v_lshrrev_b32_e32 v247, 2, v247
	v_sub_u32_e32 v247, v89, v247
	v_max_i32_e32 v247, 0, v247
	v_lshlrev_b32_e32 v247, 4, v247
	v_sub_u32_e32 v251, v244, v247
	s_movk_i32 s17, 0x1ee0
	v_mul_u32_u24_e32 v242, s17, v1
	v_add_u32_e32 v243, 0xffffff00, v242
	v_lshl_add_u32 v247, v89, 3, v242
	v_lshlrev_b32_e32 v248, 1, v245
	v_sub_u32_e32 v248, v247, v248
	v_add_u32_e32 v234, 64, v248
	v_add_u32_e32 v235, 0x42, v248
	v_add_u32_e32 v236, 0x44, v248
	v_add_u32_e32 v237, 0x46, v248
	v_lshlrev_b32_e32 v248, 1, v246
	v_sub_u32_e32 v248, v247, v248
	v_add_u32_e32 v238, 64, v248
	v_add_u32_e32 v239, 0x42, v248
	v_add_u32_e32 v240, 0x44, v248
	v_add_u32_e32 v241, 0x46, v248
	v_and_b32_e32 v247, 7, v89
	v_lshl_add_u32 v247, v247, 3, v242
	v_mov_b32_e32 v248, 0
	v_mov_b32_e32 v249, 0
	ds_write_b64 v247, v[248:249] offset:0
	ds_write_b64 v247, v[248:249] offset:608
	ds_write_b64 v247, v[248:249] offset:1216
	ds_write_b64 v247, v[248:249] offset:1824
	ds_write_b64 v247, v[248:249] offset:2432
	ds_write_b64 v247, v[248:249] offset:3040
	ds_write_b64 v247, v[248:249] offset:3648
	ds_write_b64 v247, v[248:249] offset:4256
	ds_write_b64 v247, v[248:249] offset:4864
	ds_write_b64 v247, v[248:249] offset:5472
	ds_write_b64 v247, v[248:249] offset:6080
	ds_write_b64 v247, v[248:249] offset:6688
	ds_write_b64 v247, v[248:249] offset:7296
	v_mov_b32_e32 v2, 2
	v_lshlrev_b32_sdwa v2, v2, v0 dst_sel:DWORD dst_unused:UNUSED_PAD src0_sel:DWORD src1_sel:BYTE_0
	v_mov_b32_e32 v3, 0
	s_waitcnt lgkmcnt(0)
	v_lshl_add_u64 v[4:5], s[4:5], 0, v[2:3]
	s_mov_b32 s0, 0x166000
	v_add_co_u32_e32 v4, vcc, s0, v4
	v_add_u32_e32 v6, 0x111514dc, v154
	s_nop 0
	v_addc_co_u32_e32 v5, vcc, 0, v5, vcc
	global_load_dword v90, v[4:5], off
	v_add_u32_e32 v4, 0x16640, v244
	v_min_u32_e32 v2, v150, v6
	v_min_u32_e32 v4, v4, v6
	global_load_dwordx4 v[82:85], v2, s[8:9] nt
	global_load_dwordx4 v[78:81], v4, s[8:9] nt
	v_add_u32_e32 v2, 0x2cc80, v150
	v_min_u32_e32 v2, v2, v6
	v_add_u32_e32 v4, 0x432c0, v244
	v_min_u32_e32 v4, v4, v6
	global_load_dwordx4 v[74:77], v2, s[8:9] nt
	global_load_dwordx4 v[70:73], v4, s[8:9] nt
	v_add_u32_e32 v2, 0x59900, v150
	v_min_u32_e32 v2, v2, v6
	v_add_u32_e32 v4, 0x6ff40, v244
	v_min_u32_e32 v4, v4, v6
	global_load_dwordx4 v[66:69], v2, s[8:9] nt
	global_load_dwordx4 v[54:57], v4, s[8:9] nt
	v_add_u32_e32 v2, 0x86580, v150
	v_min_u32_e32 v2, v2, v6
	v_add_u32_e32 v4, 0x9cbc0, v244
	v_min_u32_e32 v4, v4, v6
	global_load_dwordx4 v[62:65], v2, s[8:9] nt
	global_load_dwordx4 v[58:61], v4, s[8:9] nt
	v_add_u32_e32 v2, 0xb3200, v150
	v_min_u32_e32 v2, v2, v6
	v_add_u32_e32 v4, 0xc9840, v244
	v_min_u32_e32 v4, v4, v6
	global_load_dwordx4 v[46:49], v2, s[8:9] nt
	global_load_dwordx4 v[38:41], v4, s[8:9] nt
	v_add_u32_e32 v2, 0xdfe80, v150
	v_min_u32_e32 v2, v2, v6
	v_add_u32_e32 v4, 0xf64c0, v244
	s_movk_i32 s3, 0xc4
	v_or_b32_e32 v7, 0xc0, v1
	v_min_u32_e32 v4, v4, v6
	global_load_dwordx4 v[34:37], v2, s[8:9] nt
	global_load_dwordx4 v[14:17], v4, s[8:9] nt
	v_add_u32_e32 v2, 0x10cb00, v150
	v_min_u32_e32 v2, v2, v6
	v_cmp_gt_u32_e64 s[0:1], s3, v7
	v_bfe_u32 v87, v0, 4, 2
	v_and_b32_e32 v86, 15, v0
	v_cndmask_b32_e64 v2, 0, v2, s[0:1]
	global_load_dwordx4 v[10:13], v2, s[8:9] nt
	v_lshlrev_b32_e32 v2, 12, v87
	v_lshl_add_u64 v[4:5], s[12:13], 0, v[2:3]
	v_lshlrev_b32_e32 v2, 3, v0
	v_and_b32_e32 v2, 0xe00, v2
	v_lshl_add_u64 v[4:5], v[4:5], 0, v[2:3]
	v_lshlrev_b32_e32 v2, 4, v86
	v_lshl_add_u64 v[152:153], v[4:5], 0, v[2:3]
	s_movk_i32 s2, 0x4000
	v_add_co_u32_e32 v2, vcc, s2, v152
	s_mov_b32 s2, 0x8000
	s_nop 0
	v_addc_co_u32_e32 v3, vcc, 0, v153, vcc
	global_load_dwordx4 v[26:29], v[152:153], off sc1
	global_load_dwordx4 v[50:53], v[152:153], off offset:256 sc1
	global_load_dwordx4 v[18:21], v[2:3], off sc1
	global_load_dwordx4 v[42:45], v[2:3], off offset:256 sc1
	v_add_co_u32_e32 v2, vcc, s2, v152
	s_movk_i32 s2, 0xd0
	s_nop 0
	v_addc_co_u32_e32 v3, vcc, 0, v153, vcc
	v_add_co_u32_e32 v92, vcc, 0xc000, v152
	global_load_dwordx4 v[22:25], v[2:3], off sc1
	global_load_dwordx4 v[30:33], v[2:3], off offset:256 sc1
	v_addc_co_u32_e32 v93, vcc, 0, v153, vcc
	global_load_dwordx4 v[6:9], v[92:93], off sc1
	global_load_dwordx4 v[2:5], v[92:93], off offset:256 sc1
	v_cmp_gt_u32_e32 vcc, s2, v0
	v_add_u32_e32 v88, 0x111516dc, v154
	s_and_saveexec_b64 s[4:5], vcc
	s_cbranch_execz .LBB2_5
	v_cndmask_b32_e32 v91, 0, v0, vcc
	v_cmp_gt_u32_e32 vcc, s3, v91
	v_add_u32_e32 v91, s14, v91
	s_mov_b32 s2, 0xc350
	v_cmp_gt_i32_e64 s[2:3], s2, v91
	v_ashrrev_i32_e32 v92, 31, v91
	s_and_b64 s[2:3], vcc, s[2:3]
	v_cndmask_b32_e64 v93, 0, v92, s[2:3]
	v_mov_b32_e32 v92, 0xc34f
	v_cndmask_b32_e64 v92, v92, v91, s[2:3]
	v_mov_b64_e32 v[94:95], s[8:9]
	v_mad_i64_i32 v[94:95], s[12:13], v92, s15, v[94:95]
	v_add_co_u32_e32 v94, vcc, 0x1000, v94
	v_lshl_add_u64 v[92:93], v[92:93], 2, s[10:11]
	s_nop 0
	v_addc_co_u32_e32 v95, vcc, 0, v95, vcc
	global_load_dword v91, v[92:93], off
	global_load_dword v96, v[94:95], off offset:1632
	v_mov_b32_e32 v94, 0x1ee00
	s_waitcnt vmcnt(1)
	v_cndmask_b32_e64 v93, 0, v91, s[2:3]
	s_waitcnt vmcnt(0)
	v_cndmask_b32_e64 v92, 0, v96, s[2:3]
	v_lshl_add_u32 v91, v0, 3, v94
	ds_write_b64 v91, v[92:93]

.LBB2_7:
	s_or_b64 exec, exec, s[2:3]
	s_waitcnt vmcnt(21)
	v_add_u32_e32 v90, 0x200, v150
	v_min_u32_e32 v90, v90, v88
	global_load_dwordx4 v[110:113], v90, s[8:9] nt
	v_mul_u32_u24_e32 v1, 0x120, v1
	s_waitcnt vmcnt(21)
	v_cvt_pk_f16_f32 v85, v84, v85
	v_cvt_pk_f16_f32 v84, v82, v83
	v_lshl_add_u32 v1, v89, 3, v1
	s_movk_i32 s2, 0x120
	ds_write_b16 v234, v84 offset:0
	ds_write_b16_d16_hi v235, v84 offset:0
	ds_write_b16 v236, v85 offset:0
	ds_write_b16_d16_hi v237, v85 offset:0
	v_add_u32_e32 v82, 0x16840, v244
	v_min_u32_e32 v82, v82, v88
	global_load_dwordx4 v[114:117], v82, s[8:9] nt
	s_waitcnt vmcnt(21)
	v_cvt_pk_f16_f32 v81, v80, v81
	v_cvt_pk_f16_f32 v80, v78, v79
	ds_write_b16 v238, v80 offset:608
	ds_write_b16_d16_hi v239, v80 offset:608
	ds_write_b16 v240, v81 offset:608
	ds_write_b16_d16_hi v241, v81 offset:608
	v_add_u32_e32 v78, 0x2ce80, v150
	v_min_u32_e32 v78, v78, v88
	global_load_dwordx4 v[118:121], v78, s[8:9] nt
	s_waitcnt vmcnt(21)
	v_cvt_pk_f16_f32 v77, v76, v77
	v_cvt_pk_f16_f32 v76, v74, v75
	ds_write_b16 v234, v76 offset:1216
	ds_write_b16_d16_hi v235, v76 offset:1216
	ds_write_b16 v236, v77 offset:1216
	ds_write_b16_d16_hi v237, v77 offset:1216
	v_add_u32_e32 v74, 0x434c0, v244
	v_min_u32_e32 v74, v74, v88
	global_load_dwordx4 v[74:77], v74, s[8:9] nt
	s_waitcnt vmcnt(21)
	v_cvt_pk_f16_f32 v73, v72, v73
	v_cvt_pk_f16_f32 v72, v70, v71
	ds_write_b16 v238, v72 offset:1824
	ds_write_b16_d16_hi v239, v72 offset:1824
	ds_write_b16 v240, v73 offset:1824
	ds_write_b16_d16_hi v241, v73 offset:1824
	v_add_u32_e32 v70, 0x59b00, v150
	v_min_u32_e32 v70, v70, v88
	global_load_dwordx4 v[78:81], v70, s[8:9] nt
	s_waitcnt vmcnt(21)
	v_cvt_pk_f16_f32 v69, v68, v69
	v_cvt_pk_f16_f32 v68, v66, v67
	ds_write_b16 v234, v68 offset:2432
	ds_write_b16_d16_hi v235, v68 offset:2432
	ds_write_b16 v236, v69 offset:2432
	ds_write_b16_d16_hi v237, v69 offset:2432
	v_add_u32_e32 v66, 0x70140, v244
	v_min_u32_e32 v66, v66, v88
	global_load_dwordx4 v[82:85], v66, s[8:9] nt
	s_waitcnt vmcnt(21)
	v_cvt_pk_f16_f32 v57, v56, v57
	v_cvt_pk_f16_f32 v56, v54, v55
	ds_write_b16 v238, v56 offset:3040
	ds_write_b16_d16_hi v239, v56 offset:3040
	ds_write_b16 v240, v57 offset:3040
	ds_write_b16_d16_hi v241, v57 offset:3040
	v_add_u32_e32 v54, 0x86780, v150
	v_min_u32_e32 v54, v54, v88
	global_load_dwordx4 v[54:57], v54, s[8:9] nt
	s_waitcnt vmcnt(21)
	v_cvt_pk_f16_f32 v65, v64, v65
	v_cvt_pk_f16_f32 v64, v62, v63
	ds_write_b16 v234, v64 offset:3648
	ds_write_b16_d16_hi v235, v64 offset:3648
	ds_write_b16 v236, v65 offset:3648
	ds_write_b16_d16_hi v237, v65 offset:3648
	v_add_u32_e32 v62, 0x9cdc0, v244
	v_min_u32_e32 v62, v62, v88
	global_load_dwordx4 v[90:93], v62, s[8:9] nt
	s_waitcnt vmcnt(21)
	v_cvt_pk_f16_f32 v61, v60, v61
	v_cvt_pk_f16_f32 v60, v58, v59
	ds_write_b16 v238, v60 offset:4256
	ds_write_b16_d16_hi v239, v60 offset:4256
	ds_write_b16 v240, v61 offset:4256
	ds_write_b16_d16_hi v241, v61 offset:4256
	v_add_u32_e32 v58, 0xb3400, v150
	v_min_u32_e32 v58, v58, v88
	global_load_dwordx4 v[94:97], v58, s[8:9] nt
	s_waitcnt vmcnt(21)
	v_cvt_pk_f16_f32 v49, v48, v49
	v_cvt_pk_f16_f32 v48, v46, v47
	ds_write_b16 v234, v48 offset:4864
	ds_write_b16_d16_hi v235, v48 offset:4864
	ds_write_b16 v236, v49 offset:4864
	ds_write_b16_d16_hi v237, v49 offset:4864
	v_add_u32_e32 v46, 0xc9a40, v244
	v_min_u32_e32 v46, v46, v88
	global_load_dwordx4 v[98:101], v46, s[8:9] nt
	s_waitcnt vmcnt(21)
	v_cvt_pk_f16_f32 v41, v40, v41
	v_cvt_pk_f16_f32 v40, v38, v39
	ds_write_b16 v238, v40 offset:5472
	ds_write_b16_d16_hi v239, v40 offset:5472
	ds_write_b16 v240, v41 offset:5472
	ds_write_b16_d16_hi v241, v41 offset:5472
	v_add_u32_e32 v38, 0xe0080, v150
	v_min_u32_e32 v38, v38, v88
	global_load_dwordx4 v[102:105], v38, s[8:9] nt
	s_waitcnt vmcnt(21)
	v_cvt_pk_f16_f32 v37, v36, v37
	v_cvt_pk_f16_f32 v36, v34, v35
	ds_write_b16 v234, v36 offset:6080
	ds_write_b16_d16_hi v235, v36 offset:6080
	ds_write_b16 v236, v37 offset:6080
	ds_write_b16_d16_hi v237, v37 offset:6080
	v_add_u32_e32 v34, 0xf66c0, v244
	v_min_u32_e32 v34, v34, v88
	global_load_dwordx4 v[106:109], v34, s[8:9] nt
	s_waitcnt vmcnt(21)
	v_cvt_pk_f16_f32 v17, v16, v17
	v_cvt_pk_f16_f32 v16, v14, v15
	ds_write_b16 v238, v16 offset:6688
	ds_write_b16_d16_hi v239, v16 offset:6688
	ds_write_b16 v240, v17 offset:6688
	ds_write_b16_d16_hi v241, v17 offset:6688
	v_add_u32_e32 v14, 0x10cd00, v150
	v_min_u32_e32 v14, v14, v88
	v_cndmask_b32_e64 v14, 0, v14, s[0:1]
	global_load_dwordx4 v[46:49], v14, s[8:9] nt
	s_waitcnt vmcnt(21)
	v_cvt_pk_f16_f32 v13, v12, v13
	v_cvt_pk_f16_f32 v12, v10, v11
	ds_write_b16 v234, v12 offset:7296
	ds_write_b16_d16_hi v235, v12 offset:7296
	ds_write_b16 v236, v13 offset:7296
	ds_write_b16_d16_hi v237, v13 offset:7296
	s_waitcnt lgkmcnt(0)
	s_barrier
	v_sub_u32_e32 v245, v234, v243
	v_add_u32_e32 v246, 0xfffffdc0, v245
	v_min_u32_e32 v245, v245, v246
	v_add_u32_e32 v234, v242, v245
	v_sub_u32_e32 v245, v235, v243
	v_add_u32_e32 v246, 0xfffffdc0, v245
	v_min_u32_e32 v245, v245, v246
	v_add_u32_e32 v235, v242, v245
	v_sub_u32_e32 v245, v236, v243
	v_add_u32_e32 v246, 0xfffffdc0, v245
	v_min_u32_e32 v245, v245, v246
	v_add_u32_e32 v236, v242, v245
	v_sub_u32_e32 v245, v237, v243
	v_add_u32_e32 v246, 0xfffffdc0, v245
	v_min_u32_e32 v245, v245, v246
	v_add_u32_e32 v237, v242, v245
	v_sub_u32_e32 v245, v238, v243
	v_add_u32_e32 v246, 0xfffffdc0, v245
	v_min_u32_e32 v245, v245, v246
	v_add_u32_e32 v238, v242, v245
	v_sub_u32_e32 v245, v239, v243
	v_add_u32_e32 v246, 0xfffffdc0, v245
	v_min_u32_e32 v245, v245, v246
	v_add_u32_e32 v239, v242, v245
	v_sub_u32_e32 v245, v240, v243
	v_add_u32_e32 v246, 0xfffffdc0, v245
	v_min_u32_e32 v245, v245, v246
	v_add_u32_e32 v240, v242, v245
	v_sub_u32_e32 v245, v241, v243
	v_add_u32_e32 v246, 0xfffffdc0, v245
	v_min_u32_e32 v245, v245, v246
	v_add_u32_e32 v241, v242, v245
	s_mov_b32 s3, 0x10000
	v_add_co_u32_e32 v10, vcc, s3, v152
	s_mov_b32 s3, 0x14000
	s_nop 0
	v_addc_co_u32_e32 v11, vcc, 0, v153, vcc
	v_add_co_u32_e32 v58, vcc, s3, v152
	global_load_dwordx4 v[34:37], v[10:11], off sc1
	global_load_dwordx4 v[38:41], v[10:11], off offset:256 sc1
	v_addc_co_u32_e32 v59, vcc, 0, v153, vcc
	global_load_dwordx4 v[14:17], v[58:59], off sc1
	global_load_dwordx4 v[10:13], v[58:59], off offset:256 sc1
	v_lshlrev_b32_e32 v58, 4, v87
	v_add_u32_e32 v224, 0x111518dc, v154
	v_mad_u32_u24 v151, v86, s17, v58
	ds_read_b128 v[58:61], v151 offset:0
	v_add_u32_e32 v62, 0x400, v150
	s_waitcnt vmcnt(24) lgkmcnt(0)
	v_mfma_f32_16x16x32_f16 v[86:89], v[26:29], v[58:61], 0
	s_waitcnt vmcnt(23)
	v_mfma_f32_16x16x32_f16 v[122:125], v[50:53], v[58:61], 0
	v_min_u32_e32 v58, v62, v224
	global_load_dwordx4 v[58:61], v58, s[8:9] nt
	s_waitcnt vmcnt(17)
	v_cvt_pk_f16_f32 v63, v112, v113
	v_cvt_pk_f16_f32 v62, v110, v111
	v_add_u32_e32 v155, 0xea00, v1
	ds_write_b16 v234, v62 offset:0
	ds_write_b16_d16_hi v235, v62 offset:0
	ds_write_b16 v236, v63 offset:0
	ds_write_b16_d16_hi v237, v63 offset:0
	ds_read_b128 v[62:65], v151 offset:608
	ds_read_b128 v[66:69], v151 offset:1216
	s_waitcnt lgkmcnt(1)
	v_mfma_f32_16x16x32_f16 v[110:113], v[26:29], v[62:65], 0
	v_mfma_f32_16x16x32_f16 v[126:129], v[50:53], v[62:65], 0
	s_waitcnt lgkmcnt(0)
	v_mfma_f32_16x16x32_f16 v[130:133], v[26:29], v[66:69], 0
	v_mfma_f32_16x16x32_f16 v[134:137], v[50:53], v[66:69], 0
	ds_read_b128 v[62:65], v151 offset:1824
	ds_read_b128 v[66:69], v151 offset:2432
	s_waitcnt lgkmcnt(1)
	v_mfma_f32_16x16x32_f16 v[138:141], v[26:29], v[62:65], 0
	v_mfma_f32_16x16x32_f16 v[142:145], v[50:53], v[62:65], 0
	s_waitcnt lgkmcnt(0)
	v_mfma_f32_16x16x32_f16 v[146:149], v[26:29], v[66:69], 0
	v_mfma_f32_16x16x32_f16 v[156:159], v[50:53], v[66:69], 0
	v_add_u32_e32 v62, 0x16a40, v244
	v_min_u32_e32 v62, v62, v224
	global_load_dwordx4 v[62:65], v62, s[8:9] nt
	s_waitcnt vmcnt(17)
	v_cvt_pk_f16_f32 v67, v116, v117
	v_cvt_pk_f16_f32 v66, v114, v115
	ds_write_b16 v238, v66 offset:608
	ds_write_b16_d16_hi v239, v66 offset:608
	ds_write_b16 v240, v67 offset:608
	ds_write_b16_d16_hi v241, v67 offset:608
	ds_read_b128 v[66:69], v151 offset:3040
	ds_read_b128 v[70:73], v151 offset:4864
	s_waitcnt lgkmcnt(1)
	v_mfma_f32_16x16x32_f16 v[114:117], v[26:29], v[66:69], 0
	v_mfma_f32_16x16x32_f16 v[160:163], v[50:53], v[66:69], 0
	ds_read_b128 v[66:69], v151 offset:3648
	ds_read_b128 v[164:167], v151 offset:4256
	s_waitcnt lgkmcnt(1)
	v_mfma_f32_16x16x32_f16 v[168:171], v[26:29], v[66:69], 0
	v_mfma_f32_16x16x32_f16 v[172:175], v[50:53], v[66:69], 0
	s_waitcnt lgkmcnt(0)
	v_mfma_f32_16x16x32_f16 v[176:179], v[26:29], v[164:167], 0
	v_mfma_f32_16x16x32_f16 v[164:167], v[50:53], v[164:167], 0
	v_mfma_f32_16x16x32_f16 v[180:183], v[26:29], v[70:73], 0
	v_mfma_f32_16x16x32_f16 v[184:187], v[50:53], v[70:73], 0
	v_add_u32_e32 v66, 0x2d080, v150
	v_min_u32_e32 v66, v66, v224
	global_load_dwordx4 v[66:69], v66, s[8:9] nt
	s_waitcnt vmcnt(17)
	v_cvt_pk_f16_f32 v71, v120, v121
	v_cvt_pk_f16_f32 v70, v118, v119
	ds_write_b16 v234, v70 offset:1216
	ds_write_b16_d16_hi v235, v70 offset:1216
	ds_write_b16 v236, v71 offset:1216
	ds_write_b16_d16_hi v237, v71 offset:1216
	ds_read_b128 v[70:73], v151 offset:5472
	ds_read_b128 v[118:121], v151 offset:6080
	s_waitcnt lgkmcnt(1)
	v_mfma_f32_16x16x32_f16 v[188:191], v[26:29], v[70:73], 0
	v_mfma_f32_16x16x32_f16 v[192:195], v[50:53], v[70:73], 0
	ds_read_b128 v[70:73], v151 offset:6688
	ds_read_b128 v[200:203], v151 offset:7296
	s_waitcnt lgkmcnt(2)
	v_mfma_f32_16x16x32_f16 v[196:199], v[26:29], v[118:121], 0
	v_mfma_f32_16x16x32_f16 v[118:121], v[50:53], v[118:121], 0
	s_waitcnt lgkmcnt(1)
	v_mfma_f32_16x16x32_f16 v[204:207], v[26:29], v[70:73], 0
	v_mfma_f32_16x16x32_f16 v[208:211], v[50:53], v[70:73], 0
	s_waitcnt lgkmcnt(0)
	v_mfma_f32_16x16x32_f16 v[26:29], v[26:29], v[200:203], 0
	v_mfma_f32_16x16x32_f16 v[200:203], v[50:53], v[200:203], 0
	v_add_u32_e32 v50, 0x436c0, v244
	v_min_u32_e32 v50, v50, v224
	global_load_dwordx4 v[70:73], v50, s[8:9] nt
	s_waitcnt vmcnt(17)
	v_cvt_pk_f16_f32 v51, v76, v77
	v_cvt_pk_f16_f32 v50, v74, v75
	ds_write_b16 v238, v50 offset:1824
	ds_write_b16_d16_hi v239, v50 offset:1824
	ds_write_b16 v240, v51 offset:1824
	ds_write_b16_d16_hi v241, v51 offset:1824
	ds_read_b128 v[50:53], v151 offset:64
	ds_read_b128 v[74:77], v151 offset:672
	s_waitcnt lgkmcnt(1)
	v_mfma_f32_16x16x32_f16 v[86:89], v[18:21], v[50:53], v[86:89]
	v_mfma_f32_16x16x32_f16 v[122:125], v[42:45], v[50:53], v[122:125]
	s_waitcnt lgkmcnt(0)
	v_mfma_f32_16x16x32_f16 v[110:113], v[18:21], v[74:77], v[110:113]
	v_mfma_f32_16x16x32_f16 v[126:129], v[42:45], v[74:77], v[126:129]
	ds_read_b128 v[50:53], v151 offset:1280
	ds_read_b128 v[74:77], v151 offset:1888
	s_waitcnt lgkmcnt(1)
	v_mfma_f32_16x16x32_f16 v[130:133], v[18:21], v[50:53], v[130:133]
	v_mfma_f32_16x16x32_f16 v[134:137], v[42:45], v[50:53], v[134:137]
	s_waitcnt lgkmcnt(0)
	v_mfma_f32_16x16x32_f16 v[138:141], v[18:21], v[74:77], v[138:141]
	v_mfma_f32_16x16x32_f16 v[142:145], v[42:45], v[74:77], v[142:145]
	v_add_u32_e32 v50, 0x59d00, v150
	v_min_u32_e32 v50, v50, v224
	global_load_dwordx4 v[74:77], v50, s[8:9] nt
	s_waitcnt vmcnt(17)
	v_cvt_pk_f16_f32 v51, v80, v81
	v_cvt_pk_f16_f32 v50, v78, v79
	ds_write_b16 v234, v50 offset:2432
	ds_write_b16_d16_hi v235, v50 offset:2432
	ds_write_b16 v236, v51 offset:2432
	ds_write_b16_d16_hi v237, v51 offset:2432
	ds_read_b128 v[50:53], v151 offset:2496
	ds_read_b128 v[78:81], v151 offset:3104
	s_waitcnt lgkmcnt(1)
	v_mfma_f32_16x16x32_f16 v[146:149], v[18:21], v[50:53], v[146:149]
	v_mfma_f32_16x16x32_f16 v[156:159], v[42:45], v[50:53], v[156:159]
	s_waitcnt lgkmcnt(0)
	v_mfma_f32_16x16x32_f16 v[114:117], v[18:21], v[78:81], v[114:117]
	v_mfma_f32_16x16x32_f16 v[160:163], v[42:45], v[78:81], v[160:163]
	ds_read_b128 v[50:53], v151 offset:3712
	ds_read_b128 v[78:81], v151 offset:4320
	s_waitcnt lgkmcnt(1)
	v_mfma_f32_16x16x32_f16 v[168:171], v[18:21], v[50:53], v[168:171]
	v_mfma_f32_16x16x32_f16 v[172:175], v[42:45], v[50:53], v[172:175]
	s_waitcnt lgkmcnt(0)
	v_mfma_f32_16x16x32_f16 v[176:179], v[18:21], v[78:81], v[176:179]
	v_mfma_f32_16x16x32_f16 v[164:167], v[42:45], v[78:81], v[164:167]
	v_add_u32_e32 v50, 0x70340, v244
	v_min_u32_e32 v50, v50, v224
	global_load_dwordx4 v[78:81], v50, s[8:9] nt
	s_waitcnt vmcnt(17)
	v_cvt_pk_f16_f32 v51, v84, v85
	v_cvt_pk_f16_f32 v50, v82, v83
	ds_write_b16 v238, v50 offset:3040
	ds_write_b16_d16_hi v239, v50 offset:3040
	ds_write_b16 v240, v51 offset:3040
	ds_write_b16_d16_hi v241, v51 offset:3040
	ds_read_b128 v[50:53], v151 offset:4928
	ds_read_b128 v[82:85], v151 offset:5536
	s_waitcnt lgkmcnt(1)
	v_mfma_f32_16x16x32_f16 v[180:183], v[18:21], v[50:53], v[180:183]
	v_mfma_f32_16x16x32_f16 v[184:187], v[42:45], v[50:53], v[184:187]
	s_waitcnt lgkmcnt(0)
	v_mfma_f32_16x16x32_f16 v[188:191], v[18:21], v[82:85], v[188:191]
	v_mfma_f32_16x16x32_f16 v[192:195], v[42:45], v[82:85], v[192:195]
	ds_read_b128 v[50:53], v151 offset:6144
	ds_read_b128 v[82:85], v151 offset:6752
	s_waitcnt lgkmcnt(1)
	v_mfma_f32_16x16x32_f16 v[196:199], v[18:21], v[50:53], v[196:199]
	v_mfma_f32_16x16x32_f16 v[118:121], v[42:45], v[50:53], v[118:121]
	s_waitcnt lgkmcnt(0)
	v_mfma_f32_16x16x32_f16 v[204:207], v[18:21], v[82:85], v[204:207]
	v_mfma_f32_16x16x32_f16 v[208:211], v[42:45], v[82:85], v[208:211]
	v_add_u32_e32 v50, 0x86980, v150
	v_min_u32_e32 v50, v50, v224
	global_load_dwordx4 v[82:85], v50, s[8:9] nt
	s_waitcnt vmcnt(17)
	v_cvt_pk_f16_f32 v51, v56, v57
	v_cvt_pk_f16_f32 v50, v54, v55
	ds_write_b16 v234, v50 offset:3648
	ds_write_b16_d16_hi v235, v50 offset:3648
	ds_write_b16 v236, v51 offset:3648
	ds_write_b16_d16_hi v237, v51 offset:3648
	ds_read_b128 v[212:215], v151 offset:7360
	s_mov_b32 s2, 0x18000
	s_waitcnt lgkmcnt(0)
	v_mfma_f32_16x16x32_f16 v[216:219], v[18:21], v[212:215], v[26:29]
	v_add_co_u32_e32 v18, vcc, s2, v152
	s_mov_b32 s2, 0x1c000
	s_nop 0
	v_addc_co_u32_e32 v19, vcc, 0, v153, vcc
	global_load_dwordx4 v[50:53], v[18:19], off sc1
	global_load_dwordx4 v[54:57], v[18:19], off offset:256 sc1
	v_add_co_u32_e32 v18, vcc, s2, v152
	v_mfma_f32_16x16x32_f16 v[42:45], v[42:45], v[212:215], v[200:203]
	s_nop 0
	v_addc_co_u32_e32 v19, vcc, 0, v153, vcc
	global_load_dwordx4 v[26:29], v[18:19], off sc1
	s_nop 0
	global_load_dwordx4 v[18:21], v[18:19], off offset:256 sc1
	ds_read_b128 v[200:203], v151 offset:128
	ds_read_b128 v[212:215], v151 offset:736
	s_waitcnt lgkmcnt(1)
	v_mfma_f32_16x16x32_f16 v[220:223], v[22:25], v[200:203], v[86:89]
	s_nop 2
	ds_read_b128 v[86:89], v151 offset:1344
	v_mfma_f32_16x16x32_f16 v[122:125], v[30:33], v[200:203], v[122:125]
	s_waitcnt lgkmcnt(1)
	v_mfma_f32_16x16x32_f16 v[110:113], v[22:25], v[212:215], v[110:113]
	v_mfma_f32_16x16x32_f16 v[126:129], v[30:33], v[212:215], v[126:129]
	s_waitcnt lgkmcnt(0)
	v_mfma_f32_16x16x32_f16 v[130:133], v[22:25], v[86:89], v[130:133]
	v_mfma_f32_16x16x32_f16 v[134:137], v[30:33], v[86:89], v[134:137]
	v_add_u32_e32 v86, 0x9cfc0, v244
	v_min_u32_e32 v86, v86, v224
	global_load_dwordx4 v[86:89], v86, s[8:9] nt
	s_waitcnt vmcnt(21)
	v_cvt_pk_f16_f32 v93, v92, v93
	v_cvt_pk_f16_f32 v92, v90, v91
	ds_write_b16 v238, v92 offset:4256
	ds_write_b16_d16_hi v239, v92 offset:4256
	ds_write_b16 v240, v93 offset:4256
	ds_write_b16_d16_hi v241, v93 offset:4256
	ds_read_b128 v[90:93], v151 offset:1952
	ds_read_b128 v[200:203], v151 offset:2560
	s_waitcnt lgkmcnt(1)
	v_mfma_f32_16x16x32_f16 v[138:141], v[22:25], v[90:93], v[138:141]
	v_mfma_f32_16x16x32_f16 v[142:145], v[30:33], v[90:93], v[142:145]
	s_waitcnt lgkmcnt(0)
	v_mfma_f32_16x16x32_f16 v[146:149], v[22:25], v[200:203], v[146:149]
	v_mfma_f32_16x16x32_f16 v[156:159], v[30:33], v[200:203], v[156:159]
	ds_read_b128 v[90:93], v151 offset:3168
	ds_read_b128 v[200:203], v151 offset:3776
	s_waitcnt lgkmcnt(1)
	v_mfma_f32_16x16x32_f16 v[114:117], v[22:25], v[90:93], v[114:117]
	v_mfma_f32_16x16x32_f16 v[160:163], v[30:33], v[90:93], v[160:163]
	s_waitcnt lgkmcnt(0)
	v_mfma_f32_16x16x32_f16 v[168:171], v[22:25], v[200:203], v[168:171]
	v_mfma_f32_16x16x32_f16 v[172:175], v[30:33], v[200:203], v[172:175]
	v_add_u32_e32 v90, 0xb3600, v150
	v_min_u32_e32 v90, v90, v224
	global_load_dwordx4 v[90:93], v90, s[8:9] nt
	s_waitcnt vmcnt(21)
	v_cvt_pk_f16_f32 v97, v96, v97
	v_cvt_pk_f16_f32 v96, v94, v95
	ds_write_b16 v234, v96 offset:4864
	ds_write_b16_d16_hi v235, v96 offset:4864
	ds_write_b16 v236, v97 offset:4864
	ds_write_b16_d16_hi v237, v97 offset:4864
	ds_read_b128 v[94:97], v151 offset:4384
	ds_read_b128 v[200:203], v151 offset:6208
	s_waitcnt lgkmcnt(1)
	v_mfma_f32_16x16x32_f16 v[176:179], v[22:25], v[94:97], v[176:179]
	v_mfma_f32_16x16x32_f16 v[164:167], v[30:33], v[94:97], v[164:167]
	ds_read_b128 v[94:97], v151 offset:4992
	ds_read_b128 v[212:215], v151 offset:5600
	s_waitcnt lgkmcnt(1)
	v_mfma_f32_16x16x32_f16 v[180:183], v[22:25], v[94:97], v[180:183]
	v_mfma_f32_16x16x32_f16 v[184:187], v[30:33], v[94:97], v[184:187]
	s_waitcnt lgkmcnt(0)
	v_mfma_f32_16x16x32_f16 v[188:191], v[22:25], v[212:215], v[188:191]
	v_mfma_f32_16x16x32_f16 v[192:195], v[30:33], v[212:215], v[192:195]
	v_mfma_f32_16x16x32_f16 v[196:199], v[22:25], v[200:203], v[196:199]
	v_mfma_f32_16x16x32_f16 v[118:121], v[30:33], v[200:203], v[118:121]
	v_add_u32_e32 v94, 0xc9c40, v244
	v_min_u32_e32 v94, v94, v224
	global_load_dwordx4 v[94:97], v94, s[8:9] nt
	s_waitcnt vmcnt(21)
	v_cvt_pk_f16_f32 v101, v100, v101
	v_cvt_pk_f16_f32 v100, v98, v99
	ds_write_b16 v238, v100 offset:5472
	ds_write_b16_d16_hi v239, v100 offset:5472
	ds_write_b16 v240, v101 offset:5472
	ds_write_b16_d16_hi v241, v101 offset:5472
	ds_read_b128 v[98:101], v151 offset:6816
	ds_read_b128 v[200:203], v151 offset:7424
	s_waitcnt lgkmcnt(1)
	v_mfma_f32_16x16x32_f16 v[204:207], v[22:25], v[98:101], v[204:207]
	v_mfma_f32_16x16x32_f16 v[208:211], v[30:33], v[98:101], v[208:211]
	s_waitcnt lgkmcnt(0)
	v_mfma_f32_16x16x32_f16 v[30:33], v[30:33], v[200:203], v[42:45]
	s_nop 2
	ds_read_b128 v[42:45], v151 offset:192
	ds_read_b128 v[98:101], v151 offset:800
	v_mfma_f32_16x16x32_f16 v[22:25], v[22:25], v[200:203], v[216:219]
	s_waitcnt lgkmcnt(1)
	v_mfma_f32_16x16x32_f16 v[200:203], v[6:9], v[42:45], v[220:223]
	v_mfma_f32_16x16x32_f16 v[122:125], v[2:5], v[42:45], v[122:125]
	s_waitcnt lgkmcnt(0)
	v_mfma_f32_16x16x32_f16 v[212:215], v[6:9], v[98:101], v[110:113]
	v_mfma_f32_16x16x32_f16 v[126:129], v[2:5], v[98:101], v[126:129]
	v_add_u32_e32 v42, 0xe0280, v150
	v_min_u32_e32 v42, v42, v224
	global_load_dwordx4 v[98:101], v42, s[8:9] nt
	s_waitcnt vmcnt(21)
	v_cvt_pk_f16_f32 v43, v104, v105
	v_cvt_pk_f16_f32 v42, v102, v103
	ds_write_b16 v234, v42 offset:6080
	ds_write_b16_d16_hi v235, v42 offset:6080
	ds_write_b16 v236, v43 offset:6080
	ds_write_b16_d16_hi v237, v43 offset:6080
	ds_read_b128 v[42:45], v151 offset:1408
	ds_read_b128 v[102:105], v151 offset:2016
	s_waitcnt lgkmcnt(1)
	v_mfma_f32_16x16x32_f16 v[130:133], v[6:9], v[42:45], v[130:133]
	v_mfma_f32_16x16x32_f16 v[134:137], v[2:5], v[42:45], v[134:137]
	s_waitcnt lgkmcnt(0)
	v_mfma_f32_16x16x32_f16 v[138:141], v[6:9], v[102:105], v[138:141]
	v_mfma_f32_16x16x32_f16 v[142:145], v[2:5], v[102:105], v[142:145]
	ds_read_b128 v[42:45], v151 offset:2624
	ds_read_b128 v[102:105], v151 offset:3232
	s_waitcnt lgkmcnt(1)
	v_mfma_f32_16x16x32_f16 v[146:149], v[6:9], v[42:45], v[146:149]
	v_mfma_f32_16x16x32_f16 v[216:219], v[2:5], v[42:45], v[156:159]
	s_waitcnt lgkmcnt(0)
	v_mfma_f32_16x16x32_f16 v[220:223], v[6:9], v[102:105], v[114:117]
	v_mfma_f32_16x16x32_f16 v[158:161], v[2:5], v[102:105], v[160:163]
	v_add_u32_e32 v42, 0xf68c0, v244
	v_min_u32_e32 v42, v42, v224
	global_load_dwordx4 v[102:105], v42, s[8:9] nt
	s_waitcnt vmcnt(21)
	v_cvt_pk_f16_f32 v43, v108, v109
	v_cvt_pk_f16_f32 v42, v106, v107
	ds_write_b16 v238, v42 offset:6688
	ds_write_b16_d16_hi v239, v42 offset:6688
	ds_write_b16 v240, v43 offset:6688
	ds_write_b16_d16_hi v241, v43 offset:6688
	ds_read_b128 v[42:45], v151 offset:3840
	ds_read_b128 v[106:109], v151 offset:4448
	s_waitcnt lgkmcnt(1)
	v_mfma_f32_16x16x32_f16 v[168:171], v[6:9], v[42:45], v[168:171]
	v_mfma_f32_16x16x32_f16 v[172:175], v[2:5], v[42:45], v[172:175]
	s_waitcnt lgkmcnt(0)
	v_mfma_f32_16x16x32_f16 v[176:179], v[6:9], v[106:109], v[176:179]
	v_mfma_f32_16x16x32_f16 v[162:165], v[2:5], v[106:109], v[164:167]
	ds_read_b128 v[42:45], v151 offset:5056
	ds_read_b128 v[106:109], v151 offset:5664
	s_waitcnt lgkmcnt(1)
	v_mfma_f32_16x16x32_f16 v[180:183], v[6:9], v[42:45], v[180:183]
	v_mfma_f32_16x16x32_f16 v[184:187], v[2:5], v[42:45], v[184:187]
	s_waitcnt lgkmcnt(0)
	v_mfma_f32_16x16x32_f16 v[188:191], v[6:9], v[106:109], v[188:191]
	v_mfma_f32_16x16x32_f16 v[192:195], v[2:5], v[106:109], v[192:195]
	v_add_u32_e32 v42, 0x10cf00, v150
	v_min_u32_e32 v42, v42, v224
	v_cndmask_b32_e64 v42, 0, v42, s[0:1]
	global_load_dwordx4 v[106:109], v42, s[8:9] nt
	s_waitcnt vmcnt(21)
	v_cvt_pk_f16_f32 v43, v48, v49
	v_cvt_pk_f16_f32 v42, v46, v47
	ds_write_b16 v234, v42 offset:7296
	ds_write_b16_d16_hi v235, v42 offset:7296
	ds_write_b16 v236, v43 offset:7296
	ds_write_b16_d16_hi v237, v43 offset:7296
	ds_read_b128 v[42:45], v151 offset:6272
	ds_read_b128 v[46:49], v151 offset:6880
	ds_read_b128 v[110:113], v151 offset:7488
	s_mov_b32 s2, 0x20000
	v_add_co_u32_e32 v114, vcc, s2, v152
	s_mov_b32 s2, 0x24000
	s_nop 0
	v_addc_co_u32_e32 v115, vcc, 0, v153, vcc
	s_waitcnt lgkmcnt(2)
	v_mfma_f32_16x16x32_f16 v[196:199], v[6:9], v[42:45], v[196:199]
	s_waitcnt lgkmcnt(0)
	s_barrier
	v_sub_u32_e32 v245, v234, v243
	v_add_u32_e32 v246, 0xfffffdc0, v245
	v_min_u32_e32 v245, v245, v246
	v_add_u32_e32 v234, v242, v245
	v_sub_u32_e32 v245, v235, v243
	v_add_u32_e32 v246, 0xfffffdc0, v245
	v_min_u32_e32 v245, v245, v246
	v_add_u32_e32 v235, v242, v245
	v_sub_u32_e32 v245, v236, v243
	v_add_u32_e32 v246, 0xfffffdc0, v245
	v_min_u32_e32 v245, v245, v246
	v_add_u32_e32 v236, v242, v245
	v_sub_u32_e32 v245, v237, v243
	v_add_u32_e32 v246, 0xfffffdc0, v245
	v_min_u32_e32 v245, v245, v246
	v_add_u32_e32 v237, v242, v245
	v_sub_u32_e32 v245, v238, v243
	v_add_u32_e32 v246, 0xfffffdc0, v245
	v_min_u32_e32 v245, v245, v246
	v_add_u32_e32 v238, v242, v245
	v_sub_u32_e32 v245, v239, v243
	v_add_u32_e32 v246, 0xfffffdc0, v245
	v_min_u32_e32 v245, v245, v246
	v_add_u32_e32 v239, v242, v245
	v_sub_u32_e32 v245, v240, v243
	v_add_u32_e32 v246, 0xfffffdc0, v245
	v_min_u32_e32 v245, v245, v246
	v_add_u32_e32 v240, v242, v245
	v_sub_u32_e32 v245, v241, v243
	v_add_u32_e32 v246, 0xfffffdc0, v245
	v_min_u32_e32 v245, v245, v246
	v_add_u32_e32 v241, v242, v245
	v_mfma_f32_16x16x32_f16 v[204:207], v[6:9], v[46:49], v[204:207]
	v_mfma_f32_16x16x32_f16 v[228:231], v[6:9], v[110:113], v[22:25]
	v_add_co_u32_e32 v6, vcc, s2, v152
	s_nop 1
	v_addc_co_u32_e32 v7, vcc, 0, v153, vcc
	v_mfma_f32_16x16x32_f16 v[224:227], v[2:5], v[42:45], v[118:121]
	v_mfma_f32_16x16x32_f16 v[208:211], v[2:5], v[46:49], v[208:211]
	global_load_dwordx4 v[42:45], v[114:115], off sc1
	global_load_dwordx4 v[46:49], v[114:115], off offset:256 sc1
	global_load_dwordx4 v[22:25], v[6:7], off sc1
	s_nop 0
	global_load_dwordx4 v[6:9], v[6:7], off offset:256 sc1
	v_mfma_f32_16x16x32_f16 v[2:5], v[2:5], v[110:113], v[30:33]
	v_add_u32_e32 v157, 0x11151adc, v154
	s_nop 1
	ds_read_b128 v[30:33], v151 offset:256
	v_add_u32_e32 v156, 0xea00, v151
	v_add_u32_e32 v110, 0x600, v150
	s_waitcnt vmcnt(24) lgkmcnt(0)
	v_mfma_f32_16x16x32_f16 v[200:203], v[34:37], v[30:33], v[200:203]
	s_waitcnt vmcnt(23)
	v_mfma_f32_16x16x32_f16 v[30:33], v[38:41], v[30:33], v[122:125]
	v_min_u32_e32 v110, v110, v157
	global_load_dwordx4 v[110:113], v110, s[8:9] nt
	s_waitcnt vmcnt(21)
	v_cvt_pk_f16_f32 v61, v60, v61
	v_cvt_pk_f16_f32 v60, v58, v59
	ds_write_b16 v234, v60 offset:0
	ds_write_b16_d16_hi v235, v60 offset:0
	ds_write_b16 v236, v61 offset:0
	ds_write_b16_d16_hi v237, v61 offset:0
	ds_read_b128 v[58:61], v151 offset:864
	ds_read_b128 v[114:117], v151 offset:1472
	s_waitcnt lgkmcnt(1)
	v_mfma_f32_16x16x32_f16 v[122:125], v[34:37], v[58:61], v[212:215]
	v_mfma_f32_16x16x32_f16 v[58:61], v[38:41], v[58:61], v[126:129]
	s_waitcnt lgkmcnt(0)
	v_mfma_f32_16x16x32_f16 v[126:129], v[34:37], v[114:117], v[130:133]
	v_mfma_f32_16x16x32_f16 v[130:133], v[38:41], v[114:117], v[134:137]
	ds_read_b128 v[114:117], v151 offset:2080
	ds_read_b128 v[118:121], v151 offset:2688
	s_waitcnt lgkmcnt(1)
	v_mfma_f32_16x16x32_f16 v[134:137], v[34:37], v[114:117], v[138:141]
	v_mfma_f32_16x16x32_f16 v[138:141], v[38:41], v[114:117], v[142:145]
	s_waitcnt lgkmcnt(0)
	v_mfma_f32_16x16x32_f16 v[142:145], v[34:37], v[118:121], v[146:149]
	v_mfma_f32_16x16x32_f16 v[146:149], v[38:41], v[118:121], v[216:219]
	v_add_u32_e32 v114, 0x16c40, v244
	v_min_u32_e32 v114, v114, v157
	global_load_dwordx4 v[114:117], v114, s[8:9] nt
	s_waitcnt vmcnt(21)
	v_cvt_pk_f16_f32 v65, v64, v65
	v_cvt_pk_f16_f32 v64, v62, v63
	ds_write_b16 v238, v64 offset:608
	ds_write_b16_d16_hi v239, v64 offset:608
	ds_write_b16 v240, v65 offset:608
	ds_write_b16_d16_hi v241, v65 offset:608
	ds_read_b128 v[62:65], v151 offset:3296
	ds_read_b128 v[118:121], v151 offset:5120
	s_waitcnt lgkmcnt(1)
	v_mfma_f32_16x16x32_f16 v[212:215], v[34:37], v[62:65], v[220:223]
	v_mfma_f32_16x16x32_f16 v[62:65], v[38:41], v[62:65], v[158:161]
	s_nop 2
	ds_read_b128 v[158:161], v151 offset:3904
	ds_read_b128 v[216:219], v151 offset:4512
	s_waitcnt lgkmcnt(1)
	v_mfma_f32_16x16x32_f16 v[166:169], v[34:37], v[158:161], v[168:171]
	v_mfma_f32_16x16x32_f16 v[158:161], v[38:41], v[158:161], v[172:175]
	s_waitcnt lgkmcnt(0)
	v_mfma_f32_16x16x32_f16 v[170:173], v[34:37], v[216:219], v[176:179]
	v_mfma_f32_16x16x32_f16 v[162:165], v[38:41], v[216:219], v[162:165]
	v_mfma_f32_16x16x32_f16 v[174:177], v[34:37], v[118:121], v[180:183]
	v_mfma_f32_16x16x32_f16 v[178:181], v[38:41], v[118:121], v[184:187]
	v_add_u32_e32 v118, 0x2d280, v150
	v_min_u32_e32 v118, v118, v157
	global_load_dwordx4 v[118:121], v118, s[8:9] nt
	s_waitcnt vmcnt(21)
	v_cvt_pk_f16_f32 v69, v68, v69
	v_cvt_pk_f16_f32 v68, v66, v67
	ds_write_b16 v234, v68 offset:1216
	ds_write_b16_d16_hi v235, v68 offset:1216
	ds_write_b16 v236, v69 offset:1216
	ds_write_b16_d16_hi v237, v69 offset:1216
	ds_read_b128 v[66:69], v151 offset:5728
	ds_read_b128 v[182:185], v151 offset:6336
	s_waitcnt lgkmcnt(1)
	v_mfma_f32_16x16x32_f16 v[186:189], v[34:37], v[66:69], v[188:191]
	v_mfma_f32_16x16x32_f16 v[190:193], v[38:41], v[66:69], v[192:195]
	ds_read_b128 v[66:69], v151 offset:6944
	ds_read_b128 v[216:219], v151 offset:7552
	s_waitcnt lgkmcnt(2)
	v_mfma_f32_16x16x32_f16 v[194:197], v[34:37], v[182:185], v[196:199]
	v_mfma_f32_16x16x32_f16 v[182:185], v[38:41], v[182:185], v[224:227]
	s_waitcnt lgkmcnt(1)
	v_mfma_f32_16x16x32_f16 v[204:207], v[34:37], v[66:69], v[204:207]
	v_mfma_f32_16x16x32_f16 v[208:211], v[38:41], v[66:69], v[208:211]
	s_waitcnt lgkmcnt(0)
	v_mfma_f32_16x16x32_f16 v[220:223], v[34:37], v[216:219], v[228:231]
	v_mfma_f32_16x16x32_f16 v[2:5], v[38:41], v[216:219], v[2:5]
	v_add_u32_e32 v34, 0x438c0, v244
	v_min_u32_e32 v34, v34, v157
	global_load_dwordx4 v[34:37], v34, s[8:9] nt
	s_waitcnt vmcnt(21)
	v_cvt_pk_f16_f32 v39, v72, v73
	v_cvt_pk_f16_f32 v38, v70, v71
	ds_write_b16 v238, v38 offset:1824
	ds_write_b16_d16_hi v239, v38 offset:1824
	ds_write_b16 v240, v39 offset:1824
	ds_write_b16_d16_hi v241, v39 offset:1824
	ds_read_b128 v[38:41], v151 offset:320
	ds_read_b128 v[66:69], v151 offset:928
	s_waitcnt lgkmcnt(1)
	v_mfma_f32_16x16x32_f16 v[198:201], v[14:17], v[38:41], v[200:203]
	v_mfma_f32_16x16x32_f16 v[38:41], v[10:13], v[38:41], v[30:33]
	s_waitcnt lgkmcnt(0)
	v_mfma_f32_16x16x32_f16 v[216:219], v[10:13], v[66:69], v[58:61]
	s_nop 0
	ds_read_b128 v[30:33], v151 offset:1536
	s_nop 0
	ds_read_b128 v[58:61], v151 offset:2144
	v_mfma_f32_16x16x32_f16 v[122:125], v[14:17], v[66:69], v[122:125]
	s_waitcnt lgkmcnt(1)
	v_mfma_f32_16x16x32_f16 v[126:129], v[14:17], v[30:33], v[126:129]
	v_mfma_f32_16x16x32_f16 v[130:133], v[10:13], v[30:33], v[130:133]
	s_waitcnt lgkmcnt(0)
	v_mfma_f32_16x16x32_f16 v[134:137], v[14:17], v[58:61], v[134:137]
	v_mfma_f32_16x16x32_f16 v[138:141], v[10:13], v[58:61], v[138:141]
	v_add_u32_e32 v30, 0x59f00, v150
	v_min_u32_e32 v30, v30, v157
	global_load_dwordx4 v[66:69], v30, s[8:9] nt
	s_waitcnt vmcnt(21)
	v_cvt_pk_f16_f32 v31, v76, v77
	v_cvt_pk_f16_f32 v30, v74, v75
	ds_write_b16 v234, v30 offset:2432
	ds_write_b16_d16_hi v235, v30 offset:2432
	ds_write_b16 v236, v31 offset:2432
	ds_write_b16_d16_hi v237, v31 offset:2432
	ds_read_b128 v[30:33], v151 offset:2752
	ds_read_b128 v[58:61], v151 offset:3360
	s_waitcnt lgkmcnt(1)
	v_mfma_f32_16x16x32_f16 v[142:145], v[14:17], v[30:33], v[142:145]
	v_mfma_f32_16x16x32_f16 v[146:149], v[10:13], v[30:33], v[146:149]
	s_waitcnt lgkmcnt(0)
	v_mfma_f32_16x16x32_f16 v[212:215], v[14:17], v[58:61], v[212:215]
	v_mfma_f32_16x16x32_f16 v[224:227], v[10:13], v[58:61], v[62:65]
	ds_read_b128 v[30:33], v151 offset:3968
	ds_read_b128 v[58:61], v151 offset:4576
	s_waitcnt lgkmcnt(1)
	v_mfma_f32_16x16x32_f16 v[166:169], v[14:17], v[30:33], v[166:169]
	v_mfma_f32_16x16x32_f16 v[158:161], v[10:13], v[30:33], v[158:161]
	s_waitcnt lgkmcnt(0)
	v_mfma_f32_16x16x32_f16 v[170:173], v[14:17], v[58:61], v[170:173]
	v_mfma_f32_16x16x32_f16 v[162:165], v[10:13], v[58:61], v[162:165]
	v_add_u32_e32 v30, 0x70540, v244
	v_min_u32_e32 v30, v30, v157
	global_load_dwordx4 v[70:73], v30, s[8:9] nt
	s_waitcnt vmcnt(21)
	v_cvt_pk_f16_f32 v31, v80, v81
	v_cvt_pk_f16_f32 v30, v78, v79
	ds_write_b16 v238, v30 offset:3040
	ds_write_b16_d16_hi v239, v30 offset:3040
	ds_write_b16 v240, v31 offset:3040
	ds_write_b16_d16_hi v241, v31 offset:3040
	ds_read_b128 v[30:33], v151 offset:5184
	ds_read_b128 v[58:61], v151 offset:5792
	s_waitcnt lgkmcnt(1)
	v_mfma_f32_16x16x32_f16 v[174:177], v[14:17], v[30:33], v[174:177]
	v_mfma_f32_16x16x32_f16 v[178:181], v[10:13], v[30:33], v[178:181]
	s_waitcnt lgkmcnt(0)
	v_mfma_f32_16x16x32_f16 v[186:189], v[14:17], v[58:61], v[186:189]
	v_mfma_f32_16x16x32_f16 v[190:193], v[10:13], v[58:61], v[190:193]
	ds_read_b128 v[30:33], v151 offset:6400
	ds_read_b128 v[58:61], v151 offset:7008
	s_waitcnt lgkmcnt(1)
	v_mfma_f32_16x16x32_f16 v[194:197], v[14:17], v[30:33], v[194:197]
	v_mfma_f32_16x16x32_f16 v[182:185], v[10:13], v[30:33], v[182:185]
	s_waitcnt lgkmcnt(0)
	v_mfma_f32_16x16x32_f16 v[202:205], v[14:17], v[58:61], v[204:207]
	v_mfma_f32_16x16x32_f16 v[206:209], v[10:13], v[58:61], v[208:211]
	v_add_u32_e32 v30, 0x86b80, v150
	v_min_u32_e32 v30, v30, v157
	global_load_dwordx4 v[74:77], v30, s[8:9] nt
	s_waitcnt vmcnt(21)
	v_cvt_pk_f16_f32 v31, v84, v85
	v_cvt_pk_f16_f32 v30, v82, v83
	ds_write_b16 v234, v30 offset:3648
	ds_write_b16_d16_hi v235, v30 offset:3648
	ds_write_b16 v236, v31 offset:3648
	ds_write_b16_d16_hi v237, v31 offset:3648
	ds_read_b128 v[78:81], v151 offset:7616
	s_mov_b32 s2, 0x28000
	s_waitcnt lgkmcnt(0)
	v_mfma_f32_16x16x32_f16 v[220:223], v[14:17], v[78:81], v[220:223]
	v_add_co_u32_e32 v14, vcc, s2, v152
	s_mov_b32 s2, 0x2c000
	s_nop 0
	v_addc_co_u32_e32 v15, vcc, 0, v153, vcc
	global_load_dwordx4 v[58:61], v[14:15], off sc1
	global_load_dwordx4 v[62:65], v[14:15], off offset:256 sc1
	v_add_co_u32_e32 v14, vcc, s2, v152
	v_mfma_f32_16x16x32_f16 v[2:5], v[10:13], v[78:81], v[2:5]
	s_nop 0
	v_addc_co_u32_e32 v15, vcc, 0, v153, vcc
	global_load_dwordx4 v[30:33], v[14:15], off sc1
	s_nop 0
	global_load_dwordx4 v[14:17], v[14:15], off offset:256 sc1
	ds_read_b128 v[10:13], v151 offset:384
	ds_read_b128 v[78:81], v151 offset:992
	s_waitcnt vmcnt(24) lgkmcnt(1)
	v_mfma_f32_16x16x32_f16 v[198:201], v[50:53], v[10:13], v[198:201]
	s_waitcnt vmcnt(23)
	v_mfma_f32_16x16x32_f16 v[10:13], v[54:57], v[10:13], v[38:41]
	s_waitcnt lgkmcnt(0)
	v_mfma_f32_16x16x32_f16 v[38:41], v[50:53], v[78:81], v[122:125]
	v_mfma_f32_16x16x32_f16 v[122:125], v[54:57], v[78:81], v[216:219]
	ds_read_b128 v[78:81], v151 offset:1600
	s_waitcnt lgkmcnt(0)
	v_mfma_f32_16x16x32_f16 v[126:129], v[50:53], v[78:81], v[126:129]
	v_mfma_f32_16x16x32_f16 v[130:133], v[54:57], v[78:81], v[130:133]
	v_add_u32_e32 v78, 0x9d1c0, v244
	v_min_u32_e32 v78, v78, v157
	global_load_dwordx4 v[78:81], v78, s[8:9] nt
	s_waitcnt vmcnt(21)
	v_cvt_pk_f16_f32 v83, v88, v89
	v_cvt_pk_f16_f32 v82, v86, v87
	ds_write_b16 v238, v82 offset:4256
	ds_write_b16_d16_hi v239, v82 offset:4256
	ds_write_b16 v240, v83 offset:4256
	ds_write_b16_d16_hi v241, v83 offset:4256
	ds_read_b128 v[82:85], v151 offset:2208
	ds_read_b128 v[86:89], v151 offset:2816
	s_waitcnt lgkmcnt(1)
	v_mfma_f32_16x16x32_f16 v[134:137], v[50:53], v[82:85], v[134:137]
	v_mfma_f32_16x16x32_f16 v[138:141], v[54:57], v[82:85], v[138:141]
	s_waitcnt lgkmcnt(0)
	v_mfma_f32_16x16x32_f16 v[142:145], v[50:53], v[86:89], v[142:145]
	v_mfma_f32_16x16x32_f16 v[146:149], v[54:57], v[86:89], v[146:149]
	ds_read_b128 v[82:85], v151 offset:3424
	ds_read_b128 v[86:89], v151 offset:4032
	s_waitcnt lgkmcnt(1)
	v_mfma_f32_16x16x32_f16 v[210:213], v[50:53], v[82:85], v[212:215]
	v_mfma_f32_16x16x32_f16 v[214:217], v[54:57], v[82:85], v[224:227]
	s_waitcnt lgkmcnt(0)
	v_mfma_f32_16x16x32_f16 v[166:169], v[50:53], v[86:89], v[166:169]
	v_mfma_f32_16x16x32_f16 v[158:161], v[54:57], v[86:89], v[158:161]
	v_add_u32_e32 v82, 0xb3800, v150
	v_min_u32_e32 v82, v82, v157
	global_load_dwordx4 v[82:85], v82, s[8:9] nt
	s_waitcnt vmcnt(21)
	v_cvt_pk_f16_f32 v87, v92, v93
	v_cvt_pk_f16_f32 v86, v90, v91
	ds_write_b16 v234, v86 offset:4864
	ds_write_b16_d16_hi v235, v86 offset:4864
	ds_write_b16 v236, v87 offset:4864
	ds_write_b16_d16_hi v237, v87 offset:4864
	ds_read_b128 v[86:89], v151 offset:4640
	ds_read_b128 v[90:93], v151 offset:6464
	s_waitcnt lgkmcnt(1)
	v_mfma_f32_16x16x32_f16 v[170:173], v[50:53], v[86:89], v[170:173]
	v_mfma_f32_16x16x32_f16 v[162:165], v[54:57], v[86:89], v[162:165]
	ds_read_b128 v[86:89], v151 offset:5248
	ds_read_b128 v[224:227], v151 offset:5856
	s_waitcnt lgkmcnt(1)
	v_mfma_f32_16x16x32_f16 v[174:177], v[50:53], v[86:89], v[174:177]
	v_mfma_f32_16x16x32_f16 v[178:181], v[54:57], v[86:89], v[178:181]
	s_waitcnt lgkmcnt(0)
	v_mfma_f32_16x16x32_f16 v[186:189], v[50:53], v[224:227], v[186:189]
	v_mfma_f32_16x16x32_f16 v[190:193], v[54:57], v[224:227], v[190:193]
	v_mfma_f32_16x16x32_f16 v[194:197], v[50:53], v[90:93], v[194:197]
	v_mfma_f32_16x16x32_f16 v[182:185], v[54:57], v[90:93], v[182:185]
	v_add_u32_e32 v86, 0xc9e40, v244
	v_min_u32_e32 v86, v86, v157
	global_load_dwordx4 v[86:89], v86, s[8:9] nt
	s_waitcnt vmcnt(21)
	v_cvt_pk_f16_f32 v91, v96, v97
	v_cvt_pk_f16_f32 v90, v94, v95
	ds_write_b16 v238, v90 offset:5472
	ds_write_b16_d16_hi v239, v90 offset:5472
	ds_write_b16 v240, v91 offset:5472
	ds_write_b16_d16_hi v241, v91 offset:5472
	ds_read_b128 v[90:93], v151 offset:7072
	ds_read_b128 v[94:97], v151 offset:7680
	s_waitcnt lgkmcnt(1)
	v_mfma_f32_16x16x32_f16 v[202:205], v[50:53], v[90:93], v[202:205]
	v_mfma_f32_16x16x32_f16 v[206:209], v[54:57], v[90:93], v[206:209]
	s_waitcnt lgkmcnt(0)
	v_mfma_f32_16x16x32_f16 v[218:221], v[50:53], v[94:97], v[220:223]
	v_mfma_f32_16x16x32_f16 v[54:57], v[54:57], v[94:97], v[2:5]
	s_nop 2
	ds_read_b128 v[2:5], v151 offset:448
	ds_read_b128 v[50:53], v151 offset:1056
	s_waitcnt lgkmcnt(1)
	v_mfma_f32_16x16x32_f16 v[198:201], v[26:29], v[2:5], v[198:201]
	v_mfma_f32_16x16x32_f16 v[222:225], v[18:21], v[2:5], v[10:13]
	s_waitcnt lgkmcnt(0)
	v_mfma_f32_16x16x32_f16 v[226:229], v[26:29], v[50:53], v[38:41]
	v_mfma_f32_16x16x32_f16 v[122:125], v[18:21], v[50:53], v[122:125]
	v_add_u32_e32 v2, 0xe0480, v150
	v_min_u32_e32 v2, v2, v157
	global_load_dwordx4 v[90:93], v2, s[8:9] nt
	s_waitcnt vmcnt(21)
	v_cvt_pk_f16_f32 v3, v100, v101
	v_cvt_pk_f16_f32 v2, v98, v99
	ds_write_b16 v234, v2 offset:6080
	ds_write_b16_d16_hi v235, v2 offset:6080
	ds_write_b16 v236, v3 offset:6080
	ds_write_b16_d16_hi v237, v3 offset:6080
	ds_read_b128 v[2:5], v151 offset:1664
	ds_read_b128 v[10:13], v151 offset:2272
	s_waitcnt lgkmcnt(1)
	v_mfma_f32_16x16x32_f16 v[126:129], v[26:29], v[2:5], v[126:129]
	v_mfma_f32_16x16x32_f16 v[130:133], v[18:21], v[2:5], v[130:133]
	s_waitcnt lgkmcnt(0)
	v_mfma_f32_16x16x32_f16 v[134:137], v[26:29], v[10:13], v[134:137]
	v_mfma_f32_16x16x32_f16 v[138:141], v[18:21], v[10:13], v[138:141]
	ds_read_b128 v[2:5], v151 offset:2880
	ds_read_b128 v[10:13], v151 offset:3488
	s_waitcnt lgkmcnt(1)
	v_mfma_f32_16x16x32_f16 v[142:145], v[26:29], v[2:5], v[142:145]
	v_mfma_f32_16x16x32_f16 v[146:149], v[18:21], v[2:5], v[146:149]
	s_waitcnt lgkmcnt(0)
	v_mfma_f32_16x16x32_f16 v[210:213], v[26:29], v[10:13], v[210:213]
	v_mfma_f32_16x16x32_f16 v[214:217], v[18:21], v[10:13], v[214:217]
	v_add_u32_e32 v2, 0xf6ac0, v244
	v_min_u32_e32 v2, v2, v157
	global_load_dwordx4 v[94:97], v2, s[8:9] nt
	s_waitcnt vmcnt(21)
	v_cvt_pk_f16_f32 v3, v104, v105
	v_cvt_pk_f16_f32 v2, v102, v103
	ds_write_b16 v238, v2 offset:6688
	ds_write_b16_d16_hi v239, v2 offset:6688
	ds_write_b16 v240, v3 offset:6688
	ds_write_b16_d16_hi v241, v3 offset:6688
	ds_read_b128 v[2:5], v151 offset:4096
	ds_read_b128 v[10:13], v151 offset:4704
	s_waitcnt lgkmcnt(1)
	v_mfma_f32_16x16x32_f16 v[166:169], v[26:29], v[2:5], v[166:169]
	v_mfma_f32_16x16x32_f16 v[158:161], v[18:21], v[2:5], v[158:161]
	s_waitcnt lgkmcnt(0)
	v_mfma_f32_16x16x32_f16 v[170:173], v[26:29], v[10:13], v[170:173]
	v_mfma_f32_16x16x32_f16 v[162:165], v[18:21], v[10:13], v[162:165]
	ds_read_b128 v[2:5], v151 offset:5312
	ds_read_b128 v[10:13], v151 offset:5920
	s_waitcnt lgkmcnt(1)
	v_mfma_f32_16x16x32_f16 v[174:177], v[26:29], v[2:5], v[174:177]
	v_mfma_f32_16x16x32_f16 v[178:181], v[18:21], v[2:5], v[178:181]
	s_waitcnt lgkmcnt(0)
	v_mfma_f32_16x16x32_f16 v[186:189], v[26:29], v[10:13], v[186:189]
	v_mfma_f32_16x16x32_f16 v[190:193], v[18:21], v[10:13], v[190:193]
	v_add_u32_e32 v2, 0x10d100, v150
	v_min_u32_e32 v2, v2, v157
	v_cndmask_b32_e64 v2, 0, v2, s[0:1]
	global_load_dwordx4 v[98:101], v2, s[8:9] nt
	s_waitcnt vmcnt(21)
	v_cvt_pk_f16_f32 v3, v108, v109
	v_cvt_pk_f16_f32 v2, v106, v107
	ds_write_b16 v234, v2 offset:7296
	ds_write_b16_d16_hi v235, v2 offset:7296
	ds_write_b16 v236, v3 offset:7296
	ds_write_b16_d16_hi v237, v3 offset:7296
	ds_read_b128 v[2:5], v151 offset:6528
	ds_read_b128 v[10:13], v151 offset:7136
	s_mov_b32 s2, 0x30000
	ds_read_b128 v[102:105], v151 offset:7744
	s_waitcnt lgkmcnt(0)
	v_mfma_f32_16x16x32_f16 v[194:197], v[26:29], v[2:5], v[194:197]
	s_barrier
	v_sub_u32_e32 v245, v234, v243
	v_add_u32_e32 v246, 0xfffffdc0, v245
	v_min_u32_e32 v245, v245, v246
	v_add_u32_e32 v234, v242, v245
	v_sub_u32_e32 v245, v235, v243
	v_add_u32_e32 v246, 0xfffffdc0, v245
	v_min_u32_e32 v245, v245, v246
	v_add_u32_e32 v235, v242, v245
	v_sub_u32_e32 v245, v236, v243
	v_add_u32_e32 v246, 0xfffffdc0, v245
	v_min_u32_e32 v245, v245, v246
	v_add_u32_e32 v236, v242, v245
	v_sub_u32_e32 v245, v237, v243
	v_add_u32_e32 v246, 0xfffffdc0, v245
	v_min_u32_e32 v245, v245, v246
	v_add_u32_e32 v237, v242, v245
	v_sub_u32_e32 v245, v238, v243
	v_add_u32_e32 v246, 0xfffffdc0, v245
	v_min_u32_e32 v245, v245, v246
	v_add_u32_e32 v238, v242, v245
	v_sub_u32_e32 v245, v239, v243
	v_add_u32_e32 v246, 0xfffffdc0, v245
	v_min_u32_e32 v245, v245, v246
	v_add_u32_e32 v239, v242, v245
	v_sub_u32_e32 v245, v240, v243
	v_add_u32_e32 v246, 0xfffffdc0, v245
	v_min_u32_e32 v245, v245, v246
	v_add_u32_e32 v240, v242, v245
	v_sub_u32_e32 v245, v241, v243
	v_add_u32_e32 v246, 0xfffffdc0, v245
	v_min_u32_e32 v245, v245, v246
	v_add_u32_e32 v241, v242, v245
	v_mfma_f32_16x16x32_f16 v[182:185], v[18:21], v[2:5], v[182:185]
	v_add_co_u32_e32 v2, vcc, s2, v152
	s_mov_b32 s2, 0x34000
	s_nop 0
	v_addc_co_u32_e32 v3, vcc, 0, v153, vcc
	global_load_dwordx4 v[38:41], v[2:3], off sc1
	global_load_dwordx4 v[50:53], v[2:3], off offset:256 sc1
	v_add_co_u32_e32 v2, vcc, s2, v152
	v_mfma_f32_16x16x32_f16 v[202:205], v[26:29], v[10:13], v[202:205]
	s_nop 0
	v_addc_co_u32_e32 v3, vcc, 0, v153, vcc
	v_mfma_f32_16x16x32_f16 v[206:209], v[18:21], v[10:13], v[206:209]
	global_load_dwordx4 v[10:13], v[2:3], off sc1
	s_nop 0
	global_load_dwordx4 v[2:5], v[2:3], off offset:256 sc1
	v_mfma_f32_16x16x32_f16 v[26:29], v[26:29], v[102:105], v[218:221]
	v_mfma_f32_16x16x32_f16 v[18:21], v[18:21], v[102:105], v[54:57]
	v_add_u32_e32 v157, 0x11151cdc, v154
	s_nop 1
	ds_read_b128 v[54:57], v151 offset:512
	v_add_u32_e32 v102, 0x800, v150
	s_waitcnt vmcnt(24) lgkmcnt(0)
	v_mfma_f32_16x16x32_f16 v[198:201], v[42:45], v[54:57], v[198:201]
	s_waitcnt vmcnt(23)
	v_mfma_f32_16x16x32_f16 v[54:57], v[46:49], v[54:57], v[222:225]
	v_min_u32_e32 v102, v102, v157
	global_load_dwordx4 v[102:105], v102, s[8:9] nt
	s_waitcnt vmcnt(21)
	v_cvt_pk_f16_f32 v107, v112, v113
	v_cvt_pk_f16_f32 v106, v110, v111
	ds_write_b16 v234, v106 offset:0
	ds_write_b16_d16_hi v235, v106 offset:0
	ds_write_b16 v236, v107 offset:0
	ds_write_b16_d16_hi v237, v107 offset:0
	ds_read_b128 v[106:109], v151 offset:1120
	ds_read_b128 v[110:113], v151 offset:1728
	s_waitcnt lgkmcnt(1)
	v_mfma_f32_16x16x32_f16 v[218:221], v[42:45], v[106:109], v[226:229]
	v_mfma_f32_16x16x32_f16 v[122:125], v[46:49], v[106:109], v[122:125]
	s_waitcnt lgkmcnt(0)
	v_mfma_f32_16x16x32_f16 v[126:129], v[42:45], v[110:113], v[126:129]
	v_mfma_f32_16x16x32_f16 v[130:133], v[46:49], v[110:113], v[130:133]
	ds_read_b128 v[106:109], v151 offset:2336
	ds_read_b128 v[110:113], v151 offset:2944
	s_waitcnt lgkmcnt(1)
	v_mfma_f32_16x16x32_f16 v[134:137], v[42:45], v[106:109], v[134:137]
	v_mfma_f32_16x16x32_f16 v[138:141], v[46:49], v[106:109], v[138:141]
	s_waitcnt lgkmcnt(0)
	v_mfma_f32_16x16x32_f16 v[142:145], v[42:45], v[110:113], v[142:145]
	v_mfma_f32_16x16x32_f16 v[146:149], v[46:49], v[110:113], v[146:149]
	v_add_u32_e32 v106, 0x16e40, v244
	v_min_u32_e32 v106, v106, v157
	global_load_dwordx4 v[106:109], v106, s[8:9] nt
	s_waitcnt vmcnt(21)
	v_cvt_pk_f16_f32 v111, v116, v117
	v_cvt_pk_f16_f32 v110, v114, v115
	ds_write_b16 v238, v110 offset:608
	ds_write_b16_d16_hi v239, v110 offset:608
	ds_write_b16 v240, v111 offset:608
	ds_write_b16_d16_hi v241, v111 offset:608
	ds_read_b128 v[110:113], v151 offset:3552
	ds_read_b128 v[114:117], v151 offset:5376
	s_waitcnt lgkmcnt(1)
	v_mfma_f32_16x16x32_f16 v[210:213], v[42:45], v[110:113], v[210:213]
	v_mfma_f32_16x16x32_f16 v[214:217], v[46:49], v[110:113], v[214:217]
	ds_read_b128 v[110:113], v151 offset:4160
	ds_read_b128 v[222:225], v151 offset:4768
	s_waitcnt lgkmcnt(1)
	v_mfma_f32_16x16x32_f16 v[166:169], v[42:45], v[110:113], v[166:169]
	v_mfma_f32_16x16x32_f16 v[158:161], v[46:49], v[110:113], v[158:161]
	s_waitcnt lgkmcnt(0)
	v_mfma_f32_16x16x32_f16 v[170:173], v[42:45], v[222:225], v[170:173]
	v_mfma_f32_16x16x32_f16 v[162:165], v[46:49], v[222:225], v[162:165]
	v_mfma_f32_16x16x32_f16 v[174:177], v[42:45], v[114:117], v[174:177]
	v_mfma_f32_16x16x32_f16 v[178:181], v[46:49], v[114:117], v[178:181]
	v_add_u32_e32 v110, 0x2d480, v150
	v_min_u32_e32 v110, v110, v157
	global_load_dwordx4 v[110:113], v110, s[8:9] nt
	s_waitcnt vmcnt(21)
	v_cvt_pk_f16_f32 v115, v120, v121
	v_cvt_pk_f16_f32 v114, v118, v119
	ds_write_b16 v234, v114 offset:1216
	ds_write_b16_d16_hi v235, v114 offset:1216
	ds_write_b16 v236, v115 offset:1216
	ds_write_b16_d16_hi v237, v115 offset:1216
	ds_read_b128 v[114:117], v151 offset:5984
	ds_read_b128 v[118:121], v151 offset:6592
	s_waitcnt lgkmcnt(1)
	v_mfma_f32_16x16x32_f16 v[186:189], v[42:45], v[114:117], v[186:189]
	v_mfma_f32_16x16x32_f16 v[190:193], v[46:49], v[114:117], v[190:193]
	s_waitcnt lgkmcnt(0)
	v_mfma_f32_16x16x32_f16 v[194:197], v[42:45], v[118:121], v[194:197]
	v_mfma_f32_16x16x32_f16 v[182:185], v[46:49], v[118:121], v[182:185]
	ds_read_b128 v[114:117], v151 offset:7200
	ds_read_b128 v[118:121], v151 offset:7808
	s_waitcnt lgkmcnt(1)
	v_mfma_f32_16x16x32_f16 v[202:205], v[42:45], v[114:117], v[202:205]
	v_mfma_f32_16x16x32_f16 v[206:209], v[46:49], v[114:117], v[206:209]
	s_waitcnt lgkmcnt(0)
	v_mfma_f32_16x16x32_f16 v[26:29], v[42:45], v[118:121], v[26:29]
	v_mfma_f32_16x16x32_f16 v[42:45], v[46:49], v[118:121], v[18:21]
	s_nop 2
	v_add_u32_e32 v18, 0x43ac0, v244
	v_min_u32_e32 v18, v18, v157
	global_load_dwordx4 v[114:117], v18, s[8:9] nt
	s_waitcnt vmcnt(21)
	v_cvt_pk_f16_f32 v19, v36, v37
	v_cvt_pk_f16_f32 v18, v34, v35
	ds_write_b16 v238, v18 offset:1824
	ds_write_b16_d16_hi v239, v18 offset:1824
	ds_write_b16 v240, v19 offset:1824
	ds_write_b16_d16_hi v241, v19 offset:1824
	ds_read_b128 v[18:21], v151 offset:0
	ds_read_b128 v[34:37], v151 offset:608
	s_waitcnt lgkmcnt(1)
	v_mfma_f32_16x16x32_f16 v[46:49], v[22:25], v[18:21], v[198:201]
	v_mfma_f32_16x16x32_f16 v[198:201], v[6:9], v[18:21], v[54:57]
	s_waitcnt lgkmcnt(0)
	v_mfma_f32_16x16x32_f16 v[218:221], v[22:25], v[34:37], v[218:221]
	v_mfma_f32_16x16x32_f16 v[222:225], v[6:9], v[34:37], v[122:125]
	ds_read_b128 v[18:21], v151 offset:1216
	ds_read_b128 v[34:37], v151 offset:1824
	s_waitcnt lgkmcnt(1)
	v_mfma_f32_16x16x32_f16 v[126:129], v[22:25], v[18:21], v[126:129]
	v_mfma_f32_16x16x32_f16 v[130:133], v[6:9], v[18:21], v[130:133]
	s_waitcnt lgkmcnt(0)
	v_mfma_f32_16x16x32_f16 v[134:137], v[22:25], v[34:37], v[134:137]
	v_mfma_f32_16x16x32_f16 v[138:141], v[6:9], v[34:37], v[138:141]
	v_add_u32_e32 v18, 0x5a100, v150
	v_min_u32_e32 v18, v18, v157
	global_load_dwordx4 v[118:121], v18, s[8:9] nt
	s_waitcnt vmcnt(21)
	v_cvt_pk_f16_f32 v19, v68, v69
	v_cvt_pk_f16_f32 v18, v66, v67
	ds_write_b16 v234, v18 offset:2432
	ds_write_b16_d16_hi v235, v18 offset:2432
	ds_write_b16 v236, v19 offset:2432
	ds_write_b16_d16_hi v237, v19 offset:2432
	ds_read_b128 v[18:21], v151 offset:2432
	ds_read_b128 v[34:37], v151 offset:3040
	s_waitcnt lgkmcnt(1)
	v_mfma_f32_16x16x32_f16 v[142:145], v[22:25], v[18:21], v[142:145]
	v_mfma_f32_16x16x32_f16 v[146:149], v[6:9], v[18:21], v[146:149]
	s_waitcnt lgkmcnt(0)
	v_mfma_f32_16x16x32_f16 v[210:213], v[22:25], v[34:37], v[210:213]
	v_mfma_f32_16x16x32_f16 v[214:217], v[6:9], v[34:37], v[214:217]
	ds_read_b128 v[18:21], v151 offset:3648
	ds_read_b128 v[34:37], v151 offset:4256
	s_waitcnt lgkmcnt(1)
	v_mfma_f32_16x16x32_f16 v[166:169], v[22:25], v[18:21], v[166:169]
	v_mfma_f32_16x16x32_f16 v[158:161], v[6:9], v[18:21], v[158:161]
	s_waitcnt lgkmcnt(0)
	v_mfma_f32_16x16x32_f16 v[170:173], v[22:25], v[34:37], v[170:173]
	v_mfma_f32_16x16x32_f16 v[162:165], v[6:9], v[34:37], v[162:165]
	v_add_u32_e32 v18, 0x70740, v244
	v_min_u32_e32 v18, v18, v157
	global_load_dwordx4 v[122:125], v18, s[8:9] nt
	s_waitcnt vmcnt(21)
	v_cvt_pk_f16_f32 v19, v72, v73
	v_cvt_pk_f16_f32 v18, v70, v71
	ds_write_b16 v238, v18 offset:3040
	ds_write_b16_d16_hi v239, v18 offset:3040
	ds_write_b16 v240, v19 offset:3040
	ds_write_b16_d16_hi v241, v19 offset:3040
	ds_read_b128 v[18:21], v151 offset:4864
	ds_read_b128 v[34:37], v151 offset:5472
	s_waitcnt lgkmcnt(1)
	v_mfma_f32_16x16x32_f16 v[174:177], v[22:25], v[18:21], v[174:177]
	v_mfma_f32_16x16x32_f16 v[178:181], v[6:9], v[18:21], v[178:181]
	s_waitcnt lgkmcnt(0)
	v_mfma_f32_16x16x32_f16 v[186:189], v[22:25], v[34:37], v[186:189]
	v_mfma_f32_16x16x32_f16 v[190:193], v[6:9], v[34:37], v[190:193]
	ds_read_b128 v[18:21], v151 offset:6080
	ds_read_b128 v[34:37], v151 offset:6688
	s_waitcnt lgkmcnt(1)
	v_mfma_f32_16x16x32_f16 v[194:197], v[22:25], v[18:21], v[194:197]
	v_mfma_f32_16x16x32_f16 v[182:185], v[6:9], v[18:21], v[182:185]
	s_waitcnt lgkmcnt(0)
	v_mfma_f32_16x16x32_f16 v[202:205], v[22:25], v[34:37], v[202:205]
	v_mfma_f32_16x16x32_f16 v[206:209], v[6:9], v[34:37], v[206:209]
	v_add_u32_e32 v18, 0x86d80, v150
	v_min_u32_e32 v18, v18, v157
	global_load_dwordx4 v[70:73], v18, s[8:9] nt
	s_waitcnt vmcnt(21)
	v_cvt_pk_f16_f32 v19, v76, v77
	v_cvt_pk_f16_f32 v18, v74, v75
	ds_write_b16 v234, v18 offset:3648
	ds_write_b16_d16_hi v235, v18 offset:3648
	ds_write_b16 v236, v19 offset:3648
	ds_write_b16_d16_hi v237, v19 offset:3648
	s_mov_b32 s2, 0x38000
	v_add_co_u32_e32 v18, vcc, s2, v152
	s_mov_b32 s2, 0x3c000
	s_nop 0
	v_addc_co_u32_e32 v19, vcc, 0, v153, vcc
	ds_read_b128 v[74:77], v151 offset:7296
	global_load_dwordx4 v[54:57], v[18:19], off sc1
	global_load_dwordx4 v[66:69], v[18:19], off offset:256 sc1
	v_add_co_u32_e32 v18, vcc, s2, v152
	s_waitcnt lgkmcnt(0)
	v_mfma_f32_16x16x32_f16 v[22:25], v[22:25], v[74:77], v[26:29]
	v_addc_co_u32_e32 v19, vcc, 0, v153, vcc
	global_load_dwordx4 v[34:37], v[18:19], off sc1
	s_nop 0
	global_load_dwordx4 v[18:21], v[18:19], off offset:256 sc1
	v_mfma_f32_16x16x32_f16 v[6:9], v[6:9], v[74:77], v[42:45]
	ds_read_b128 v[26:29], v151 offset:64
	s_nop 1
	ds_read_b128 v[42:45], v151 offset:672
	s_waitcnt vmcnt(24) lgkmcnt(1)
	v_mfma_f32_16x16x32_f16 v[46:49], v[58:61], v[26:29], v[46:49]
	s_waitcnt vmcnt(23)
	v_mfma_f32_16x16x32_f16 v[26:29], v[62:65], v[26:29], v[198:201]
	s_nop 2
	ds_read_b128 v[198:201], v151 offset:1280
	s_waitcnt lgkmcnt(1)
	v_mfma_f32_16x16x32_f16 v[74:77], v[58:61], v[42:45], v[218:221]
	v_mfma_f32_16x16x32_f16 v[42:45], v[62:65], v[42:45], v[222:225]
	s_waitcnt lgkmcnt(0)
	v_mfma_f32_16x16x32_f16 v[218:221], v[58:61], v[198:201], v[126:129]
	v_mfma_f32_16x16x32_f16 v[130:133], v[62:65], v[198:201], v[130:133]
	s_nop 1
	v_add_u32_e32 v126, 0x9d3c0, v244
	v_min_u32_e32 v126, v126, v157
	global_load_dwordx4 v[126:129], v126, s[8:9] nt
	s_waitcnt vmcnt(21)
	v_cvt_pk_f16_f32 v81, v80, v81
	v_cvt_pk_f16_f32 v80, v78, v79
	ds_write_b16 v238, v80 offset:4256
	ds_write_b16_d16_hi v239, v80 offset:4256
	ds_write_b16 v240, v81 offset:4256
	ds_write_b16_d16_hi v241, v81 offset:4256
	ds_read_b128 v[78:81], v151 offset:1888
	ds_read_b128 v[198:201], v151 offset:2496
	s_waitcnt lgkmcnt(1)
	v_mfma_f32_16x16x32_f16 v[134:137], v[58:61], v[78:81], v[134:137]
	v_mfma_f32_16x16x32_f16 v[138:141], v[62:65], v[78:81], v[138:141]
	s_waitcnt lgkmcnt(0)
	v_mfma_f32_16x16x32_f16 v[142:145], v[58:61], v[198:201], v[142:145]
	v_mfma_f32_16x16x32_f16 v[146:149], v[62:65], v[198:201], v[146:149]
	ds_read_b128 v[78:81], v151 offset:3104
	ds_read_b128 v[198:201], v151 offset:3712
	s_waitcnt lgkmcnt(1)
	v_mfma_f32_16x16x32_f16 v[210:213], v[58:61], v[78:81], v[210:213]
	v_mfma_f32_16x16x32_f16 v[214:217], v[62:65], v[78:81], v[214:217]
	s_waitcnt lgkmcnt(0)
	v_mfma_f32_16x16x32_f16 v[166:169], v[58:61], v[198:201], v[166:169]
	v_mfma_f32_16x16x32_f16 v[158:161], v[62:65], v[198:201], v[158:161]
	v_add_u32_e32 v78, 0xb3a00, v150
	v_min_u32_e32 v78, v78, v157
	global_load_dwordx4 v[78:81], v78, s[8:9] nt
	s_waitcnt vmcnt(21)
	v_cvt_pk_f16_f32 v85, v84, v85
	v_cvt_pk_f16_f32 v84, v82, v83
	ds_write_b16 v234, v84 offset:4864
	ds_write_b16_d16_hi v235, v84 offset:4864
	ds_write_b16 v236, v85 offset:4864
	ds_write_b16_d16_hi v237, v85 offset:4864
	ds_read_b128 v[82:85], v151 offset:4320
	ds_read_b128 v[198:201], v151 offset:6144
	s_waitcnt lgkmcnt(1)
	v_mfma_f32_16x16x32_f16 v[170:173], v[58:61], v[82:85], v[170:173]
	v_mfma_f32_16x16x32_f16 v[162:165], v[62:65], v[82:85], v[162:165]
	ds_read_b128 v[82:85], v151 offset:4928
	ds_read_b128 v[222:225], v151 offset:5536
	s_waitcnt lgkmcnt(1)
	v_mfma_f32_16x16x32_f16 v[174:177], v[58:61], v[82:85], v[174:177]
	v_mfma_f32_16x16x32_f16 v[178:181], v[62:65], v[82:85], v[178:181]
	s_waitcnt lgkmcnt(0)
	v_mfma_f32_16x16x32_f16 v[186:189], v[58:61], v[222:225], v[186:189]
	v_mfma_f32_16x16x32_f16 v[190:193], v[62:65], v[222:225], v[190:193]
	v_mfma_f32_16x16x32_f16 v[194:197], v[58:61], v[198:201], v[194:197]
	v_mfma_f32_16x16x32_f16 v[182:185], v[62:65], v[198:201], v[182:185]
	v_add_u32_e32 v82, 0xca040, v244
	v_min_u32_e32 v82, v82, v157
	global_load_dwordx4 v[82:85], v82, s[8:9] nt
	s_waitcnt vmcnt(21)
	v_cvt_pk_f16_f32 v89, v88, v89
	v_cvt_pk_f16_f32 v88, v86, v87
	ds_write_b16 v238, v88 offset:5472
	ds_write_b16_d16_hi v239, v88 offset:5472
	ds_write_b16 v240, v89 offset:5472
	ds_write_b16_d16_hi v241, v89 offset:5472
	ds_read_b128 v[86:89], v151 offset:6752
	ds_read_b128 v[198:201], v151 offset:7360
	s_waitcnt lgkmcnt(1)
	v_mfma_f32_16x16x32_f16 v[202:205], v[58:61], v[86:89], v[202:205]
	s_waitcnt lgkmcnt(0)
	v_mfma_f32_16x16x32_f16 v[22:25], v[58:61], v[198:201], v[22:25]
	v_mfma_f32_16x16x32_f16 v[198:201], v[62:65], v[198:201], v[6:9]
	s_nop 2
	ds_read_b128 v[6:9], v151 offset:128
	ds_read_b128 v[58:61], v151 offset:736
	v_mfma_f32_16x16x32_f16 v[206:209], v[62:65], v[86:89], v[206:209]
	s_waitcnt lgkmcnt(1)
	v_mfma_f32_16x16x32_f16 v[222:225], v[30:33], v[6:9], v[46:49]
	v_mfma_f32_16x16x32_f16 v[226:229], v[14:17], v[6:9], v[26:29]
	s_waitcnt lgkmcnt(0)
	v_mfma_f32_16x16x32_f16 v[74:77], v[30:33], v[58:61], v[74:77]
	v_mfma_f32_16x16x32_f16 v[230:233], v[14:17], v[58:61], v[42:45]
	v_add_u32_e32 v6, 0xe0680, v150
	v_min_u32_e32 v6, v6, v157
	global_load_dwordx4 v[58:61], v6, s[8:9] nt
	s_waitcnt vmcnt(21)
	v_cvt_pk_f16_f32 v7, v92, v93
	v_cvt_pk_f16_f32 v6, v90, v91
	ds_write_b16 v234, v6 offset:6080
	ds_write_b16_d16_hi v235, v6 offset:6080
	ds_write_b16 v236, v7 offset:6080
	ds_write_b16_d16_hi v237, v7 offset:6080
	ds_read_b128 v[6:9], v151 offset:1344
	ds_read_b128 v[26:29], v151 offset:1952
	s_waitcnt lgkmcnt(1)
	v_mfma_f32_16x16x32_f16 v[90:93], v[30:33], v[6:9], v[218:221]
	v_mfma_f32_16x16x32_f16 v[130:133], v[14:17], v[6:9], v[130:133]
	s_waitcnt lgkmcnt(0)
	v_mfma_f32_16x16x32_f16 v[134:137], v[30:33], v[26:29], v[134:137]
	v_mfma_f32_16x16x32_f16 v[138:141], v[14:17], v[26:29], v[138:141]
	ds_read_b128 v[6:9], v151 offset:2560
	ds_read_b128 v[26:29], v151 offset:3168
	s_waitcnt lgkmcnt(1)
	v_mfma_f32_16x16x32_f16 v[142:145], v[30:33], v[6:9], v[142:145]
	v_mfma_f32_16x16x32_f16 v[146:149], v[14:17], v[6:9], v[146:149]
	s_waitcnt lgkmcnt(0)
	v_mfma_f32_16x16x32_f16 v[210:213], v[30:33], v[26:29], v[210:213]
	v_mfma_f32_16x16x32_f16 v[214:217], v[14:17], v[26:29], v[214:217]
	v_add_u32_e32 v6, 0xf6cc0, v244
	v_min_u32_e32 v6, v6, v157
	global_load_dwordx4 v[62:65], v6, s[8:9] nt
	s_waitcnt vmcnt(21)
	v_cvt_pk_f16_f32 v7, v96, v97
	v_cvt_pk_f16_f32 v6, v94, v95
	ds_write_b16 v238, v6 offset:6688
	ds_write_b16_d16_hi v239, v6 offset:6688
	ds_write_b16 v240, v7 offset:6688
	ds_write_b16_d16_hi v241, v7 offset:6688
	ds_read_b128 v[6:9], v151 offset:3776
	ds_read_b128 v[26:29], v151 offset:4384
	s_waitcnt lgkmcnt(1)
	v_mfma_f32_16x16x32_f16 v[94:97], v[30:33], v[6:9], v[166:169]
	v_mfma_f32_16x16x32_f16 v[158:161], v[14:17], v[6:9], v[158:161]
	s_waitcnt lgkmcnt(0)
	v_mfma_f32_16x16x32_f16 v[166:169], v[30:33], v[26:29], v[170:173]
	v_mfma_f32_16x16x32_f16 v[162:165], v[14:17], v[26:29], v[162:165]
	ds_read_b128 v[6:9], v151 offset:4992
	ds_read_b128 v[26:29], v151 offset:5600
	s_waitcnt lgkmcnt(1)
	v_mfma_f32_16x16x32_f16 v[170:173], v[30:33], v[6:9], v[174:177]
	v_mfma_f32_16x16x32_f16 v[174:177], v[14:17], v[6:9], v[178:181]
	s_waitcnt lgkmcnt(0)
	v_mfma_f32_16x16x32_f16 v[178:181], v[30:33], v[26:29], v[186:189]
	v_mfma_f32_16x16x32_f16 v[186:189], v[14:17], v[26:29], v[190:193]
	v_add_u32_e32 v6, 0x10d300, v150
	v_min_u32_e32 v6, v6, v157
	v_cndmask_b32_e64 v6, 0, v6, s[0:1]
	global_load_dwordx4 v[86:89], v6, s[8:9] nt
	s_waitcnt vmcnt(21)
	v_cvt_pk_f16_f32 v7, v100, v101
	v_cvt_pk_f16_f32 v6, v98, v99
	ds_write_b16 v234, v6 offset:7296
	ds_write_b16_d16_hi v235, v6 offset:7296
	ds_write_b16 v236, v7 offset:7296
	ds_write_b16_d16_hi v237, v7 offset:7296
	ds_read_b128 v[6:9], v151 offset:6208
	ds_read_b128 v[26:29], v151 offset:6816
	s_mov_b32 s2, 0x40000
	ds_read_b128 v[190:193], v151 offset:7424
	s_waitcnt lgkmcnt(0)
	v_mfma_f32_16x16x32_f16 v[98:101], v[30:33], v[6:9], v[194:197]
	s_barrier
	v_sub_u32_e32 v245, v234, v243
	v_add_u32_e32 v246, 0xfffffdc0, v245
	v_min_u32_e32 v245, v245, v246
	v_add_u32_e32 v234, v242, v245
	v_sub_u32_e32 v245, v235, v243
	v_add_u32_e32 v246, 0xfffffdc0, v245
	v_min_u32_e32 v245, v245, v246
	v_add_u32_e32 v235, v242, v245
	v_sub_u32_e32 v245, v236, v243
	v_add_u32_e32 v246, 0xfffffdc0, v245
	v_min_u32_e32 v245, v245, v246
	v_add_u32_e32 v236, v242, v245
	v_sub_u32_e32 v245, v237, v243
	v_add_u32_e32 v246, 0xfffffdc0, v245
	v_min_u32_e32 v245, v245, v246
	v_add_u32_e32 v237, v242, v245
	v_sub_u32_e32 v245, v238, v243
	v_add_u32_e32 v246, 0xfffffdc0, v245
	v_min_u32_e32 v245, v245, v246
	v_add_u32_e32 v238, v242, v245
	v_sub_u32_e32 v245, v239, v243
	v_add_u32_e32 v246, 0xfffffdc0, v245
	v_min_u32_e32 v245, v245, v246
	v_add_u32_e32 v239, v242, v245
	v_sub_u32_e32 v245, v240, v243
	v_add_u32_e32 v246, 0xfffffdc0, v245
	v_min_u32_e32 v245, v245, v246
	v_add_u32_e32 v240, v242, v245
	v_sub_u32_e32 v245, v241, v243
	v_add_u32_e32 v246, 0xfffffdc0, v245
	v_min_u32_e32 v245, v245, v246
	v_add_u32_e32 v241, v242, v245
	v_mfma_f32_16x16x32_f16 v[182:185], v[14:17], v[6:9], v[182:185]
	v_add_co_u32_e32 v6, vcc, s2, v152
	s_mov_b32 s2, 0x44000
	s_nop 0
	v_addc_co_u32_e32 v7, vcc, 0, v153, vcc
	global_load_dwordx4 v[42:45], v[6:7], off sc1
	global_load_dwordx4 v[46:49], v[6:7], off offset:256 sc1
	v_add_co_u32_e32 v6, vcc, s2, v152
	v_mfma_f32_16x16x32_f16 v[194:197], v[30:33], v[26:29], v[202:205]
	s_nop 0
	v_addc_co_u32_e32 v7, vcc, 0, v153, vcc
	v_mfma_f32_16x16x32_f16 v[202:205], v[14:17], v[26:29], v[206:209]
	global_load_dwordx4 v[26:29], v[6:7], off sc1
	s_nop 0
	global_load_dwordx4 v[6:9], v[6:7], off offset:256 sc1
	v_mfma_f32_16x16x32_f16 v[22:25], v[30:33], v[190:193], v[22:25]
	v_mfma_f32_16x16x32_f16 v[30:33], v[14:17], v[190:193], v[198:201]
	v_add_u32_e32 v157, 0x11151edc, v154
	ds_read_b128 v[14:17], v151 offset:192
	v_add_u32_e32 v206, 0xa00, v150
	s_waitcnt vmcnt(24) lgkmcnt(0)
	v_mfma_f32_16x16x32_f16 v[190:193], v[38:41], v[14:17], v[222:225]
	s_waitcnt vmcnt(23)
	v_mfma_f32_16x16x32_f16 v[198:201], v[50:53], v[14:17], v[226:229]
	v_min_u32_e32 v14, v206, v157
	global_load_dwordx4 v[14:17], v14, s[8:9] nt
	s_waitcnt vmcnt(21)
	v_cvt_pk_f16_f32 v105, v104, v105
	v_cvt_pk_f16_f32 v104, v102, v103
	ds_write_b16 v234, v104 offset:0
	ds_write_b16_d16_hi v235, v104 offset:0
	ds_write_b16 v236, v105 offset:0
	ds_write_b16_d16_hi v237, v105 offset:0
	ds_read_b128 v[102:105], v151 offset:800
	ds_read_b128 v[206:209], v151 offset:1408
	s_waitcnt lgkmcnt(1)
	v_mfma_f32_16x16x32_f16 v[74:77], v[38:41], v[102:105], v[74:77]
	s_waitcnt lgkmcnt(0)
	v_mfma_f32_16x16x32_f16 v[218:221], v[38:41], v[206:209], v[90:93]
	v_mfma_f32_16x16x32_f16 v[130:133], v[50:53], v[206:209], v[130:133]
	s_nop 1
	ds_read_b128 v[90:93], v151 offset:2016
	ds_read_b128 v[206:209], v151 offset:2624
	v_mfma_f32_16x16x32_f16 v[102:105], v[50:53], v[102:105], v[230:233]
	s_waitcnt lgkmcnt(1)
	v_mfma_f32_16x16x32_f16 v[134:137], v[38:41], v[90:93], v[134:137]
	v_mfma_f32_16x16x32_f16 v[138:141], v[50:53], v[90:93], v[138:141]
	s_waitcnt lgkmcnt(0)
	v_mfma_f32_16x16x32_f16 v[142:145], v[38:41], v[206:209], v[142:145]
	v_mfma_f32_16x16x32_f16 v[146:149], v[50:53], v[206:209], v[146:149]
	v_add_u32_e32 v90, 0x17040, v244
	v_min_u32_e32 v90, v90, v157
	global_load_dwordx4 v[90:93], v90, s[8:9] nt
	s_waitcnt vmcnt(21)
	v_cvt_pk_f16_f32 v109, v108, v109
	v_cvt_pk_f16_f32 v108, v106, v107
	ds_write_b16 v238, v108 offset:608
	ds_write_b16_d16_hi v239, v108 offset:608
	ds_write_b16 v240, v109 offset:608
	ds_write_b16_d16_hi v241, v109 offset:608
	ds_read_b128 v[106:109], v151 offset:3232
	ds_read_b128 v[206:209], v151 offset:5056
	s_waitcnt lgkmcnt(1)
	v_mfma_f32_16x16x32_f16 v[210:213], v[38:41], v[106:109], v[210:213]
	v_mfma_f32_16x16x32_f16 v[106:109], v[50:53], v[106:109], v[214:217]
	s_nop 2
	ds_read_b128 v[214:217], v151 offset:3840
	ds_read_b128 v[222:225], v151 offset:4448
	s_waitcnt lgkmcnt(1)
	v_mfma_f32_16x16x32_f16 v[226:229], v[38:41], v[214:217], v[94:97]
	v_mfma_f32_16x16x32_f16 v[158:161], v[50:53], v[214:217], v[158:161]
	s_waitcnt lgkmcnt(0)
	v_mfma_f32_16x16x32_f16 v[166:169], v[38:41], v[222:225], v[166:169]
	v_mfma_f32_16x16x32_f16 v[162:165], v[50:53], v[222:225], v[162:165]
	v_mfma_f32_16x16x32_f16 v[170:173], v[38:41], v[206:209], v[170:173]
	v_mfma_f32_16x16x32_f16 v[174:177], v[50:53], v[206:209], v[174:177]
	v_add_u32_e32 v94, 0x2d680, v150
	v_min_u32_e32 v94, v94, v157
	global_load_dwordx4 v[94:97], v94, s[8:9] nt
	s_waitcnt vmcnt(21)
	v_cvt_pk_f16_f32 v113, v112, v113
	v_cvt_pk_f16_f32 v112, v110, v111
	ds_write_b16 v234, v112 offset:1216
	ds_write_b16_d16_hi v235, v112 offset:1216
	ds_write_b16 v236, v113 offset:1216
	ds_write_b16_d16_hi v237, v113 offset:1216
	ds_read_b128 v[110:113], v151 offset:5664
	ds_read_b128 v[206:209], v151 offset:6272
	s_waitcnt lgkmcnt(1)
	v_mfma_f32_16x16x32_f16 v[178:181], v[38:41], v[110:113], v[178:181]
	v_mfma_f32_16x16x32_f16 v[110:113], v[50:53], v[110:113], v[186:189]
	s_waitcnt lgkmcnt(0)
	v_mfma_f32_16x16x32_f16 v[186:189], v[38:41], v[206:209], v[98:101]
	v_mfma_f32_16x16x32_f16 v[182:185], v[50:53], v[206:209], v[182:185]
	s_nop 1
	ds_read_b128 v[98:101], v151 offset:6880
	ds_read_b128 v[206:209], v151 offset:7488
	s_waitcnt lgkmcnt(1)
	v_mfma_f32_16x16x32_f16 v[194:197], v[38:41], v[98:101], v[194:197]
	v_mfma_f32_16x16x32_f16 v[202:205], v[50:53], v[98:101], v[202:205]
	s_waitcnt lgkmcnt(0)
	v_mfma_f32_16x16x32_f16 v[22:25], v[38:41], v[206:209], v[22:25]
	v_mfma_f32_16x16x32_f16 v[30:33], v[50:53], v[206:209], v[30:33]
	v_add_u32_e32 v38, 0x43cc0, v244
	v_min_u32_e32 v38, v38, v157
	global_load_dwordx4 v[98:101], v38, s[8:9] nt
	s_waitcnt vmcnt(21)
	v_cvt_pk_f16_f32 v39, v116, v117
	v_cvt_pk_f16_f32 v38, v114, v115
	ds_write_b16 v238, v38 offset:1824
	ds_write_b16_d16_hi v239, v38 offset:1824
	ds_write_b16 v240, v39 offset:1824
	ds_write_b16_d16_hi v241, v39 offset:1824
	ds_read_b128 v[38:41], v151 offset:256
	ds_read_b128 v[50:53], v151 offset:864
	s_waitcnt lgkmcnt(1)
	v_mfma_f32_16x16x32_f16 v[114:117], v[10:13], v[38:41], v[190:193]
	v_mfma_f32_16x16x32_f16 v[190:193], v[2:5], v[38:41], v[198:201]
	s_waitcnt lgkmcnt(0)
	v_mfma_f32_16x16x32_f16 v[198:201], v[10:13], v[50:53], v[74:77]
	ds_read_b128 v[38:41], v151 offset:1472
	s_nop 1
	ds_read_b128 v[74:77], v151 offset:2080
	v_mfma_f32_16x16x32_f16 v[50:53], v[2:5], v[50:53], v[102:105]
	s_waitcnt lgkmcnt(1)
	v_mfma_f32_16x16x32_f16 v[206:209], v[10:13], v[38:41], v[218:221]
	v_mfma_f32_16x16x32_f16 v[130:133], v[2:5], v[38:41], v[130:133]
	s_waitcnt lgkmcnt(0)
	v_mfma_f32_16x16x32_f16 v[134:137], v[10:13], v[74:77], v[134:137]
	v_mfma_f32_16x16x32_f16 v[138:141], v[2:5], v[74:77], v[138:141]
	v_add_u32_e32 v38, 0x5a300, v150
	v_min_u32_e32 v38, v38, v157
	global_load_dwordx4 v[102:105], v38, s[8:9] nt
	s_waitcnt vmcnt(21)
	v_cvt_pk_f16_f32 v39, v120, v121
	v_cvt_pk_f16_f32 v38, v118, v119
	ds_write_b16 v234, v38 offset:2432
	ds_write_b16_d16_hi v235, v38 offset:2432
	ds_write_b16 v236, v39 offset:2432
	ds_write_b16_d16_hi v237, v39 offset:2432
	ds_read_b128 v[38:41], v151 offset:2688
	ds_read_b128 v[74:77], v151 offset:3296
	s_waitcnt lgkmcnt(1)
	v_mfma_f32_16x16x32_f16 v[118:121], v[10:13], v[38:41], v[142:145]
	v_mfma_f32_16x16x32_f16 v[142:145], v[2:5], v[38:41], v[146:149]
	s_waitcnt lgkmcnt(0)
	v_mfma_f32_16x16x32_f16 v[146:149], v[10:13], v[74:77], v[210:213]
	v_mfma_f32_16x16x32_f16 v[210:213], v[2:5], v[74:77], v[106:109]
	ds_read_b128 v[38:41], v151 offset:3904
	ds_read_b128 v[74:77], v151 offset:4512
	s_waitcnt lgkmcnt(1)
	v_mfma_f32_16x16x32_f16 v[214:217], v[10:13], v[38:41], v[226:229]
	v_mfma_f32_16x16x32_f16 v[158:161], v[2:5], v[38:41], v[158:161]
	s_waitcnt lgkmcnt(0)
	v_mfma_f32_16x16x32_f16 v[166:169], v[10:13], v[74:77], v[166:169]
	v_mfma_f32_16x16x32_f16 v[162:165], v[2:5], v[74:77], v[162:165]
	v_add_u32_e32 v38, 0x70940, v244
	v_min_u32_e32 v38, v38, v157
	global_load_dwordx4 v[106:109], v38, s[8:9] nt
	s_waitcnt vmcnt(21)
	v_cvt_pk_f16_f32 v39, v124, v125
	v_cvt_pk_f16_f32 v38, v122, v123
	ds_write_b16 v238, v38 offset:3040
	ds_write_b16_d16_hi v239, v38 offset:3040
	ds_write_b16 v240, v39 offset:3040
	ds_write_b16_d16_hi v241, v39 offset:3040
	ds_read_b128 v[38:41], v151 offset:5120
	ds_read_b128 v[74:77], v151 offset:5728
	s_waitcnt lgkmcnt(1)
	v_mfma_f32_16x16x32_f16 v[122:125], v[10:13], v[38:41], v[170:173]
	v_mfma_f32_16x16x32_f16 v[170:173], v[2:5], v[38:41], v[174:177]
	s_waitcnt lgkmcnt(0)
	v_mfma_f32_16x16x32_f16 v[174:177], v[10:13], v[74:77], v[178:181]
	v_mfma_f32_16x16x32_f16 v[178:181], v[2:5], v[74:77], v[110:113]
	ds_read_b128 v[38:41], v151 offset:6336
	ds_read_b128 v[74:77], v151 offset:6944
	s_waitcnt lgkmcnt(1)
	v_mfma_f32_16x16x32_f16 v[186:189], v[10:13], v[38:41], v[186:189]
	v_mfma_f32_16x16x32_f16 v[182:185], v[2:5], v[38:41], v[182:185]
	s_waitcnt lgkmcnt(0)
	v_mfma_f32_16x16x32_f16 v[194:197], v[10:13], v[74:77], v[194:197]
	v_mfma_f32_16x16x32_f16 v[202:205], v[2:5], v[74:77], v[202:205]
	v_add_u32_e32 v38, 0x86f80, v150
	v_min_u32_e32 v38, v38, v157
	global_load_dwordx4 v[110:113], v38, s[8:9] nt
	s_waitcnt vmcnt(21)
	v_cvt_pk_f16_f32 v39, v72, v73
	v_cvt_pk_f16_f32 v38, v70, v71
	ds_write_b16 v234, v38 offset:3648
	ds_write_b16_d16_hi v235, v38 offset:3648
	ds_write_b16 v236, v39 offset:3648
	ds_write_b16_d16_hi v237, v39 offset:3648
	ds_read_b128 v[218:221], v151 offset:7552
	s_mov_b32 s2, 0x48000
	s_waitcnt lgkmcnt(0)
	v_mfma_f32_16x16x32_f16 v[10:13], v[10:13], v[218:221], v[22:25]
	s_nop 2
	v_add_co_u32_e32 v22, vcc, s2, v152
	s_mov_b32 s2, 0x4c000
	s_nop 0
	v_addc_co_u32_e32 v23, vcc, 0, v153, vcc
	global_load_dwordx4 v[70:73], v[22:23], off sc1
	global_load_dwordx4 v[74:77], v[22:23], off offset:256 sc1
	v_add_co_u32_e32 v22, vcc, s2, v152
	v_mfma_f32_16x16x32_f16 v[30:33], v[2:5], v[218:221], v[30:33]
	s_nop 0
	v_addc_co_u32_e32 v23, vcc, 0, v153, vcc
	global_load_dwordx4 v[38:41], v[22:23], off sc1
	s_nop 0
	global_load_dwordx4 v[22:25], v[22:23], off offset:256 sc1
	ds_read_b128 v[2:5], v151 offset:320
	ds_read_b128 v[218:221], v151 offset:928
	s_waitcnt vmcnt(24) lgkmcnt(1)
	v_mfma_f32_16x16x32_f16 v[222:225], v[54:57], v[2:5], v[114:117]
	s_waitcnt vmcnt(23)
	v_mfma_f32_16x16x32_f16 v[190:193], v[66:69], v[2:5], v[190:193]
	ds_read_b128 v[2:5], v151 offset:1536
	s_waitcnt lgkmcnt(1)
	v_mfma_f32_16x16x32_f16 v[198:201], v[54:57], v[218:221], v[198:201]
	v_mfma_f32_16x16x32_f16 v[50:53], v[66:69], v[218:221], v[50:53]
	s_waitcnt lgkmcnt(0)
	v_mfma_f32_16x16x32_f16 v[206:209], v[54:57], v[2:5], v[206:209]
	v_mfma_f32_16x16x32_f16 v[130:133], v[66:69], v[2:5], v[130:133]
	v_add_u32_e32 v2, 0x9d5c0, v244
	v_min_u32_e32 v2, v2, v157
	global_load_dwordx4 v[2:5], v2, s[8:9] nt
	s_waitcnt vmcnt(21)
	v_cvt_pk_f16_f32 v115, v128, v129
	v_cvt_pk_f16_f32 v114, v126, v127
	ds_write_b16 v238, v114 offset:4256
	ds_write_b16_d16_hi v239, v114 offset:4256
	ds_write_b16 v240, v115 offset:4256
	ds_write_b16_d16_hi v241, v115 offset:4256
	ds_read_b128 v[114:117], v151 offset:2144
	ds_read_b128 v[126:129], v151 offset:2752
	s_waitcnt lgkmcnt(1)
	v_mfma_f32_16x16x32_f16 v[134:137], v[54:57], v[114:117], v[134:137]
	v_mfma_f32_16x16x32_f16 v[138:141], v[66:69], v[114:117], v[138:141]
	s_waitcnt lgkmcnt(0)
	v_mfma_f32_16x16x32_f16 v[118:121], v[54:57], v[126:129], v[118:121]
	v_mfma_f32_16x16x32_f16 v[126:129], v[66:69], v[126:129], v[142:145]
	ds_read_b128 v[114:117], v151 offset:3360
	s_nop 1
	ds_read_b128 v[142:145], v151 offset:3968
	s_waitcnt lgkmcnt(1)
	v_mfma_f32_16x16x32_f16 v[146:149], v[54:57], v[114:117], v[146:149]
	v_mfma_f32_16x16x32_f16 v[210:213], v[66:69], v[114:117], v[210:213]
	s_waitcnt lgkmcnt(0)
	v_mfma_f32_16x16x32_f16 v[214:217], v[54:57], v[142:145], v[214:217]
	v_mfma_f32_16x16x32_f16 v[142:145], v[66:69], v[142:145], v[158:161]
	v_add_u32_e32 v114, 0xb3c00, v150
	v_min_u32_e32 v114, v114, v157
	global_load_dwordx4 v[114:117], v114, s[8:9] nt
	s_waitcnt vmcnt(21)
	v_cvt_pk_f16_f32 v81, v80, v81
	v_cvt_pk_f16_f32 v80, v78, v79
	ds_write_b16 v234, v80 offset:4864
	ds_write_b16_d16_hi v235, v80 offset:4864
	ds_write_b16 v236, v81 offset:4864
	ds_write_b16_d16_hi v237, v81 offset:4864
	ds_read_b128 v[78:81], v151 offset:4576
	ds_read_b128 v[158:161], v151 offset:6400
	s_waitcnt lgkmcnt(1)
	v_mfma_f32_16x16x32_f16 v[166:169], v[54:57], v[78:81], v[166:169]
	v_mfma_f32_16x16x32_f16 v[162:165], v[66:69], v[78:81], v[162:165]
	ds_read_b128 v[78:81], v151 offset:5184
	ds_read_b128 v[218:221], v151 offset:5792
	s_waitcnt lgkmcnt(1)
	v_mfma_f32_16x16x32_f16 v[122:125], v[54:57], v[78:81], v[122:125]
	v_mfma_f32_16x16x32_f16 v[170:173], v[66:69], v[78:81], v[170:173]
	s_waitcnt lgkmcnt(0)
	v_mfma_f32_16x16x32_f16 v[174:177], v[54:57], v[218:221], v[174:177]
	v_mfma_f32_16x16x32_f16 v[178:181], v[66:69], v[218:221], v[178:181]
	v_mfma_f32_16x16x32_f16 v[186:189], v[54:57], v[158:161], v[186:189]
	v_mfma_f32_16x16x32_f16 v[158:161], v[66:69], v[158:161], v[182:185]
	v_add_u32_e32 v78, 0xca240, v244
	v_min_u32_e32 v78, v78, v157
	global_load_dwordx4 v[78:81], v78, s[8:9] nt
	s_waitcnt vmcnt(21)
	v_cvt_pk_f16_f32 v85, v84, v85
	v_cvt_pk_f16_f32 v84, v82, v83
	ds_write_b16 v238, v84 offset:5472
	ds_write_b16_d16_hi v239, v84 offset:5472
	ds_write_b16 v240, v85 offset:5472
	ds_write_b16_d16_hi v241, v85 offset:5472
	ds_read_b128 v[82:85], v151 offset:7008
	ds_read_b128 v[182:185], v151 offset:7616
	s_waitcnt lgkmcnt(1)
	v_mfma_f32_16x16x32_f16 v[194:197], v[54:57], v[82:85], v[194:197]
	s_waitcnt lgkmcnt(0)
	v_mfma_f32_16x16x32_f16 v[10:13], v[54:57], v[182:185], v[10:13]
	v_mfma_f32_16x16x32_f16 v[182:185], v[66:69], v[182:185], v[30:33]
	s_nop 2
	ds_read_b128 v[30:33], v151 offset:384
	ds_read_b128 v[54:57], v151 offset:992
	v_mfma_f32_16x16x32_f16 v[202:205], v[66:69], v[82:85], v[202:205]
	s_waitcnt lgkmcnt(1)
	v_mfma_f32_16x16x32_f16 v[218:221], v[34:37], v[30:33], v[222:225]
	v_mfma_f32_16x16x32_f16 v[190:193], v[18:21], v[30:33], v[190:193]
	s_waitcnt lgkmcnt(0)
	v_mfma_f32_16x16x32_f16 v[198:201], v[34:37], v[54:57], v[198:201]
	v_mfma_f32_16x16x32_f16 v[222:225], v[18:21], v[54:57], v[50:53]
	v_add_u32_e32 v30, 0xe0880, v150
	v_min_u32_e32 v30, v30, v157
	global_load_dwordx4 v[66:69], v30, s[8:9] nt
	s_waitcnt vmcnt(21)
	v_cvt_pk_f16_f32 v31, v60, v61
	v_cvt_pk_f16_f32 v30, v58, v59
	ds_write_b16 v234, v30 offset:6080
	ds_write_b16_d16_hi v235, v30 offset:6080
	ds_write_b16 v236, v31 offset:6080
	ds_write_b16_d16_hi v237, v31 offset:6080
	ds_read_b128 v[30:33], v151 offset:1600
	ds_read_b128 v[50:53], v151 offset:2208
	s_waitcnt lgkmcnt(1)
	v_mfma_f32_16x16x32_f16 v[58:61], v[34:37], v[30:33], v[206:209]
	v_mfma_f32_16x16x32_f16 v[130:133], v[18:21], v[30:33], v[130:133]
	s_waitcnt lgkmcnt(0)
	v_mfma_f32_16x16x32_f16 v[134:137], v[34:37], v[50:53], v[134:137]
	v_mfma_f32_16x16x32_f16 v[138:141], v[18:21], v[50:53], v[138:141]
	ds_read_b128 v[30:33], v151 offset:2816
	ds_read_b128 v[50:53], v151 offset:3424
	s_waitcnt lgkmcnt(1)
	v_mfma_f32_16x16x32_f16 v[206:209], v[34:37], v[30:33], v[118:121]
	v_mfma_f32_16x16x32_f16 v[126:129], v[18:21], v[30:33], v[126:129]
	s_waitcnt lgkmcnt(0)
	v_mfma_f32_16x16x32_f16 v[146:149], v[34:37], v[50:53], v[146:149]
	v_mfma_f32_16x16x32_f16 v[210:213], v[18:21], v[50:53], v[210:213]
	v_add_u32_e32 v30, 0xf6ec0, v244
	v_min_u32_e32 v30, v30, v157
	global_load_dwordx4 v[82:85], v30, s[8:9] nt
	s_waitcnt vmcnt(21)
	v_cvt_pk_f16_f32 v31, v64, v65
	v_cvt_pk_f16_f32 v30, v62, v63
	ds_write_b16 v238, v30 offset:6688
	ds_write_b16_d16_hi v239, v30 offset:6688
	ds_write_b16 v240, v31 offset:6688
	ds_write_b16_d16_hi v241, v31 offset:6688
	ds_read_b128 v[30:33], v151 offset:4032
	ds_read_b128 v[50:53], v151 offset:4640
	s_waitcnt lgkmcnt(1)
	v_mfma_f32_16x16x32_f16 v[62:65], v[34:37], v[30:33], v[214:217]
	v_mfma_f32_16x16x32_f16 v[142:145], v[18:21], v[30:33], v[142:145]
	s_waitcnt lgkmcnt(0)
	v_mfma_f32_16x16x32_f16 v[166:169], v[34:37], v[50:53], v[166:169]
	v_mfma_f32_16x16x32_f16 v[162:165], v[18:21], v[50:53], v[162:165]
	ds_read_b128 v[30:33], v151 offset:5248
	ds_read_b128 v[50:53], v151 offset:5856
	s_waitcnt lgkmcnt(1)
	v_mfma_f32_16x16x32_f16 v[214:217], v[34:37], v[30:33], v[122:125]
	v_mfma_f32_16x16x32_f16 v[170:173], v[18:21], v[30:33], v[170:173]
	s_waitcnt lgkmcnt(0)
	v_mfma_f32_16x16x32_f16 v[174:177], v[34:37], v[50:53], v[174:177]
	v_mfma_f32_16x16x32_f16 v[178:181], v[18:21], v[50:53], v[178:181]
	v_add_u32_e32 v30, 0x10d500, v150
	v_min_u32_e32 v30, v30, v157
	v_cndmask_b32_e64 v30, 0, v30, s[0:1]
	global_load_dwordx4 v[118:121], v30, s[8:9] nt
	s_waitcnt vmcnt(21)
	v_cvt_pk_f16_f32 v31, v88, v89
	v_cvt_pk_f16_f32 v30, v86, v87
	ds_write_b16 v234, v30 offset:7296
	ds_write_b16_d16_hi v235, v30 offset:7296
	ds_write_b16 v236, v31 offset:7296
	ds_write_b16_d16_hi v237, v31 offset:7296
	ds_read_b128 v[30:33], v151 offset:6464
	ds_read_b128 v[50:53], v151 offset:7072
	ds_read_b128 v[122:125], v151 offset:7680
	s_mov_b32 s2, 0x50000
	s_waitcnt lgkmcnt(0)
	v_mfma_f32_16x16x32_f16 v[86:89], v[34:37], v[30:33], v[186:189]
	s_barrier
	v_sub_u32_e32 v245, v234, v243
	v_add_u32_e32 v246, 0xfffffdc0, v245
	v_min_u32_e32 v245, v245, v246
	v_add_u32_e32 v234, v242, v245
	v_sub_u32_e32 v245, v235, v243
	v_add_u32_e32 v246, 0xfffffdc0, v245
	v_min_u32_e32 v245, v245, v246
	v_add_u32_e32 v235, v242, v245
	v_sub_u32_e32 v245, v236, v243
	v_add_u32_e32 v246, 0xfffffdc0, v245
	v_min_u32_e32 v245, v245, v246
	v_add_u32_e32 v236, v242, v245
	v_sub_u32_e32 v245, v237, v243
	v_add_u32_e32 v246, 0xfffffdc0, v245
	v_min_u32_e32 v245, v245, v246
	v_add_u32_e32 v237, v242, v245
	v_sub_u32_e32 v245, v238, v243
	v_add_u32_e32 v246, 0xfffffdc0, v245
	v_min_u32_e32 v245, v245, v246
	v_add_u32_e32 v238, v242, v245
	v_sub_u32_e32 v245, v239, v243
	v_add_u32_e32 v246, 0xfffffdc0, v245
	v_min_u32_e32 v245, v245, v246
	v_add_u32_e32 v239, v242, v245
	v_sub_u32_e32 v245, v240, v243
	v_add_u32_e32 v246, 0xfffffdc0, v245
	v_min_u32_e32 v245, v245, v246
	v_add_u32_e32 v240, v242, v245
	v_sub_u32_e32 v245, v241, v243
	v_add_u32_e32 v246, 0xfffffdc0, v245
	v_min_u32_e32 v245, v245, v246
	v_add_u32_e32 v241, v242, v245
	v_mfma_f32_16x16x32_f16 v[158:161], v[18:21], v[30:33], v[158:161]
	v_add_co_u32_e32 v30, vcc, s2, v152
	s_mov_b32 s2, 0x54000
	s_nop 0
	v_addc_co_u32_e32 v31, vcc, 0, v153, vcc
	v_mfma_f32_16x16x32_f16 v[186:189], v[34:37], v[50:53], v[194:197]
	v_mfma_f32_16x16x32_f16 v[34:37], v[34:37], v[122:125], v[10:13]
	s_nop 2
	v_add_co_u32_e32 v10, vcc, s2, v152
	v_mfma_f32_16x16x32_f16 v[194:197], v[18:21], v[50:53], v[202:205]
	s_nop 0
	v_addc_co_u32_e32 v11, vcc, 0, v153, vcc
	global_load_dwordx4 v[50:53], v[30:31], off sc1
	global_load_dwordx4 v[54:57], v[30:31], off offset:256 sc1
	s_nop 0
	global_load_dwordx4 v[30:33], v[10:11], off sc1
	s_nop 0
	global_load_dwordx4 v[10:13], v[10:11], off offset:256 sc1
	v_mfma_f32_16x16x32_f16 v[182:185], v[18:21], v[122:125], v[182:185]
	v_add_u32_e32 v157, 0x111520dc, v154
	ds_read_b128 v[18:21], v151 offset:448
	v_add_u32_e32 v122, 0xc00, v150
	s_waitcnt vmcnt(24) lgkmcnt(0)
	v_mfma_f32_16x16x32_f16 v[202:205], v[42:45], v[18:21], v[218:221]
	s_waitcnt vmcnt(23)
	v_mfma_f32_16x16x32_f16 v[190:193], v[46:49], v[18:21], v[190:193]
	v_min_u32_e32 v18, v122, v157
	global_load_dwordx4 v[18:21], v18, s[8:9] nt
	s_waitcnt vmcnt(21)
	v_cvt_pk_f16_f32 v17, v16, v17
	v_cvt_pk_f16_f32 v16, v14, v15
	ds_write_b16 v234, v16 offset:0
	ds_write_b16_d16_hi v235, v16 offset:0
	ds_write_b16 v236, v17 offset:0
	ds_write_b16_d16_hi v237, v17 offset:0
	ds_read_b128 v[14:17], v151 offset:1056
	ds_read_b128 v[122:125], v151 offset:1664
	s_waitcnt lgkmcnt(1)
	v_mfma_f32_16x16x32_f16 v[198:201], v[42:45], v[14:17], v[198:201]
	s_waitcnt lgkmcnt(0)
	v_mfma_f32_16x16x32_f16 v[58:61], v[42:45], v[122:125], v[58:61]
	v_mfma_f32_16x16x32_f16 v[218:221], v[46:49], v[122:125], v[130:133]
	ds_read_b128 v[122:125], v151 offset:2272
	s_nop 1
	ds_read_b128 v[130:133], v151 offset:2880
	v_mfma_f32_16x16x32_f16 v[14:17], v[46:49], v[14:17], v[222:225]
	s_waitcnt lgkmcnt(1)
	v_mfma_f32_16x16x32_f16 v[134:137], v[42:45], v[122:125], v[134:137]
	v_mfma_f32_16x16x32_f16 v[138:141], v[46:49], v[122:125], v[138:141]
	s_waitcnt lgkmcnt(0)
	v_mfma_f32_16x16x32_f16 v[206:209], v[42:45], v[130:133], v[206:209]
	v_mfma_f32_16x16x32_f16 v[222:225], v[46:49], v[130:133], v[126:129]
	v_add_u32_e32 v122, 0x17240, v244
	v_min_u32_e32 v122, v122, v157
	global_load_dwordx4 v[122:125], v122, s[8:9] nt
	s_waitcnt vmcnt(21)
	v_cvt_pk_f16_f32 v93, v92, v93
	v_cvt_pk_f16_f32 v92, v90, v91
	ds_write_b16 v238, v92 offset:608
	ds_write_b16_d16_hi v239, v92 offset:608
	ds_write_b16 v240, v93 offset:608
	ds_write_b16_d16_hi v241, v93 offset:608
	ds_read_b128 v[90:93], v151 offset:3488
	ds_read_b128 v[126:129], v151 offset:5312
	s_waitcnt lgkmcnt(1)
	v_mfma_f32_16x16x32_f16 v[146:149], v[42:45], v[90:93], v[146:149]
	v_mfma_f32_16x16x32_f16 v[90:93], v[46:49], v[90:93], v[210:213]
	ds_read_b128 v[130:133], v151 offset:4096
	s_nop 1
	ds_read_b128 v[210:213], v151 offset:4704
	s_waitcnt lgkmcnt(1)
	v_mfma_f32_16x16x32_f16 v[62:65], v[42:45], v[130:133], v[62:65]
	v_mfma_f32_16x16x32_f16 v[142:145], v[46:49], v[130:133], v[142:145]
	s_waitcnt lgkmcnt(0)
	v_mfma_f32_16x16x32_f16 v[166:169], v[42:45], v[210:213], v[166:169]
	v_mfma_f32_16x16x32_f16 v[162:165], v[46:49], v[210:213], v[162:165]
	v_mfma_f32_16x16x32_f16 v[210:213], v[42:45], v[126:129], v[214:217]
	v_mfma_f32_16x16x32_f16 v[170:173], v[46:49], v[126:129], v[170:173]
	v_add_u32_e32 v126, 0x2d880, v150
	v_min_u32_e32 v126, v126, v157
	global_load_dwordx4 v[126:129], v126, s[8:9] nt
	s_waitcnt vmcnt(21)
	v_cvt_pk_f16_f32 v97, v96, v97
	v_cvt_pk_f16_f32 v96, v94, v95
	ds_write_b16 v234, v96 offset:1216
	ds_write_b16_d16_hi v235, v96 offset:1216
	ds_write_b16 v236, v97 offset:1216
	ds_write_b16_d16_hi v237, v97 offset:1216
	ds_read_b128 v[94:97], v151 offset:5920
	ds_read_b128 v[130:133], v151 offset:6528
	s_waitcnt lgkmcnt(1)
	v_mfma_f32_16x16x32_f16 v[174:177], v[42:45], v[94:97], v[174:177]
	v_mfma_f32_16x16x32_f16 v[94:97], v[46:49], v[94:97], v[178:181]
	s_waitcnt lgkmcnt(0)
	v_mfma_f32_16x16x32_f16 v[86:89], v[42:45], v[130:133], v[86:89]
	v_mfma_f32_16x16x32_f16 v[158:161], v[46:49], v[130:133], v[158:161]
	ds_read_b128 v[130:133], v151 offset:7136
	ds_read_b128 v[178:181], v151 offset:7744
	s_waitcnt lgkmcnt(1)
	v_mfma_f32_16x16x32_f16 v[186:189], v[42:45], v[130:133], v[186:189]
	v_mfma_f32_16x16x32_f16 v[194:197], v[46:49], v[130:133], v[194:197]
	s_waitcnt lgkmcnt(0)
	v_mfma_f32_16x16x32_f16 v[34:37], v[42:45], v[178:181], v[34:37]
	v_mfma_f32_16x16x32_f16 v[42:45], v[46:49], v[178:181], v[182:185]
	v_add_u32_e32 v46, 0x43ec0, v244
	v_min_u32_e32 v46, v46, v157
	global_load_dwordx4 v[130:133], v46, s[8:9] nt
	s_waitcnt vmcnt(21)
	v_cvt_pk_f16_f32 v47, v100, v101
	v_cvt_pk_f16_f32 v46, v98, v99
	ds_write_b16 v238, v46 offset:1824
	ds_write_b16_d16_hi v239, v46 offset:1824
	ds_write_b16 v240, v47 offset:1824
	ds_write_b16_d16_hi v241, v47 offset:1824
	ds_read_b128 v[46:49], v151 offset:512
	ds_read_b128 v[98:101], v151 offset:1120
	s_waitcnt lgkmcnt(1)
	v_mfma_f32_16x16x32_f16 v[178:181], v[26:29], v[46:49], v[202:205]
	v_mfma_f32_16x16x32_f16 v[46:49], v[6:9], v[46:49], v[190:193]
	s_waitcnt lgkmcnt(0)
	v_mfma_f32_16x16x32_f16 v[182:185], v[26:29], v[98:101], v[198:201]
	v_mfma_f32_16x16x32_f16 v[98:101], v[6:9], v[98:101], v[14:17]
	s_nop 2
	ds_read_b128 v[14:17], v151 offset:1728
	ds_read_b128 v[190:193], v151 offset:2336
	s_waitcnt lgkmcnt(1)
	v_mfma_f32_16x16x32_f16 v[198:201], v[26:29], v[14:17], v[58:61]
	v_mfma_f32_16x16x32_f16 v[202:205], v[6:9], v[14:17], v[218:221]
	s_waitcnt lgkmcnt(0)
	v_mfma_f32_16x16x32_f16 v[214:217], v[26:29], v[190:193], v[134:137]
	v_mfma_f32_16x16x32_f16 v[190:193], v[6:9], v[190:193], v[138:141]
	v_add_u32_e32 v14, 0x5a500, v150
	v_min_u32_e32 v14, v14, v157
	global_load_dwordx4 v[134:137], v14, s[8:9] nt
	s_waitcnt vmcnt(21)
	v_cvt_pk_f16_f32 v15, v104, v105
	v_cvt_pk_f16_f32 v14, v102, v103
	ds_write_b16 v234, v14 offset:2432
	ds_write_b16_d16_hi v235, v14 offset:2432
	ds_write_b16 v236, v15 offset:2432
	ds_write_b16_d16_hi v237, v15 offset:2432
	ds_read_b128 v[14:17], v151 offset:2944
	ds_read_b128 v[58:61], v151 offset:3552
	s_waitcnt lgkmcnt(1)
	v_mfma_f32_16x16x32_f16 v[102:105], v[26:29], v[14:17], v[206:209]
	v_mfma_f32_16x16x32_f16 v[206:209], v[6:9], v[14:17], v[222:225]
	s_waitcnt lgkmcnt(0)
	v_mfma_f32_16x16x32_f16 v[218:221], v[26:29], v[58:61], v[146:149]
	v_mfma_f32_16x16x32_f16 v[90:93], v[6:9], v[58:61], v[90:93]
	ds_read_b128 v[14:17], v151 offset:4160
	ds_read_b128 v[58:61], v151 offset:4768
	s_waitcnt lgkmcnt(1)
	v_mfma_f32_16x16x32_f16 v[222:225], v[26:29], v[14:17], v[62:65]
	v_mfma_f32_16x16x32_f16 v[226:229], v[6:9], v[14:17], v[142:145]
	s_waitcnt lgkmcnt(0)
	v_mfma_f32_16x16x32_f16 v[166:169], v[26:29], v[58:61], v[166:169]
	v_mfma_f32_16x16x32_f16 v[162:165], v[6:9], v[58:61], v[162:165]
	v_add_u32_e32 v14, 0x70b40, v244
	v_min_u32_e32 v14, v14, v157
	global_load_dwordx4 v[138:141], v14, s[8:9] nt
	s_waitcnt vmcnt(21)
	v_cvt_pk_f16_f32 v15, v108, v109
	v_cvt_pk_f16_f32 v14, v106, v107
	ds_write_b16 v238, v14 offset:3040
	ds_write_b16_d16_hi v239, v14 offset:3040
	ds_write_b16 v240, v15 offset:3040
	ds_write_b16_d16_hi v241, v15 offset:3040
	ds_read_b128 v[14:17], v151 offset:5376
	ds_read_b128 v[58:61], v151 offset:5984
	s_waitcnt lgkmcnt(1)
	v_mfma_f32_16x16x32_f16 v[106:109], v[26:29], v[14:17], v[210:213]
	v_mfma_f32_16x16x32_f16 v[170:173], v[6:9], v[14:17], v[170:173]
	s_waitcnt lgkmcnt(0)
	v_mfma_f32_16x16x32_f16 v[174:177], v[26:29], v[58:61], v[174:177]
	v_mfma_f32_16x16x32_f16 v[94:97], v[6:9], v[58:61], v[94:97]
	ds_read_b128 v[14:17], v151 offset:6592
	ds_read_b128 v[58:61], v151 offset:7200
	s_waitcnt lgkmcnt(1)
	v_mfma_f32_16x16x32_f16 v[86:89], v[26:29], v[14:17], v[86:89]
	v_mfma_f32_16x16x32_f16 v[158:161], v[6:9], v[14:17], v[158:161]
	s_waitcnt lgkmcnt(0)
	v_mfma_f32_16x16x32_f16 v[186:189], v[26:29], v[58:61], v[186:189]
	v_mfma_f32_16x16x32_f16 v[194:197], v[6:9], v[58:61], v[194:197]
	v_add_u32_e32 v14, 0x87180, v150
	v_min_u32_e32 v14, v14, v157
	global_load_dwordx4 v[142:145], v14, s[8:9] nt
	s_waitcnt vmcnt(21)
	v_cvt_pk_f16_f32 v15, v112, v113
	v_cvt_pk_f16_f32 v14, v110, v111
	ds_write_b16 v234, v14 offset:3648
	ds_write_b16_d16_hi v235, v14 offset:3648
	ds_write_b16 v236, v15 offset:3648
	ds_write_b16_d16_hi v237, v15 offset:3648
	ds_read_b128 v[110:113], v151 offset:7808
	s_mov_b32 s2, 0x58000
	v_add_co_u32_e32 v14, vcc, s2, v152
	s_mov_b32 s2, 0x5c000
	s_nop 0
	v_addc_co_u32_e32 v15, vcc, 0, v153, vcc
	global_load_dwordx4 v[58:61], v[14:15], off sc1
	global_load_dwordx4 v[62:65], v[14:15], off offset:256 sc1
	v_add_co_u32_e32 v14, vcc, s2, v152
	s_waitcnt lgkmcnt(0)
	v_mfma_f32_16x16x32_f16 v[26:29], v[26:29], v[110:113], v[34:37]
	v_addc_co_u32_e32 v15, vcc, 0, v153, vcc
	s_nop 1
	global_load_dwordx4 v[34:37], v[14:15], off sc1
	s_nop 0
	global_load_dwordx4 v[14:17], v[14:15], off offset:256 sc1
	v_mfma_f32_16x16x32_f16 v[42:45], v[6:9], v[110:113], v[42:45]
	ds_read_b128 v[6:9], v151 offset:0
	ds_read_b128 v[110:113], v151 offset:608
	s_waitcnt vmcnt(24) lgkmcnt(1)
	v_mfma_f32_16x16x32_f16 v[178:181], v[70:73], v[6:9], v[178:181]
	s_waitcnt vmcnt(23)
	v_mfma_f32_16x16x32_f16 v[46:49], v[74:77], v[6:9], v[46:49]
	ds_read_b128 v[6:9], v151 offset:1216
	s_waitcnt lgkmcnt(1)
	v_mfma_f32_16x16x32_f16 v[182:185], v[70:73], v[110:113], v[182:185]
	v_mfma_f32_16x16x32_f16 v[98:101], v[74:77], v[110:113], v[98:101]
	s_waitcnt lgkmcnt(0)
	v_mfma_f32_16x16x32_f16 v[198:201], v[70:73], v[6:9], v[198:201]
	v_mfma_f32_16x16x32_f16 v[202:205], v[74:77], v[6:9], v[202:205]
	v_add_u32_e32 v6, 0x9d7c0, v244
	v_min_u32_e32 v6, v6, v157
	global_load_dwordx4 v[146:149], v6, s[8:9] nt
	s_waitcnt vmcnt(21)
	v_cvt_pk_f16_f32 v5, v4, v5
	v_cvt_pk_f16_f32 v4, v2, v3
	ds_write_b16 v238, v4 offset:4256
	ds_write_b16_d16_hi v239, v4 offset:4256
	ds_write_b16 v240, v5 offset:4256
	ds_write_b16_d16_hi v241, v5 offset:4256
	ds_read_b128 v[2:5], v151 offset:1824
	ds_read_b128 v[6:9], v151 offset:2432
	s_waitcnt lgkmcnt(1)
	v_mfma_f32_16x16x32_f16 v[210:213], v[70:73], v[2:5], v[214:217]
	v_mfma_f32_16x16x32_f16 v[2:5], v[74:77], v[2:5], v[190:193]
	s_waitcnt lgkmcnt(0)
	v_mfma_f32_16x16x32_f16 v[102:105], v[70:73], v[6:9], v[102:105]
	v_mfma_f32_16x16x32_f16 v[190:193], v[74:77], v[6:9], v[206:209]
	ds_read_b128 v[6:9], v151 offset:3040
	ds_read_b128 v[110:113], v151 offset:3648
	s_waitcnt lgkmcnt(1)
	v_mfma_f32_16x16x32_f16 v[206:209], v[70:73], v[6:9], v[218:221]
	v_mfma_f32_16x16x32_f16 v[90:93], v[74:77], v[6:9], v[90:93]
	s_waitcnt lgkmcnt(0)
	v_mfma_f32_16x16x32_f16 v[214:217], v[70:73], v[110:113], v[222:225]
	v_mfma_f32_16x16x32_f16 v[218:221], v[74:77], v[110:113], v[226:229]
	v_add_u32_e32 v6, 0xb3e00, v150
	v_min_u32_e32 v6, v6, v157
	global_load_dwordx4 v[110:113], v6, s[8:9] nt
	s_waitcnt vmcnt(21)
	v_cvt_pk_f16_f32 v7, v116, v117
	v_cvt_pk_f16_f32 v6, v114, v115
	ds_write_b16 v234, v6 offset:4864
	ds_write_b16_d16_hi v235, v6 offset:4864
	ds_write_b16 v236, v7 offset:4864
	ds_write_b16_d16_hi v237, v7 offset:4864
	ds_read_b128 v[6:9], v151 offset:4256
	ds_read_b128 v[114:117], v151 offset:6080
	s_waitcnt lgkmcnt(1)
	v_mfma_f32_16x16x32_f16 v[166:169], v[70:73], v[6:9], v[166:169]
	v_mfma_f32_16x16x32_f16 v[162:165], v[74:77], v[6:9], v[162:165]
	ds_read_b128 v[6:9], v151 offset:4864
	ds_read_b128 v[222:225], v151 offset:5472
	s_waitcnt lgkmcnt(2)
	v_mfma_f32_16x16x32_f16 v[86:89], v[70:73], v[114:117], v[86:89]
	v_mfma_f32_16x16x32_f16 v[114:117], v[74:77], v[114:117], v[158:161]
	s_waitcnt lgkmcnt(1)
	v_mfma_f32_16x16x32_f16 v[106:109], v[70:73], v[6:9], v[106:109]
	v_mfma_f32_16x16x32_f16 v[170:173], v[74:77], v[6:9], v[170:173]
	s_waitcnt lgkmcnt(0)
	v_mfma_f32_16x16x32_f16 v[174:177], v[70:73], v[222:225], v[174:177]
	v_mfma_f32_16x16x32_f16 v[94:97], v[74:77], v[222:225], v[94:97]
	v_add_u32_e32 v6, 0xca440, v244
	v_min_u32_e32 v6, v6, v157
	global_load_dwordx4 v[6:9], v6, s[8:9] nt
	s_waitcnt vmcnt(21)
	v_cvt_pk_f16_f32 v81, v80, v81
	v_cvt_pk_f16_f32 v80, v78, v79
	ds_write_b16 v238, v80 offset:5472
	ds_write_b16_d16_hi v239, v80 offset:5472
	ds_write_b16 v240, v81 offset:5472
	ds_write_b16_d16_hi v241, v81 offset:5472
	ds_read_b128 v[78:81], v151 offset:6688
	ds_read_b128 v[158:161], v151 offset:7296
	s_waitcnt lgkmcnt(1)
	v_mfma_f32_16x16x32_f16 v[186:189], v[70:73], v[78:81], v[186:189]
	s_waitcnt lgkmcnt(0)
	v_mfma_f32_16x16x32_f16 v[26:29], v[70:73], v[158:161], v[26:29]
	v_mfma_f32_16x16x32_f16 v[158:161], v[74:77], v[158:161], v[42:45]
	s_nop 2
	ds_read_b128 v[42:45], v151 offset:64
	ds_read_b128 v[70:73], v151 offset:672
	v_mfma_f32_16x16x32_f16 v[194:197], v[74:77], v[78:81], v[194:197]
	s_waitcnt lgkmcnt(1)
	v_mfma_f32_16x16x32_f16 v[178:181], v[38:41], v[42:45], v[178:181]
	v_mfma_f32_16x16x32_f16 v[222:225], v[22:25], v[42:45], v[46:49]
	s_waitcnt lgkmcnt(0)
	v_mfma_f32_16x16x32_f16 v[182:185], v[38:41], v[70:73], v[182:185]
	v_mfma_f32_16x16x32_f16 v[98:101], v[22:25], v[70:73], v[98:101]
	v_add_u32_e32 v42, 0xe0a80, v150
	v_min_u32_e32 v42, v42, v157
	global_load_dwordx4 v[70:73], v42, s[8:9] nt
	s_waitcnt vmcnt(21)
	v_cvt_pk_f16_f32 v43, v68, v69
	v_cvt_pk_f16_f32 v42, v66, v67
	ds_write_b16 v234, v42 offset:6080
	ds_write_b16_d16_hi v235, v42 offset:6080
	ds_write_b16 v236, v43 offset:6080
	ds_write_b16_d16_hi v237, v43 offset:6080
	ds_read_b128 v[42:45], v151 offset:1280
	ds_read_b128 v[46:49], v151 offset:1888
	s_waitcnt lgkmcnt(1)
	v_mfma_f32_16x16x32_f16 v[66:69], v[38:41], v[42:45], v[198:201]
	v_mfma_f32_16x16x32_f16 v[198:201], v[22:25], v[42:45], v[202:205]
	s_waitcnt lgkmcnt(0)
	v_mfma_f32_16x16x32_f16 v[202:205], v[38:41], v[46:49], v[210:213]
	v_mfma_f32_16x16x32_f16 v[210:213], v[22:25], v[46:49], v[2:5]
	s_nop 2
	ds_read_b128 v[2:5], v151 offset:2496
	ds_read_b128 v[42:45], v151 offset:3104
	s_waitcnt lgkmcnt(1)
	v_mfma_f32_16x16x32_f16 v[102:105], v[38:41], v[2:5], v[102:105]
	v_mfma_f32_16x16x32_f16 v[190:193], v[22:25], v[2:5], v[190:193]
	s_waitcnt lgkmcnt(0)
	v_mfma_f32_16x16x32_f16 v[206:209], v[38:41], v[42:45], v[206:209]
	v_mfma_f32_16x16x32_f16 v[90:93], v[22:25], v[42:45], v[90:93]
	v_add_u32_e32 v2, 0xf70c0, v244
	v_min_u32_e32 v2, v2, v157
	global_load_dwordx4 v[74:77], v2, s[8:9] nt
	s_waitcnt vmcnt(21)
	v_cvt_pk_f16_f32 v3, v84, v85
	v_cvt_pk_f16_f32 v2, v82, v83
	ds_write_b16 v238, v2 offset:6688
	ds_write_b16_d16_hi v239, v2 offset:6688
	ds_write_b16 v240, v3 offset:6688
	ds_write_b16_d16_hi v241, v3 offset:6688
	ds_read_b128 v[2:5], v151 offset:3712
	ds_read_b128 v[42:45], v151 offset:4320
	s_waitcnt lgkmcnt(1)
	v_mfma_f32_16x16x32_f16 v[214:217], v[38:41], v[2:5], v[214:217]
	v_mfma_f32_16x16x32_f16 v[218:221], v[22:25], v[2:5], v[218:221]
	s_waitcnt lgkmcnt(0)
	v_mfma_f32_16x16x32_f16 v[166:169], v[38:41], v[42:45], v[166:169]
	v_mfma_f32_16x16x32_f16 v[162:165], v[22:25], v[42:45], v[162:165]
	ds_read_b128 v[2:5], v151 offset:4928
	ds_read_b128 v[42:45], v151 offset:5536
	s_waitcnt lgkmcnt(1)
	v_mfma_f32_16x16x32_f16 v[106:109], v[38:41], v[2:5], v[106:109]
	v_mfma_f32_16x16x32_f16 v[170:173], v[22:25], v[2:5], v[170:173]
	s_waitcnt lgkmcnt(0)
	v_mfma_f32_16x16x32_f16 v[174:177], v[38:41], v[42:45], v[174:177]
	v_mfma_f32_16x16x32_f16 v[94:97], v[22:25], v[42:45], v[94:97]
	v_add_u32_e32 v2, 0x10d700, v150
	v_min_u32_e32 v2, v2, v157
	v_cndmask_b32_e64 v2, 0, v2, s[0:1]
	global_load_dwordx4 v[78:81], v2, s[8:9] nt
	s_waitcnt vmcnt(21)
	v_cvt_pk_f16_f32 v3, v120, v121
	v_cvt_pk_f16_f32 v2, v118, v119
	ds_write_b16 v234, v2 offset:7296
	ds_write_b16_d16_hi v235, v2 offset:7296
	ds_write_b16 v236, v3 offset:7296
	ds_write_b16_d16_hi v237, v3 offset:7296
	ds_read_b128 v[2:5], v151 offset:6144
	ds_read_b128 v[42:45], v151 offset:6752
	ds_read_b128 v[82:85], v151 offset:7360
	s_mov_b32 s2, 0x60000
	s_waitcnt lgkmcnt(0)
	v_mfma_f32_16x16x32_f16 v[118:121], v[38:41], v[2:5], v[86:89]
	s_barrier
	v_sub_u32_e32 v245, v234, v243
	v_add_u32_e32 v246, 0xfffffdc0, v245
	v_min_u32_e32 v245, v245, v246
	v_add_u32_e32 v234, v242, v245
	v_sub_u32_e32 v245, v235, v243
	v_add_u32_e32 v246, 0xfffffdc0, v245
	v_min_u32_e32 v245, v245, v246
	v_add_u32_e32 v235, v242, v245
	v_sub_u32_e32 v245, v236, v243
	v_add_u32_e32 v246, 0xfffffdc0, v245
	v_min_u32_e32 v245, v245, v246
	v_add_u32_e32 v236, v242, v245
	v_sub_u32_e32 v245, v237, v243
	v_add_u32_e32 v246, 0xfffffdc0, v245
	v_min_u32_e32 v245, v245, v246
	v_add_u32_e32 v237, v242, v245
	v_sub_u32_e32 v245, v238, v243
	v_add_u32_e32 v246, 0xfffffdc0, v245
	v_min_u32_e32 v245, v245, v246
	v_add_u32_e32 v238, v242, v245
	v_sub_u32_e32 v245, v239, v243
	v_add_u32_e32 v246, 0xfffffdc0, v245
	v_min_u32_e32 v245, v245, v246
	v_add_u32_e32 v239, v242, v245
	v_sub_u32_e32 v245, v240, v243
	v_add_u32_e32 v246, 0xfffffdc0, v245
	v_min_u32_e32 v245, v245, v246
	v_add_u32_e32 v240, v242, v245
	v_sub_u32_e32 v245, v241, v243
	v_add_u32_e32 v246, 0xfffffdc0, v245
	v_min_u32_e32 v245, v245, v246
	v_add_u32_e32 v241, v242, v245
	v_mfma_f32_16x16x32_f16 v[114:117], v[22:25], v[2:5], v[114:117]
	v_add_co_u32_e32 v2, vcc, s2, v152
	s_mov_b32 s2, 0x64000
	s_nop 0
	v_addc_co_u32_e32 v3, vcc, 0, v153, vcc
	v_mfma_f32_16x16x32_f16 v[186:189], v[38:41], v[42:45], v[186:189]
	v_mfma_f32_16x16x32_f16 v[194:197], v[22:25], v[42:45], v[194:197]
	global_load_dwordx4 v[42:45], v[2:3], off sc1
	global_load_dwordx4 v[46:49], v[2:3], off offset:256 sc1
	v_add_co_u32_e32 v2, vcc, s2, v152
	v_mfma_f32_16x16x32_f16 v[38:41], v[38:41], v[82:85], v[26:29]
	s_nop 0
	v_addc_co_u32_e32 v3, vcc, 0, v153, vcc
	s_nop 0
	global_load_dwordx4 v[26:29], v[2:3], off sc1
	s_nop 0
	global_load_dwordx4 v[2:5], v[2:3], off offset:256 sc1
	v_mfma_f32_16x16x32_f16 v[22:25], v[22:25], v[82:85], v[158:161]
	v_add_u32_e32 v157, 0x111522dc, v154
	ds_read_b128 v[82:85], v151 offset:128
	v_add_u32_e32 v86, 0xe00, v150
	s_waitcnt vmcnt(24) lgkmcnt(0)
	v_mfma_f32_16x16x32_f16 v[158:161], v[50:53], v[82:85], v[178:181]
	s_waitcnt vmcnt(23)
	v_mfma_f32_16x16x32_f16 v[178:181], v[54:57], v[82:85], v[222:225]
	v_min_u32_e32 v82, v86, v157
	global_load_dwordx4 v[82:85], v82, s[8:9] nt
	s_waitcnt vmcnt(21)
	v_cvt_pk_f16_f32 v21, v20, v21
	v_cvt_pk_f16_f32 v20, v18, v19
	ds_write_b16 v234, v20 offset:0
	ds_write_b16_d16_hi v235, v20 offset:0
	ds_write_b16 v236, v21 offset:0
	ds_write_b16_d16_hi v237, v21 offset:0
	ds_read_b128 v[18:21], v151 offset:736
	ds_read_b128 v[86:89], v151 offset:1344
	s_waitcnt lgkmcnt(1)
	v_mfma_f32_16x16x32_f16 v[182:185], v[50:53], v[18:21], v[182:185]
	v_mfma_f32_16x16x32_f16 v[18:21], v[54:57], v[18:21], v[98:101]
	s_waitcnt lgkmcnt(0)
	v_mfma_f32_16x16x32_f16 v[66:69], v[50:53], v[86:89], v[66:69]
	v_mfma_f32_16x16x32_f16 v[98:101], v[54:57], v[86:89], v[198:201]
	ds_read_b128 v[86:89], v151 offset:1952
	s_nop 1
	ds_read_b128 v[198:201], v151 offset:2560
	s_waitcnt lgkmcnt(1)
	v_mfma_f32_16x16x32_f16 v[202:205], v[50:53], v[86:89], v[202:205]
	v_mfma_f32_16x16x32_f16 v[210:213], v[54:57], v[86:89], v[210:213]
	s_waitcnt lgkmcnt(0)
	v_mfma_f32_16x16x32_f16 v[102:105], v[50:53], v[198:201], v[102:105]
	v_mfma_f32_16x16x32_f16 v[190:193], v[54:57], v[198:201], v[190:193]
	v_add_u32_e32 v86, 0x17440, v244
	v_min_u32_e32 v86, v86, v157
	global_load_dwordx4 v[86:89], v86, s[8:9] nt
	s_waitcnt vmcnt(21)
	v_cvt_pk_f16_f32 v125, v124, v125
	v_cvt_pk_f16_f32 v124, v122, v123
	ds_write_b16 v238, v124 offset:608
	ds_write_b16_d16_hi v239, v124 offset:608
	ds_write_b16 v240, v125 offset:608
	ds_write_b16_d16_hi v241, v125 offset:608
	ds_read_b128 v[122:125], v151 offset:3168
	ds_read_b128 v[198:201], v151 offset:4992
	s_waitcnt lgkmcnt(1)
	v_mfma_f32_16x16x32_f16 v[206:209], v[50:53], v[122:125], v[206:209]
	v_mfma_f32_16x16x32_f16 v[122:125], v[54:57], v[122:125], v[90:93]
	s_nop 2
	ds_read_b128 v[90:93], v151 offset:3776
	ds_read_b128 v[222:225], v151 offset:4384
	s_waitcnt lgkmcnt(1)
	v_mfma_f32_16x16x32_f16 v[214:217], v[50:53], v[90:93], v[214:217]
	v_mfma_f32_16x16x32_f16 v[218:221], v[54:57], v[90:93], v[218:221]
	s_waitcnt lgkmcnt(0)
	v_mfma_f32_16x16x32_f16 v[166:169], v[50:53], v[222:225], v[166:169]
	v_mfma_f32_16x16x32_f16 v[162:165], v[54:57], v[222:225], v[162:165]
	v_mfma_f32_16x16x32_f16 v[106:109], v[50:53], v[198:201], v[106:109]
	v_mfma_f32_16x16x32_f16 v[170:173], v[54:57], v[198:201], v[170:173]
	v_add_u32_e32 v90, 0x2da80, v150
	v_min_u32_e32 v90, v90, v157
	global_load_dwordx4 v[90:93], v90, s[8:9] nt
	s_waitcnt vmcnt(21)
	v_cvt_pk_f16_f32 v129, v128, v129
	v_cvt_pk_f16_f32 v128, v126, v127
	ds_write_b16 v234, v128 offset:1216
	ds_write_b16_d16_hi v235, v128 offset:1216
	ds_write_b16 v236, v129 offset:1216
	ds_write_b16_d16_hi v237, v129 offset:1216
	ds_read_b128 v[126:129], v151 offset:5600
	ds_read_b128 v[198:201], v151 offset:6208
	s_waitcnt lgkmcnt(1)
	v_mfma_f32_16x16x32_f16 v[174:177], v[50:53], v[126:129], v[174:177]
	v_mfma_f32_16x16x32_f16 v[126:129], v[54:57], v[126:129], v[94:97]
	s_waitcnt lgkmcnt(0)
	v_mfma_f32_16x16x32_f16 v[118:121], v[50:53], v[198:201], v[118:121]
	v_mfma_f32_16x16x32_f16 v[114:117], v[54:57], v[198:201], v[114:117]
	ds_read_b128 v[94:97], v151 offset:6816
	ds_read_b128 v[198:201], v151 offset:7424
	s_waitcnt lgkmcnt(1)
	v_mfma_f32_16x16x32_f16 v[186:189], v[50:53], v[94:97], v[186:189]
	v_mfma_f32_16x16x32_f16 v[194:197], v[54:57], v[94:97], v[194:197]
	s_waitcnt lgkmcnt(0)
	v_mfma_f32_16x16x32_f16 v[38:41], v[50:53], v[198:201], v[38:41]
	v_mfma_f32_16x16x32_f16 v[22:25], v[54:57], v[198:201], v[22:25]
	v_add_u32_e32 v50, 0x440c0, v244
	v_min_u32_e32 v50, v50, v157
	global_load_dwordx4 v[94:97], v50, s[8:9] nt
	s_waitcnt vmcnt(21)
	v_cvt_pk_f16_f32 v51, v132, v133
	v_cvt_pk_f16_f32 v50, v130, v131
	ds_write_b16 v238, v50 offset:1824
	ds_write_b16_d16_hi v239, v50 offset:1824
	ds_write_b16 v240, v51 offset:1824
	ds_write_b16_d16_hi v241, v51 offset:1824
	ds_read_b128 v[50:53], v151 offset:192
	ds_read_b128 v[54:57], v151 offset:800
	s_waitcnt lgkmcnt(1)
	v_mfma_f32_16x16x32_f16 v[130:133], v[30:33], v[50:53], v[158:161]
	v_mfma_f32_16x16x32_f16 v[50:53], v[10:13], v[50:53], v[178:181]
	s_waitcnt lgkmcnt(0)
	v_mfma_f32_16x16x32_f16 v[158:161], v[30:33], v[54:57], v[182:185]
	v_mfma_f32_16x16x32_f16 v[178:181], v[10:13], v[54:57], v[18:21]
	s_nop 2
	ds_read_b128 v[18:21], v151 offset:1408
	ds_read_b128 v[54:57], v151 offset:2016
	s_waitcnt lgkmcnt(1)
	v_mfma_f32_16x16x32_f16 v[182:185], v[30:33], v[18:21], v[66:69]
	v_mfma_f32_16x16x32_f16 v[198:201], v[10:13], v[18:21], v[98:101]
	s_waitcnt lgkmcnt(0)
	v_mfma_f32_16x16x32_f16 v[202:205], v[30:33], v[54:57], v[202:205]
	v_mfma_f32_16x16x32_f16 v[210:213], v[10:13], v[54:57], v[210:213]
	v_add_u32_e32 v18, 0x5a700, v150
	v_min_u32_e32 v18, v18, v157
	global_load_dwordx4 v[98:101], v18, s[8:9] nt
	s_waitcnt vmcnt(21)
	v_cvt_pk_f16_f32 v19, v136, v137
	v_cvt_pk_f16_f32 v18, v134, v135
	ds_write_b16 v234, v18 offset:2432
	ds_write_b16_d16_hi v235, v18 offset:2432
	ds_write_b16 v236, v19 offset:2432
	ds_write_b16_d16_hi v237, v19 offset:2432
	ds_read_b128 v[18:21], v151 offset:2624
	ds_read_b128 v[54:57], v151 offset:3232
	s_waitcnt lgkmcnt(1)
	v_mfma_f32_16x16x32_f16 v[134:137], v[30:33], v[18:21], v[102:105]
	v_mfma_f32_16x16x32_f16 v[190:193], v[10:13], v[18:21], v[190:193]
	s_waitcnt lgkmcnt(0)
	v_mfma_f32_16x16x32_f16 v[206:209], v[30:33], v[54:57], v[206:209]
	v_mfma_f32_16x16x32_f16 v[122:125], v[10:13], v[54:57], v[122:125]
	ds_read_b128 v[18:21], v151 offset:3840
	ds_read_b128 v[54:57], v151 offset:4448
	s_waitcnt lgkmcnt(1)
	v_mfma_f32_16x16x32_f16 v[214:217], v[30:33], v[18:21], v[214:217]
	v_mfma_f32_16x16x32_f16 v[218:221], v[10:13], v[18:21], v[218:221]
	s_waitcnt lgkmcnt(0)
	v_mfma_f32_16x16x32_f16 v[166:169], v[30:33], v[54:57], v[166:169]
	v_mfma_f32_16x16x32_f16 v[162:165], v[10:13], v[54:57], v[162:165]
	v_add_u32_e32 v18, 0x70d40, v244
	v_min_u32_e32 v18, v18, v157
	global_load_dwordx4 v[102:105], v18, s[8:9] nt
	s_waitcnt vmcnt(21)
	v_cvt_pk_f16_f32 v19, v140, v141
	v_cvt_pk_f16_f32 v18, v138, v139
	ds_write_b16 v238, v18 offset:3040
	ds_write_b16_d16_hi v239, v18 offset:3040
	ds_write_b16 v240, v19 offset:3040
	ds_write_b16_d16_hi v241, v19 offset:3040
	ds_read_b128 v[18:21], v151 offset:5056
	ds_read_b128 v[54:57], v151 offset:5664
	s_waitcnt lgkmcnt(1)
	v_mfma_f32_16x16x32_f16 v[138:141], v[30:33], v[18:21], v[106:109]
	v_mfma_f32_16x16x32_f16 v[170:173], v[10:13], v[18:21], v[170:173]
	s_waitcnt lgkmcnt(0)
	v_mfma_f32_16x16x32_f16 v[174:177], v[30:33], v[54:57], v[174:177]
	v_mfma_f32_16x16x32_f16 v[126:129], v[10:13], v[54:57], v[126:129]
	ds_read_b128 v[18:21], v151 offset:6272
	ds_read_b128 v[54:57], v151 offset:6880
	s_waitcnt lgkmcnt(1)
	v_mfma_f32_16x16x32_f16 v[118:121], v[30:33], v[18:21], v[118:121]
	v_mfma_f32_16x16x32_f16 v[222:225], v[10:13], v[18:21], v[114:117]
	s_waitcnt lgkmcnt(0)
	v_mfma_f32_16x16x32_f16 v[186:189], v[30:33], v[54:57], v[186:189]
	v_mfma_f32_16x16x32_f16 v[194:197], v[10:13], v[54:57], v[194:197]
	v_add_u32_e32 v18, 0x87380, v150
	v_min_u32_e32 v18, v18, v157
	global_load_dwordx4 v[106:109], v18, s[8:9] nt
	s_waitcnt vmcnt(21)
	v_cvt_pk_f16_f32 v19, v144, v145
	v_cvt_pk_f16_f32 v18, v142, v143
	ds_write_b16 v234, v18 offset:3648
	ds_write_b16_d16_hi v235, v18 offset:3648
	ds_write_b16 v236, v19 offset:3648
	ds_write_b16_d16_hi v237, v19 offset:3648
	ds_read_b128 v[114:117], v151 offset:7488
	s_mov_b32 s2, 0x68000
	v_add_co_u32_e32 v18, vcc, s2, v152
	s_mov_b32 s2, 0x6c000
	s_nop 0
	v_addc_co_u32_e32 v19, vcc, 0, v153, vcc
	global_load_dwordx4 v[54:57], v[18:19], off sc1
	global_load_dwordx4 v[66:69], v[18:19], off offset:256 sc1
	v_add_co_u32_e32 v18, vcc, s2, v152
	s_waitcnt lgkmcnt(0)
	v_mfma_f32_16x16x32_f16 v[38:41], v[30:33], v[114:117], v[38:41]
	v_addc_co_u32_e32 v19, vcc, 0, v153, vcc
	global_load_dwordx4 v[30:33], v[18:19], off sc1
	s_nop 0
	global_load_dwordx4 v[18:21], v[18:19], off offset:256 sc1
	v_mfma_f32_16x16x32_f16 v[22:25], v[10:13], v[114:117], v[22:25]
	ds_read_b128 v[10:13], v151 offset:256
	ds_read_b128 v[114:117], v151 offset:864
	s_waitcnt vmcnt(24) lgkmcnt(1)
	v_mfma_f32_16x16x32_f16 v[130:133], v[58:61], v[10:13], v[130:133]
	s_waitcnt vmcnt(23)
	v_mfma_f32_16x16x32_f16 v[50:53], v[62:65], v[10:13], v[50:53]
	ds_read_b128 v[10:13], v151 offset:1472
	s_waitcnt lgkmcnt(1)
	v_mfma_f32_16x16x32_f16 v[142:145], v[58:61], v[114:117], v[158:161]
	v_mfma_f32_16x16x32_f16 v[158:161], v[62:65], v[114:117], v[178:181]
	s_waitcnt lgkmcnt(0)
	v_mfma_f32_16x16x32_f16 v[178:181], v[58:61], v[10:13], v[182:185]
	v_mfma_f32_16x16x32_f16 v[182:185], v[62:65], v[10:13], v[198:201]
	v_add_u32_e32 v10, 0x9d9c0, v244
	v_min_u32_e32 v10, v10, v157
	global_load_dwordx4 v[10:13], v10, s[8:9] nt
	s_waitcnt vmcnt(21)
	v_cvt_pk_f16_f32 v115, v148, v149
	v_cvt_pk_f16_f32 v114, v146, v147
	ds_write_b16 v238, v114 offset:4256
	ds_write_b16_d16_hi v239, v114 offset:4256
	ds_write_b16 v240, v115 offset:4256
	ds_write_b16_d16_hi v241, v115 offset:4256
	ds_read_b128 v[114:117], v151 offset:2080
	ds_read_b128 v[146:149], v151 offset:2688
	s_waitcnt lgkmcnt(1)
	v_mfma_f32_16x16x32_f16 v[198:201], v[58:61], v[114:117], v[202:205]
	v_mfma_f32_16x16x32_f16 v[202:205], v[62:65], v[114:117], v[210:213]
	s_waitcnt lgkmcnt(0)
	v_mfma_f32_16x16x32_f16 v[134:137], v[58:61], v[146:149], v[134:137]
	v_mfma_f32_16x16x32_f16 v[146:149], v[62:65], v[146:149], v[190:193]
	ds_read_b128 v[114:117], v151 offset:3296
	s_nop 1
	ds_read_b128 v[190:193], v151 offset:3904
	s_waitcnt lgkmcnt(1)
	v_mfma_f32_16x16x32_f16 v[206:209], v[58:61], v[114:117], v[206:209]
	v_mfma_f32_16x16x32_f16 v[122:125], v[62:65], v[114:117], v[122:125]
	s_waitcnt lgkmcnt(0)
	v_mfma_f32_16x16x32_f16 v[210:213], v[58:61], v[190:193], v[214:217]
	v_mfma_f32_16x16x32_f16 v[190:193], v[62:65], v[190:193], v[218:221]
	v_add_u32_e32 v114, 0xb4000, v150
	v_min_u32_e32 v114, v114, v157
	global_load_dwordx4 v[114:117], v114, s[8:9] nt
	s_waitcnt vmcnt(21)
	v_cvt_pk_f16_f32 v113, v112, v113
	v_cvt_pk_f16_f32 v112, v110, v111
	ds_write_b16 v234, v112 offset:4864
	ds_write_b16_d16_hi v235, v112 offset:4864
	ds_write_b16 v236, v113 offset:4864
	ds_write_b16_d16_hi v237, v113 offset:4864
	s_mov_b32 s2, 0xb4000
	ds_read_b128 v[110:113], v151 offset:4512
	ds_read_b128 v[214:217], v151 offset:6336
	s_waitcnt lgkmcnt(1)
	v_mfma_f32_16x16x32_f16 v[166:169], v[58:61], v[110:113], v[166:169]
	v_mfma_f32_16x16x32_f16 v[162:165], v[62:65], v[110:113], v[162:165]
	ds_read_b128 v[110:113], v151 offset:5120
	ds_read_b128 v[218:221], v151 offset:5728
	s_waitcnt lgkmcnt(1)
	v_mfma_f32_16x16x32_f16 v[138:141], v[58:61], v[110:113], v[138:141]
	v_mfma_f32_16x16x32_f16 v[170:173], v[62:65], v[110:113], v[170:173]
	s_waitcnt lgkmcnt(0)
	v_mfma_f32_16x16x32_f16 v[174:177], v[58:61], v[218:221], v[174:177]
	v_mfma_f32_16x16x32_f16 v[126:129], v[62:65], v[218:221], v[126:129]
	v_mfma_f32_16x16x32_f16 v[118:121], v[58:61], v[214:217], v[118:121]
	v_mfma_f32_16x16x32_f16 v[214:217], v[62:65], v[214:217], v[222:225]
	v_add_u32_e32 v110, 0xca640, v244
	v_min_u32_e32 v110, v110, v157
	global_load_dwordx4 v[110:113], v110, s[8:9] nt
	s_waitcnt vmcnt(21)
	v_cvt_pk_f16_f32 v9, v8, v9
	v_cvt_pk_f16_f32 v8, v6, v7
	ds_write_b16 v238, v8 offset:5472
	ds_write_b16_d16_hi v239, v8 offset:5472
	ds_write_b16 v240, v9 offset:5472
	ds_write_b16_d16_hi v241, v9 offset:5472
	ds_read_b128 v[6:9], v151 offset:6944
	ds_read_b128 v[218:221], v151 offset:7552
	s_waitcnt lgkmcnt(1)
	v_mfma_f32_16x16x32_f16 v[186:189], v[58:61], v[6:9], v[186:189]
	v_mfma_f32_16x16x32_f16 v[6:9], v[62:65], v[6:9], v[194:197]
	s_waitcnt lgkmcnt(0)
	v_mfma_f32_16x16x32_f16 v[58:61], v[58:61], v[218:221], v[38:41]
	v_mfma_f32_16x16x32_f16 v[194:197], v[62:65], v[218:221], v[22:25]
	s_nop 2
	ds_read_b128 v[22:25], v151 offset:320
	ds_read_b128 v[38:41], v151 offset:928
	s_waitcnt lgkmcnt(1)
	v_mfma_f32_16x16x32_f16 v[130:133], v[34:37], v[22:25], v[130:133]
	v_mfma_f32_16x16x32_f16 v[218:221], v[14:17], v[22:25], v[50:53]
	s_waitcnt lgkmcnt(0)
	v_mfma_f32_16x16x32_f16 v[142:145], v[34:37], v[38:41], v[142:145]
	v_mfma_f32_16x16x32_f16 v[158:161], v[14:17], v[38:41], v[158:161]
	v_add_u32_e32 v22, 0xe0c80, v150
	v_min_u32_e32 v22, v22, v157
	global_load_dwordx4 v[62:65], v22, s[8:9] nt
	s_waitcnt vmcnt(21)
	v_cvt_pk_f16_f32 v23, v72, v73
	v_cvt_pk_f16_f32 v22, v70, v71
	ds_write_b16 v234, v22 offset:6080
	ds_write_b16_d16_hi v235, v22 offset:6080
	ds_write_b16 v236, v23 offset:6080
	ds_write_b16_d16_hi v237, v23 offset:6080
	ds_read_b128 v[22:25], v151 offset:1536
	ds_read_b128 v[38:41], v151 offset:2144
	s_waitcnt lgkmcnt(1)
	v_mfma_f32_16x16x32_f16 v[178:181], v[34:37], v[22:25], v[178:181]
	v_mfma_f32_16x16x32_f16 v[182:185], v[14:17], v[22:25], v[182:185]
	s_waitcnt lgkmcnt(0)
	v_mfma_f32_16x16x32_f16 v[198:201], v[34:37], v[38:41], v[198:201]
	v_mfma_f32_16x16x32_f16 v[202:205], v[14:17], v[38:41], v[202:205]
	ds_read_b128 v[22:25], v151 offset:2752
	ds_read_b128 v[38:41], v151 offset:3360
	s_waitcnt lgkmcnt(1)
	v_mfma_f32_16x16x32_f16 v[134:137], v[34:37], v[22:25], v[134:137]
	v_mfma_f32_16x16x32_f16 v[146:149], v[14:17], v[22:25], v[146:149]
	s_waitcnt lgkmcnt(0)
	v_mfma_f32_16x16x32_f16 v[206:209], v[34:37], v[38:41], v[206:209]
	v_mfma_f32_16x16x32_f16 v[122:125], v[14:17], v[38:41], v[122:125]
	v_add_u32_e32 v22, 0xf72c0, v244
	v_min_u32_e32 v22, v22, v157
	global_load_dwordx4 v[70:73], v22, s[8:9] nt
	s_waitcnt vmcnt(21)
	v_cvt_pk_f16_f32 v23, v76, v77
	v_cvt_pk_f16_f32 v22, v74, v75
	ds_write_b16 v238, v22 offset:6688
	ds_write_b16_d16_hi v239, v22 offset:6688
	ds_write_b16 v240, v23 offset:6688
	ds_write_b16_d16_hi v241, v23 offset:6688
	ds_read_b128 v[22:25], v151 offset:3968
	ds_read_b128 v[38:41], v151 offset:4576
	s_waitcnt lgkmcnt(1)
	v_mfma_f32_16x16x32_f16 v[210:213], v[34:37], v[22:25], v[210:213]
	v_mfma_f32_16x16x32_f16 v[190:193], v[14:17], v[22:25], v[190:193]
	s_waitcnt lgkmcnt(0)
	v_mfma_f32_16x16x32_f16 v[166:169], v[34:37], v[38:41], v[166:169]
	v_mfma_f32_16x16x32_f16 v[162:165], v[14:17], v[38:41], v[162:165]
	ds_read_b128 v[22:25], v151 offset:5184
	ds_read_b128 v[38:41], v151 offset:5792
	s_waitcnt lgkmcnt(1)
	v_mfma_f32_16x16x32_f16 v[138:141], v[34:37], v[22:25], v[138:141]
	v_mfma_f32_16x16x32_f16 v[170:173], v[14:17], v[22:25], v[170:173]
	s_waitcnt lgkmcnt(0)
	v_mfma_f32_16x16x32_f16 v[174:177], v[34:37], v[38:41], v[174:177]
	v_mfma_f32_16x16x32_f16 v[126:129], v[14:17], v[38:41], v[126:129]
	v_add_u32_e32 v22, 0x10d900, v150
	v_min_u32_e32 v22, v22, v157
	v_cndmask_b32_e64 v22, 0, v22, s[0:1]
	global_load_dwordx4 v[74:77], v22, s[8:9] nt
	s_waitcnt vmcnt(21)
	v_cvt_pk_f16_f32 v23, v80, v81
	v_cvt_pk_f16_f32 v22, v78, v79
	ds_write_b16 v234, v22 offset:7296
	ds_write_b16_d16_hi v235, v22 offset:7296
	ds_write_b16 v236, v23 offset:7296
	ds_write_b16_d16_hi v237, v23 offset:7296
	ds_read_b128 v[22:25], v151 offset:6400
	ds_read_b128 v[38:41], v151 offset:7008
	s_mov_b32 s3, 0x70000
	ds_read_b128 v[78:81], v151 offset:7616
	s_waitcnt lgkmcnt(0)
	v_mfma_f32_16x16x32_f16 v[118:121], v[34:37], v[22:25], v[118:121]
	s_barrier
	v_sub_u32_e32 v245, v234, v243
	v_add_u32_e32 v246, 0xfffffdc0, v245
	v_min_u32_e32 v245, v245, v246
	v_add_u32_e32 v234, v242, v245
	v_sub_u32_e32 v245, v235, v243
	v_add_u32_e32 v246, 0xfffffdc0, v245
	v_min_u32_e32 v245, v245, v246
	v_add_u32_e32 v235, v242, v245
	v_sub_u32_e32 v245, v236, v243
	v_add_u32_e32 v246, 0xfffffdc0, v245
	v_min_u32_e32 v245, v245, v246
	v_add_u32_e32 v236, v242, v245
	v_sub_u32_e32 v245, v237, v243
	v_add_u32_e32 v246, 0xfffffdc0, v245
	v_min_u32_e32 v245, v245, v246
	v_add_u32_e32 v237, v242, v245
	v_sub_u32_e32 v245, v238, v243
	v_add_u32_e32 v246, 0xfffffdc0, v245
	v_min_u32_e32 v245, v245, v246
	v_add_u32_e32 v238, v242, v245
	v_sub_u32_e32 v245, v239, v243
	v_add_u32_e32 v246, 0xfffffdc0, v245
	v_min_u32_e32 v245, v245, v246
	v_add_u32_e32 v239, v242, v245
	v_sub_u32_e32 v245, v240, v243
	v_add_u32_e32 v246, 0xfffffdc0, v245
	v_min_u32_e32 v245, v245, v246
	v_add_u32_e32 v240, v242, v245
	v_sub_u32_e32 v245, v241, v243
	v_add_u32_e32 v246, 0xfffffdc0, v245
	v_min_u32_e32 v245, v245, v246
	v_add_u32_e32 v241, v242, v245
	v_mfma_f32_16x16x32_f16 v[214:217], v[14:17], v[22:25], v[214:217]
	v_add_co_u32_e32 v22, vcc, s3, v152
	s_mov_b32 s3, 0x74000
	s_nop 0
	v_addc_co_u32_e32 v23, vcc, 0, v153, vcc
	v_mfma_f32_16x16x32_f16 v[222:225], v[14:17], v[38:41], v[6:9]
	s_nop 2
	v_add_co_u32_e32 v6, vcc, s3, v152
	v_mfma_f32_16x16x32_f16 v[186:189], v[34:37], v[38:41], v[186:189]
	s_nop 0
	v_addc_co_u32_e32 v7, vcc, 0, v153, vcc
	global_load_dwordx4 v[38:41], v[22:23], off sc1
	global_load_dwordx4 v[50:53], v[22:23], off offset:256 sc1
	s_nop 0
	global_load_dwordx4 v[22:25], v[6:7], off sc1
	s_nop 0
	global_load_dwordx4 v[6:9], v[6:7], off offset:256 sc1
	v_mfma_f32_16x16x32_f16 v[34:37], v[34:37], v[78:81], v[58:61]
	v_mfma_f32_16x16x32_f16 v[14:17], v[14:17], v[78:81], v[194:197]
	v_add_u32_e32 v157, 0x111524dc, v154
	s_nop 0
	ds_read_b128 v[58:61], v151 offset:384
	v_add_u32_e32 v78, 0x1000, v150
	s_waitcnt vmcnt(24) lgkmcnt(0)
	v_mfma_f32_16x16x32_f16 v[130:133], v[42:45], v[58:61], v[130:133]
	s_waitcnt vmcnt(23)
	v_mfma_f32_16x16x32_f16 v[58:61], v[46:49], v[58:61], v[218:221]
	v_min_u32_e32 v78, v78, v157
	global_load_dwordx4 v[78:81], v78, s[8:9] nt
	s_waitcnt vmcnt(21)
	v_cvt_pk_f16_f32 v85, v84, v85
	v_cvt_pk_f16_f32 v84, v82, v83
	ds_write_b16 v234, v84 offset:0
	ds_write_b16_d16_hi v235, v84 offset:0
	ds_write_b16 v236, v85 offset:0
	ds_write_b16_d16_hi v237, v85 offset:0
	ds_read_b128 v[82:85], v151 offset:992
	ds_read_b128 v[194:197], v151 offset:1600
	s_waitcnt lgkmcnt(1)
	v_mfma_f32_16x16x32_f16 v[142:145], v[42:45], v[82:85], v[142:145]
	v_mfma_f32_16x16x32_f16 v[158:161], v[46:49], v[82:85], v[158:161]
	s_waitcnt lgkmcnt(0)
	v_mfma_f32_16x16x32_f16 v[178:181], v[42:45], v[194:197], v[178:181]
	v_mfma_f32_16x16x32_f16 v[182:185], v[46:49], v[194:197], v[182:185]
	ds_read_b128 v[82:85], v151 offset:2208
	ds_read_b128 v[194:197], v151 offset:2816
	s_waitcnt lgkmcnt(1)
	v_mfma_f32_16x16x32_f16 v[198:201], v[42:45], v[82:85], v[198:201]
	v_mfma_f32_16x16x32_f16 v[202:205], v[46:49], v[82:85], v[202:205]
	s_waitcnt lgkmcnt(0)
	v_mfma_f32_16x16x32_f16 v[134:137], v[42:45], v[194:197], v[134:137]
	v_mfma_f32_16x16x32_f16 v[146:149], v[46:49], v[194:197], v[146:149]
	v_add_u32_e32 v82, 0x17640, v244
	v_min_u32_e32 v82, v82, v157
	global_load_dwordx4 v[82:85], v82, s[8:9] nt
	s_waitcnt vmcnt(21)
	v_cvt_pk_f16_f32 v89, v88, v89
	v_cvt_pk_f16_f32 v88, v86, v87
	ds_write_b16 v238, v88 offset:608
	ds_write_b16_d16_hi v239, v88 offset:608
	ds_write_b16 v240, v89 offset:608
	ds_write_b16_d16_hi v241, v89 offset:608
	ds_read_b128 v[86:89], v151 offset:3424
	ds_read_b128 v[194:197], v151 offset:5248
	s_waitcnt lgkmcnt(1)
	v_mfma_f32_16x16x32_f16 v[206:209], v[42:45], v[86:89], v[206:209]
	v_mfma_f32_16x16x32_f16 v[122:125], v[46:49], v[86:89], v[122:125]
	ds_read_b128 v[86:89], v151 offset:4032
	ds_read_b128 v[218:221], v151 offset:4640
	s_waitcnt lgkmcnt(1)
	v_mfma_f32_16x16x32_f16 v[210:213], v[42:45], v[86:89], v[210:213]
	v_mfma_f32_16x16x32_f16 v[190:193], v[46:49], v[86:89], v[190:193]
	s_waitcnt lgkmcnt(0)
	v_mfma_f32_16x16x32_f16 v[166:169], v[42:45], v[218:221], v[166:169]
	v_mfma_f32_16x16x32_f16 v[162:165], v[46:49], v[218:221], v[162:165]
	v_mfma_f32_16x16x32_f16 v[138:141], v[42:45], v[194:197], v[138:141]
	v_mfma_f32_16x16x32_f16 v[170:173], v[46:49], v[194:197], v[170:173]
	v_add_u32_e32 v86, 0x2dc80, v150
	v_min_u32_e32 v86, v86, v157
	global_load_dwordx4 v[86:89], v86, s[8:9] nt
	s_waitcnt vmcnt(21)
	v_cvt_pk_f16_f32 v93, v92, v93
	v_cvt_pk_f16_f32 v92, v90, v91
	ds_write_b16 v234, v92 offset:1216
	ds_write_b16_d16_hi v235, v92 offset:1216
	ds_write_b16 v236, v93 offset:1216
	ds_write_b16_d16_hi v237, v93 offset:1216
	ds_read_b128 v[90:93], v151 offset:5856
	ds_read_b128 v[194:197], v151 offset:6464
	s_waitcnt lgkmcnt(1)
	v_mfma_f32_16x16x32_f16 v[174:177], v[42:45], v[90:93], v[174:177]
	v_mfma_f32_16x16x32_f16 v[126:129], v[46:49], v[90:93], v[126:129]
	s_waitcnt lgkmcnt(0)
	v_mfma_f32_16x16x32_f16 v[118:121], v[42:45], v[194:197], v[118:121]
	v_mfma_f32_16x16x32_f16 v[194:197], v[46:49], v[194:197], v[214:217]
	ds_read_b128 v[90:93], v151 offset:7072
	s_nop 1
	ds_read_b128 v[214:217], v151 offset:7680
	s_waitcnt lgkmcnt(1)
	v_mfma_f32_16x16x32_f16 v[186:189], v[42:45], v[90:93], v[186:189]
	v_mfma_f32_16x16x32_f16 v[218:221], v[46:49], v[90:93], v[222:225]
	s_waitcnt lgkmcnt(0)
	v_mfma_f32_16x16x32_f16 v[34:37], v[42:45], v[214:217], v[34:37]
	v_mfma_f32_16x16x32_f16 v[46:49], v[46:49], v[214:217], v[14:17]
	s_nop 2
	v_add_u32_e32 v14, 0x442c0, v244
	v_min_u32_e32 v14, v14, v157
	global_load_dwordx4 v[90:93], v14, s[8:9] nt
	s_waitcnt vmcnt(21)
	v_cvt_pk_f16_f32 v15, v96, v97
	v_cvt_pk_f16_f32 v14, v94, v95
	ds_write_b16 v238, v14 offset:1824
	ds_write_b16_d16_hi v239, v14 offset:1824
	ds_write_b16 v240, v15 offset:1824
	ds_write_b16_d16_hi v241, v15 offset:1824
	ds_read_b128 v[14:17], v151 offset:448
	ds_read_b128 v[42:45], v151 offset:1056
	s_waitcnt lgkmcnt(1)
	v_mfma_f32_16x16x32_f16 v[130:133], v[26:29], v[14:17], v[130:133]
	v_mfma_f32_16x16x32_f16 v[214:217], v[2:5], v[14:17], v[58:61]
	s_waitcnt lgkmcnt(0)
	v_mfma_f32_16x16x32_f16 v[142:145], v[26:29], v[42:45], v[142:145]
	v_mfma_f32_16x16x32_f16 v[158:161], v[2:5], v[42:45], v[158:161]
	ds_read_b128 v[14:17], v151 offset:1664
	ds_read_b128 v[42:45], v151 offset:2272
	s_waitcnt lgkmcnt(1)
	v_mfma_f32_16x16x32_f16 v[178:181], v[26:29], v[14:17], v[178:181]
	v_mfma_f32_16x16x32_f16 v[182:185], v[2:5], v[14:17], v[182:185]
	s_waitcnt lgkmcnt(0)
	v_mfma_f32_16x16x32_f16 v[198:201], v[26:29], v[42:45], v[198:201]
	v_mfma_f32_16x16x32_f16 v[202:205], v[2:5], v[42:45], v[202:205]
	v_add_u32_e32 v14, 0x5a900, v150
	v_min_u32_e32 v14, v14, v157
	global_load_dwordx4 v[94:97], v14, s[8:9] nt
	s_waitcnt vmcnt(21)
	v_cvt_pk_f16_f32 v15, v100, v101
	v_cvt_pk_f16_f32 v14, v98, v99
	ds_write_b16 v234, v14 offset:2432
	ds_write_b16_d16_hi v235, v14 offset:2432
	ds_write_b16 v236, v15 offset:2432
	ds_write_b16_d16_hi v237, v15 offset:2432
	ds_read_b128 v[14:17], v151 offset:2880
	ds_read_b128 v[42:45], v151 offset:3488
	s_waitcnt lgkmcnt(1)
	v_mfma_f32_16x16x32_f16 v[134:137], v[26:29], v[14:17], v[134:137]
	v_mfma_f32_16x16x32_f16 v[146:149], v[2:5], v[14:17], v[146:149]
	s_waitcnt lgkmcnt(0)
	v_mfma_f32_16x16x32_f16 v[206:209], v[26:29], v[42:45], v[206:209]
	v_mfma_f32_16x16x32_f16 v[122:125], v[2:5], v[42:45], v[122:125]
	ds_read_b128 v[14:17], v151 offset:4096
	ds_read_b128 v[42:45], v151 offset:4704
	s_waitcnt lgkmcnt(1)
	v_mfma_f32_16x16x32_f16 v[210:213], v[26:29], v[14:17], v[210:213]
	v_mfma_f32_16x16x32_f16 v[190:193], v[2:5], v[14:17], v[190:193]
	s_waitcnt lgkmcnt(0)
	v_mfma_f32_16x16x32_f16 v[166:169], v[26:29], v[42:45], v[166:169]
	v_mfma_f32_16x16x32_f16 v[162:165], v[2:5], v[42:45], v[162:165]
	v_add_u32_e32 v14, 0x70f40, v244
	v_min_u32_e32 v14, v14, v157
	global_load_dwordx4 v[98:101], v14, s[8:9] nt
	s_waitcnt vmcnt(21)
	v_cvt_pk_f16_f32 v15, v104, v105
	v_cvt_pk_f16_f32 v14, v102, v103
	ds_write_b16 v238, v14 offset:3040
	ds_write_b16_d16_hi v239, v14 offset:3040
	ds_write_b16 v240, v15 offset:3040
	ds_write_b16_d16_hi v241, v15 offset:3040
	ds_read_b128 v[14:17], v151 offset:5312
	ds_read_b128 v[42:45], v151 offset:5920
	s_waitcnt lgkmcnt(1)
	v_mfma_f32_16x16x32_f16 v[138:141], v[26:29], v[14:17], v[138:141]
	v_mfma_f32_16x16x32_f16 v[170:173], v[2:5], v[14:17], v[170:173]
	s_waitcnt lgkmcnt(0)
	v_mfma_f32_16x16x32_f16 v[174:177], v[26:29], v[42:45], v[174:177]
	v_mfma_f32_16x16x32_f16 v[126:129], v[2:5], v[42:45], v[126:129]
	ds_read_b128 v[14:17], v151 offset:6528
	ds_read_b128 v[42:45], v151 offset:7136
	s_waitcnt lgkmcnt(1)
	v_mfma_f32_16x16x32_f16 v[118:121], v[26:29], v[14:17], v[118:121]
	v_mfma_f32_16x16x32_f16 v[194:197], v[2:5], v[14:17], v[194:197]
	s_waitcnt lgkmcnt(0)
	v_mfma_f32_16x16x32_f16 v[186:189], v[26:29], v[42:45], v[186:189]
	v_mfma_f32_16x16x32_f16 v[218:221], v[2:5], v[42:45], v[218:221]
	v_add_u32_e32 v14, 0x87580, v150
	v_min_u32_e32 v14, v14, v157
	global_load_dwordx4 v[102:105], v14, s[8:9] nt
	s_waitcnt vmcnt(21)
	v_cvt_pk_f16_f32 v15, v108, v109
	v_cvt_pk_f16_f32 v14, v106, v107
	ds_write_b16 v234, v14 offset:3648
	ds_write_b16_d16_hi v235, v14 offset:3648
	ds_write_b16 v236, v15 offset:3648
	ds_write_b16_d16_hi v237, v15 offset:3648
	ds_read_b128 v[106:109], v151 offset:7744
	s_mov_b32 s3, 0x78000
	v_add_co_u32_e32 v14, vcc, s3, v152
	s_mov_b32 s3, 0x7c000
	s_nop 0
	v_addc_co_u32_e32 v15, vcc, 0, v153, vcc
	global_load_dwordx4 v[42:45], v[14:15], off sc1
	global_load_dwordx4 v[58:61], v[14:15], off offset:256 sc1
	v_add_co_u32_e32 v14, vcc, s3, v152
	s_waitcnt lgkmcnt(0)
	v_mfma_f32_16x16x32_f16 v[26:29], v[26:29], v[106:109], v[34:37]
	v_addc_co_u32_e32 v15, vcc, 0, v153, vcc
	s_nop 1
	global_load_dwordx4 v[34:37], v[14:15], off sc1
	s_nop 0
	global_load_dwordx4 v[14:17], v[14:15], off offset:256 sc1
	v_mfma_f32_16x16x32_f16 v[46:49], v[2:5], v[106:109], v[46:49]
	ds_read_b128 v[2:5], v151 offset:512
	ds_read_b128 v[106:109], v151 offset:1120
	s_waitcnt vmcnt(24) lgkmcnt(1)
	v_mfma_f32_16x16x32_f16 v[130:133], v[54:57], v[2:5], v[130:133]
	s_waitcnt vmcnt(23)
	v_mfma_f32_16x16x32_f16 v[214:217], v[66:69], v[2:5], v[214:217]
	ds_read_b128 v[2:5], v151 offset:1728
	s_waitcnt lgkmcnt(1)
	v_mfma_f32_16x16x32_f16 v[142:145], v[54:57], v[106:109], v[142:145]
	v_mfma_f32_16x16x32_f16 v[158:161], v[66:69], v[106:109], v[158:161]
	s_waitcnt lgkmcnt(0)
	v_mfma_f32_16x16x32_f16 v[178:181], v[54:57], v[2:5], v[178:181]
	v_mfma_f32_16x16x32_f16 v[182:185], v[66:69], v[2:5], v[182:185]
	v_add_u32_e32 v2, 0x9dbc0, v244
	v_min_u32_e32 v2, v2, v157
	global_load_dwordx4 v[2:5], v2, s[8:9] nt
	s_waitcnt vmcnt(21)
	v_cvt_pk_f16_f32 v13, v12, v13
	v_cvt_pk_f16_f32 v12, v10, v11
	ds_write_b16 v238, v12 offset:4256
	ds_write_b16_d16_hi v239, v12 offset:4256
	ds_write_b16 v240, v13 offset:4256
	ds_write_b16_d16_hi v241, v13 offset:4256
	ds_read_b128 v[10:13], v151 offset:2336
	ds_read_b128 v[106:109], v151 offset:2944
	s_waitcnt lgkmcnt(1)
	v_mfma_f32_16x16x32_f16 v[198:201], v[54:57], v[10:13], v[198:201]
	v_mfma_f32_16x16x32_f16 v[10:13], v[66:69], v[10:13], v[202:205]
	s_waitcnt lgkmcnt(0)
	v_mfma_f32_16x16x32_f16 v[134:137], v[54:57], v[106:109], v[134:137]
	v_mfma_f32_16x16x32_f16 v[146:149], v[66:69], v[106:109], v[146:149]
	ds_read_b128 v[106:109], v151 offset:3552
	ds_read_b128 v[202:205], v151 offset:4160
	s_waitcnt lgkmcnt(1)
	v_mfma_f32_16x16x32_f16 v[206:209], v[54:57], v[106:109], v[206:209]
	v_mfma_f32_16x16x32_f16 v[122:125], v[66:69], v[106:109], v[122:125]
	s_waitcnt lgkmcnt(0)
	v_mfma_f32_16x16x32_f16 v[210:213], v[54:57], v[202:205], v[210:213]
	v_mfma_f32_16x16x32_f16 v[190:193], v[66:69], v[202:205], v[190:193]
	v_add_u32_e32 v106, 0xb4200, v150
	v_min_u32_e32 v106, v106, v157
	global_load_dwordx4 v[106:109], v106, s[8:9] nt
	s_waitcnt vmcnt(21)
	v_cvt_pk_f16_f32 v117, v116, v117
	v_cvt_pk_f16_f32 v116, v114, v115
	ds_write_b16 v234, v116 offset:4864
	ds_write_b16_d16_hi v235, v116 offset:4864
	ds_write_b16 v236, v117 offset:4864
	ds_write_b16_d16_hi v237, v117 offset:4864
	ds_read_b128 v[114:117], v151 offset:4768
	ds_read_b128 v[202:205], v151 offset:6592
	s_waitcnt lgkmcnt(1)
	v_mfma_f32_16x16x32_f16 v[166:169], v[54:57], v[114:117], v[166:169]
	v_mfma_f32_16x16x32_f16 v[162:165], v[66:69], v[114:117], v[162:165]
	ds_read_b128 v[114:117], v151 offset:5376
	ds_read_b128 v[222:225], v151 offset:5984
	s_waitcnt lgkmcnt(1)
	v_mfma_f32_16x16x32_f16 v[138:141], v[54:57], v[114:117], v[138:141]
	v_mfma_f32_16x16x32_f16 v[170:173], v[66:69], v[114:117], v[170:173]
	s_waitcnt lgkmcnt(0)
	v_mfma_f32_16x16x32_f16 v[174:177], v[54:57], v[222:225], v[174:177]
	v_mfma_f32_16x16x32_f16 v[126:129], v[66:69], v[222:225], v[126:129]
	v_mfma_f32_16x16x32_f16 v[222:225], v[54:57], v[202:205], v[118:121]
	v_mfma_f32_16x16x32_f16 v[194:197], v[66:69], v[202:205], v[194:197]
	v_add_u32_e32 v114, 0xca840, v244
	v_min_u32_e32 v114, v114, v157
	global_load_dwordx4 v[114:117], v114, s[8:9] nt
	s_waitcnt vmcnt(21)
	v_cvt_pk_f16_f32 v113, v112, v113
	v_cvt_pk_f16_f32 v112, v110, v111
	ds_write_b16 v238, v112 offset:5472
	ds_write_b16_d16_hi v239, v112 offset:5472
	ds_write_b16 v240, v113 offset:5472
	ds_write_b16_d16_hi v241, v113 offset:5472
	ds_read_b128 v[110:113], v151 offset:7200
	ds_read_b128 v[118:121], v151 offset:7808
	s_waitcnt lgkmcnt(1)
	v_mfma_f32_16x16x32_f16 v[186:189], v[54:57], v[110:113], v[186:189]
	v_mfma_f32_16x16x32_f16 v[202:205], v[66:69], v[110:113], v[218:221]
	s_waitcnt lgkmcnt(0)
	v_mfma_f32_16x16x32_f16 v[26:29], v[54:57], v[118:121], v[26:29]
	v_mfma_f32_16x16x32_f16 v[66:69], v[66:69], v[118:121], v[46:49]
	s_nop 2
	ds_read_b128 v[46:49], v151 offset:0
	ds_read_b128 v[54:57], v151 offset:608
	s_waitcnt lgkmcnt(1)
	v_mfma_f32_16x16x32_f16 v[130:133], v[30:33], v[46:49], v[130:133]
	v_mfma_f32_16x16x32_f16 v[214:217], v[18:21], v[46:49], v[214:217]
	s_waitcnt lgkmcnt(0)
	v_mfma_f32_16x16x32_f16 v[142:145], v[30:33], v[54:57], v[142:145]
	v_mfma_f32_16x16x32_f16 v[158:161], v[18:21], v[54:57], v[158:161]
	v_add_u32_e32 v46, 0xe0e80, v150
	v_min_u32_e32 v46, v46, v157
	global_load_dwordx4 v[110:113], v46, s[8:9] nt
	s_waitcnt vmcnt(21)
	v_cvt_pk_f16_f32 v47, v64, v65
	v_cvt_pk_f16_f32 v46, v62, v63
	ds_write_b16 v234, v46 offset:6080
	ds_write_b16_d16_hi v235, v46 offset:6080
	ds_write_b16 v236, v47 offset:6080
	ds_write_b16_d16_hi v237, v47 offset:6080
	ds_read_b128 v[46:49], v151 offset:1216
	ds_read_b128 v[54:57], v151 offset:1824
	s_waitcnt lgkmcnt(1)
	v_mfma_f32_16x16x32_f16 v[62:65], v[30:33], v[46:49], v[178:181]
	v_mfma_f32_16x16x32_f16 v[178:181], v[18:21], v[46:49], v[182:185]
	s_waitcnt lgkmcnt(0)
	v_mfma_f32_16x16x32_f16 v[182:185], v[30:33], v[54:57], v[198:201]
	v_mfma_f32_16x16x32_f16 v[198:201], v[18:21], v[54:57], v[10:13]
	s_nop 2
	ds_read_b128 v[10:13], v151 offset:2432
	ds_read_b128 v[46:49], v151 offset:3040
	s_waitcnt lgkmcnt(1)
	v_mfma_f32_16x16x32_f16 v[134:137], v[30:33], v[10:13], v[134:137]
	v_mfma_f32_16x16x32_f16 v[146:149], v[18:21], v[10:13], v[146:149]
	s_waitcnt lgkmcnt(0)
	v_mfma_f32_16x16x32_f16 v[206:209], v[30:33], v[46:49], v[206:209]
	v_mfma_f32_16x16x32_f16 v[122:125], v[18:21], v[46:49], v[122:125]
	v_add_u32_e32 v10, 0xf74c0, v244
	v_min_u32_e32 v10, v10, v157
	global_load_dwordx4 v[118:121], v10, s[8:9] nt
	s_waitcnt vmcnt(21)
	v_cvt_pk_f16_f32 v11, v72, v73
	v_cvt_pk_f16_f32 v10, v70, v71
	ds_write_b16 v238, v10 offset:6688
	ds_write_b16_d16_hi v239, v10 offset:6688
	ds_write_b16 v240, v11 offset:6688
	ds_write_b16_d16_hi v241, v11 offset:6688
	ds_read_b128 v[10:13], v151 offset:3648
	ds_read_b128 v[46:49], v151 offset:4256
	s_waitcnt lgkmcnt(1)
	v_mfma_f32_16x16x32_f16 v[210:213], v[30:33], v[10:13], v[210:213]
	v_mfma_f32_16x16x32_f16 v[190:193], v[18:21], v[10:13], v[190:193]
	s_waitcnt lgkmcnt(0)
	v_mfma_f32_16x16x32_f16 v[166:169], v[30:33], v[46:49], v[166:169]
	v_mfma_f32_16x16x32_f16 v[162:165], v[18:21], v[46:49], v[162:165]
	ds_read_b128 v[10:13], v151 offset:4864
	ds_read_b128 v[46:49], v151 offset:5472
	s_waitcnt lgkmcnt(1)
	v_mfma_f32_16x16x32_f16 v[138:141], v[30:33], v[10:13], v[138:141]
	v_mfma_f32_16x16x32_f16 v[170:173], v[18:21], v[10:13], v[170:173]
	s_waitcnt lgkmcnt(0)
	v_mfma_f32_16x16x32_f16 v[174:177], v[30:33], v[46:49], v[174:177]
	v_mfma_f32_16x16x32_f16 v[126:129], v[18:21], v[46:49], v[126:129]
	v_add_u32_e32 v10, 0x10db00, v150
	v_min_u32_e32 v10, v10, v157
	v_cndmask_b32_e64 v10, 0, v10, s[0:1]
	global_load_dwordx4 v[70:73], v10, s[8:9] nt
	s_waitcnt vmcnt(21)
	v_cvt_pk_f16_f32 v11, v76, v77
	v_cvt_pk_f16_f32 v10, v74, v75
	ds_write_b16 v234, v10 offset:7296
	ds_write_b16_d16_hi v235, v10 offset:7296
	ds_write_b16 v236, v11 offset:7296
	ds_write_b16_d16_hi v237, v11 offset:7296
	ds_read_b128 v[10:13], v151 offset:6080
	ds_read_b128 v[46:49], v151 offset:6688
	ds_read_b128 v[74:77], v151 offset:7296
	s_mov_b32 s3, 0x80000
	s_waitcnt lgkmcnt(0)
	v_mfma_f32_16x16x32_f16 v[218:221], v[30:33], v[10:13], v[222:225]
	s_barrier
	v_sub_u32_e32 v245, v234, v243
	v_add_u32_e32 v246, 0xfffffdc0, v245
	v_min_u32_e32 v245, v245, v246
	v_add_u32_e32 v234, v242, v245
	v_sub_u32_e32 v245, v235, v243
	v_add_u32_e32 v246, 0xfffffdc0, v245
	v_min_u32_e32 v245, v245, v246
	v_add_u32_e32 v235, v242, v245
	v_sub_u32_e32 v245, v236, v243
	v_add_u32_e32 v246, 0xfffffdc0, v245
	v_min_u32_e32 v245, v245, v246
	v_add_u32_e32 v236, v242, v245
	v_sub_u32_e32 v245, v237, v243
	v_add_u32_e32 v246, 0xfffffdc0, v245
	v_min_u32_e32 v245, v245, v246
	v_add_u32_e32 v237, v242, v245
	v_sub_u32_e32 v245, v238, v243
	v_add_u32_e32 v246, 0xfffffdc0, v245
	v_min_u32_e32 v245, v245, v246
	v_add_u32_e32 v238, v242, v245
	v_sub_u32_e32 v245, v239, v243
	v_add_u32_e32 v246, 0xfffffdc0, v245
	v_min_u32_e32 v245, v245, v246
	v_add_u32_e32 v239, v242, v245
	v_sub_u32_e32 v245, v240, v243
	v_add_u32_e32 v246, 0xfffffdc0, v245
	v_min_u32_e32 v245, v245, v246
	v_add_u32_e32 v240, v242, v245
	v_sub_u32_e32 v245, v241, v243
	v_add_u32_e32 v246, 0xfffffdc0, v245
	v_min_u32_e32 v245, v245, v246
	v_add_u32_e32 v241, v242, v245
	v_mfma_f32_16x16x32_f16 v[194:197], v[18:21], v[10:13], v[194:197]
	v_add_co_u32_e32 v10, vcc, s3, v152
	s_mov_b32 s3, 0x84000
	s_nop 0
	v_addc_co_u32_e32 v11, vcc, 0, v153, vcc
	v_mfma_f32_16x16x32_f16 v[186:189], v[30:33], v[46:49], v[186:189]
	v_mfma_f32_16x16x32_f16 v[202:205], v[18:21], v[46:49], v[202:205]
	global_load_dwordx4 v[46:49], v[10:11], off sc1
	global_load_dwordx4 v[54:57], v[10:11], off offset:256 sc1
	v_add_co_u32_e32 v10, vcc, s3, v152
	v_mfma_f32_16x16x32_f16 v[30:33], v[30:33], v[74:77], v[26:29]
	s_nop 0
	v_addc_co_u32_e32 v11, vcc, 0, v153, vcc
	s_nop 0
	global_load_dwordx4 v[26:29], v[10:11], off sc1
	s_nop 0
	global_load_dwordx4 v[10:13], v[10:11], off offset:256 sc1
	v_mfma_f32_16x16x32_f16 v[18:21], v[18:21], v[74:77], v[66:69]
	v_add_u32_e32 v157, 0x111526dc, v154
	s_nop 1
	ds_read_b128 v[66:69], v151 offset:64
	v_add_u32_e32 v74, 0x1200, v150
	s_waitcnt vmcnt(24) lgkmcnt(0)
	v_mfma_f32_16x16x32_f16 v[130:133], v[38:41], v[66:69], v[130:133]
	s_waitcnt vmcnt(23)
	v_mfma_f32_16x16x32_f16 v[66:69], v[50:53], v[66:69], v[214:217]
	v_min_u32_e32 v74, v74, v157
	global_load_dwordx4 v[74:77], v74, s[8:9] nt
	s_waitcnt vmcnt(21)
	v_cvt_pk_f16_f32 v81, v80, v81
	v_cvt_pk_f16_f32 v80, v78, v79
	ds_write_b16 v234, v80 offset:0
	ds_write_b16_d16_hi v235, v80 offset:0
	ds_write_b16 v236, v81 offset:0
	ds_write_b16_d16_hi v237, v81 offset:0
	ds_read_b128 v[78:81], v151 offset:672
	ds_read_b128 v[214:217], v151 offset:1280
	s_waitcnt lgkmcnt(1)
	v_mfma_f32_16x16x32_f16 v[142:145], v[38:41], v[78:81], v[142:145]
	v_mfma_f32_16x16x32_f16 v[158:161], v[50:53], v[78:81], v[158:161]
	s_waitcnt lgkmcnt(0)
	v_mfma_f32_16x16x32_f16 v[62:65], v[38:41], v[214:217], v[62:65]
	v_mfma_f32_16x16x32_f16 v[178:181], v[50:53], v[214:217], v[178:181]
	ds_read_b128 v[78:81], v151 offset:1888
	ds_read_b128 v[214:217], v151 offset:2496
	s_waitcnt lgkmcnt(1)
	v_mfma_f32_16x16x32_f16 v[182:185], v[38:41], v[78:81], v[182:185]
	v_mfma_f32_16x16x32_f16 v[198:201], v[50:53], v[78:81], v[198:201]
	s_waitcnt lgkmcnt(0)
	v_mfma_f32_16x16x32_f16 v[134:137], v[38:41], v[214:217], v[134:137]
	v_mfma_f32_16x16x32_f16 v[146:149], v[50:53], v[214:217], v[146:149]
	v_add_u32_e32 v78, 0x17840, v244
	v_min_u32_e32 v78, v78, v157
	global_load_dwordx4 v[78:81], v78, s[8:9] nt
	s_waitcnt vmcnt(21)
	v_cvt_pk_f16_f32 v85, v84, v85
	v_cvt_pk_f16_f32 v84, v82, v83
	ds_write_b16 v238, v84 offset:608
	ds_write_b16_d16_hi v239, v84 offset:608
	ds_write_b16 v240, v85 offset:608
	ds_write_b16_d16_hi v241, v85 offset:608
	ds_read_b128 v[82:85], v151 offset:3104
	ds_read_b128 v[214:217], v151 offset:4928
	s_waitcnt lgkmcnt(1)
	v_mfma_f32_16x16x32_f16 v[206:209], v[38:41], v[82:85], v[206:209]
	v_mfma_f32_16x16x32_f16 v[122:125], v[50:53], v[82:85], v[122:125]
	ds_read_b128 v[82:85], v151 offset:3712
	ds_read_b128 v[222:225], v151 offset:4320
	s_waitcnt lgkmcnt(1)
	v_mfma_f32_16x16x32_f16 v[210:213], v[38:41], v[82:85], v[210:213]
	v_mfma_f32_16x16x32_f16 v[190:193], v[50:53], v[82:85], v[190:193]
	s_waitcnt lgkmcnt(0)
	v_mfma_f32_16x16x32_f16 v[166:169], v[38:41], v[222:225], v[166:169]
	v_mfma_f32_16x16x32_f16 v[162:165], v[50:53], v[222:225], v[162:165]
	v_mfma_f32_16x16x32_f16 v[138:141], v[38:41], v[214:217], v[138:141]
	v_mfma_f32_16x16x32_f16 v[170:173], v[50:53], v[214:217], v[170:173]
	v_add_u32_e32 v82, 0x2de80, v150
	v_min_u32_e32 v82, v82, v157
	global_load_dwordx4 v[82:85], v82, s[8:9] nt
	s_waitcnt vmcnt(21)
	v_cvt_pk_f16_f32 v89, v88, v89
	v_cvt_pk_f16_f32 v88, v86, v87
	ds_write_b16 v234, v88 offset:1216
	ds_write_b16_d16_hi v235, v88 offset:1216
	ds_write_b16 v236, v89 offset:1216
	ds_write_b16_d16_hi v237, v89 offset:1216
	ds_read_b128 v[86:89], v151 offset:5536
	ds_read_b128 v[214:217], v151 offset:6144
	s_waitcnt lgkmcnt(1)
	v_mfma_f32_16x16x32_f16 v[174:177], v[38:41], v[86:89], v[174:177]
	v_mfma_f32_16x16x32_f16 v[126:129], v[50:53], v[86:89], v[126:129]
	s_waitcnt lgkmcnt(0)
	v_mfma_f32_16x16x32_f16 v[218:221], v[38:41], v[214:217], v[218:221]
	v_mfma_f32_16x16x32_f16 v[194:197], v[50:53], v[214:217], v[194:197]
	ds_read_b128 v[86:89], v151 offset:6752
	ds_read_b128 v[214:217], v151 offset:7360
	s_waitcnt lgkmcnt(1)
	v_mfma_f32_16x16x32_f16 v[186:189], v[38:41], v[86:89], v[186:189]
	v_mfma_f32_16x16x32_f16 v[202:205], v[50:53], v[86:89], v[202:205]
	s_waitcnt lgkmcnt(0)
	v_mfma_f32_16x16x32_f16 v[30:33], v[38:41], v[214:217], v[30:33]
	v_mfma_f32_16x16x32_f16 v[38:41], v[50:53], v[214:217], v[18:21]
	s_nop 2
	v_add_u32_e32 v18, 0x444c0, v244
	v_min_u32_e32 v18, v18, v157
	global_load_dwordx4 v[50:53], v18, s[8:9] nt
	s_waitcnt vmcnt(21)
	v_cvt_pk_f16_f32 v19, v92, v93
	v_cvt_pk_f16_f32 v18, v90, v91
	ds_write_b16 v238, v18 offset:1824
	ds_write_b16_d16_hi v239, v18 offset:1824
	ds_write_b16 v240, v19 offset:1824
	ds_write_b16_d16_hi v241, v19 offset:1824
	ds_read_b128 v[18:21], v151 offset:128
	ds_read_b128 v[86:89], v151 offset:736
	s_waitcnt lgkmcnt(1)
	v_mfma_f32_16x16x32_f16 v[130:133], v[22:25], v[18:21], v[130:133]
	v_mfma_f32_16x16x32_f16 v[214:217], v[6:9], v[18:21], v[66:69]
	ds_read_b128 v[18:21], v151 offset:1344
	s_nop 1
	ds_read_b128 v[66:69], v151 offset:1952
	s_waitcnt lgkmcnt(2)
	v_mfma_f32_16x16x32_f16 v[142:145], v[22:25], v[86:89], v[142:145]
	v_mfma_f32_16x16x32_f16 v[158:161], v[6:9], v[86:89], v[158:161]
	s_waitcnt lgkmcnt(1)
	v_mfma_f32_16x16x32_f16 v[222:225], v[22:25], v[18:21], v[62:65]
	v_mfma_f32_16x16x32_f16 v[178:181], v[6:9], v[18:21], v[178:181]
	s_waitcnt lgkmcnt(0)
	v_mfma_f32_16x16x32_f16 v[182:185], v[22:25], v[66:69], v[182:185]
	v_mfma_f32_16x16x32_f16 v[198:201], v[6:9], v[66:69], v[198:201]
	v_add_u32_e32 v18, 0x5ab00, v150
	v_min_u32_e32 v18, v18, v157
	global_load_dwordx4 v[86:89], v18, s[8:9] nt
	s_waitcnt vmcnt(21)
	v_cvt_pk_f16_f32 v19, v96, v97
	v_cvt_pk_f16_f32 v18, v94, v95
	ds_write_b16 v234, v18 offset:2432
	ds_write_b16_d16_hi v235, v18 offset:2432
	ds_write_b16 v236, v19 offset:2432
	ds_write_b16_d16_hi v237, v19 offset:2432
	ds_read_b128 v[18:21], v151 offset:2560
	ds_read_b128 v[62:65], v151 offset:3168
	s_waitcnt lgkmcnt(1)
	v_mfma_f32_16x16x32_f16 v[134:137], v[22:25], v[18:21], v[134:137]
	v_mfma_f32_16x16x32_f16 v[146:149], v[6:9], v[18:21], v[146:149]
	s_waitcnt lgkmcnt(0)
	v_mfma_f32_16x16x32_f16 v[206:209], v[22:25], v[62:65], v[206:209]
	v_mfma_f32_16x16x32_f16 v[122:125], v[6:9], v[62:65], v[122:125]
	ds_read_b128 v[18:21], v151 offset:3776
	ds_read_b128 v[62:65], v151 offset:4384
	s_waitcnt lgkmcnt(1)
	v_mfma_f32_16x16x32_f16 v[210:213], v[22:25], v[18:21], v[210:213]
	v_mfma_f32_16x16x32_f16 v[190:193], v[6:9], v[18:21], v[190:193]
	s_waitcnt lgkmcnt(0)
	v_mfma_f32_16x16x32_f16 v[166:169], v[22:25], v[62:65], v[166:169]
	v_mfma_f32_16x16x32_f16 v[162:165], v[6:9], v[62:65], v[162:165]
	v_add_u32_e32 v18, 0x71140, v244
	v_min_u32_e32 v18, v18, v157
	global_load_dwordx4 v[90:93], v18, s[8:9] nt
	s_waitcnt vmcnt(21)
	v_cvt_pk_f16_f32 v19, v100, v101
	v_cvt_pk_f16_f32 v18, v98, v99
	ds_write_b16 v238, v18 offset:3040
	ds_write_b16_d16_hi v239, v18 offset:3040
	ds_write_b16 v240, v19 offset:3040
	ds_write_b16_d16_hi v241, v19 offset:3040
	ds_read_b128 v[18:21], v151 offset:4992
	ds_read_b128 v[62:65], v151 offset:5600
	s_waitcnt lgkmcnt(1)
	v_mfma_f32_16x16x32_f16 v[98:101], v[22:25], v[18:21], v[138:141]
	v_mfma_f32_16x16x32_f16 v[138:141], v[6:9], v[18:21], v[170:173]
	s_waitcnt lgkmcnt(0)
	v_mfma_f32_16x16x32_f16 v[170:173], v[22:25], v[62:65], v[174:177]
	v_mfma_f32_16x16x32_f16 v[126:129], v[6:9], v[62:65], v[126:129]
	ds_read_b128 v[18:21], v151 offset:6208
	ds_read_b128 v[62:65], v151 offset:6816
	s_waitcnt lgkmcnt(1)
	v_mfma_f32_16x16x32_f16 v[174:177], v[22:25], v[18:21], v[218:221]
	v_mfma_f32_16x16x32_f16 v[194:197], v[6:9], v[18:21], v[194:197]
	s_waitcnt lgkmcnt(0)
	v_mfma_f32_16x16x32_f16 v[186:189], v[22:25], v[62:65], v[186:189]
	v_mfma_f32_16x16x32_f16 v[202:205], v[6:9], v[62:65], v[202:205]
	v_add_u32_e32 v18, 0x87780, v150
	v_min_u32_e32 v18, v18, v157
	global_load_dwordx4 v[94:97], v18, s[8:9] nt
	s_waitcnt vmcnt(21)
	v_cvt_pk_f16_f32 v19, v104, v105
	v_cvt_pk_f16_f32 v18, v102, v103
	ds_write_b16 v234, v18 offset:3648
	ds_write_b16_d16_hi v235, v18 offset:3648
	ds_write_b16 v236, v19 offset:3648
	ds_write_b16_d16_hi v237, v19 offset:3648
	ds_read_b128 v[102:105], v151 offset:7424
	s_mov_b32 s3, 0x88000
	v_add_co_u32_e32 v18, vcc, s3, v152
	s_mov_b32 s3, 0x8c000
	s_nop 0
	v_addc_co_u32_e32 v19, vcc, 0, v153, vcc
	global_load_dwordx4 v[62:65], v[18:19], off sc1
	global_load_dwordx4 v[66:69], v[18:19], off offset:256 sc1
	v_add_co_u32_e32 v18, vcc, s3, v152
	s_waitcnt lgkmcnt(0)
	v_mfma_f32_16x16x32_f16 v[22:25], v[22:25], v[102:105], v[30:33]
	v_addc_co_u32_e32 v19, vcc, 0, v153, vcc
	s_nop 1
	global_load_dwordx4 v[30:33], v[18:19], off sc1
	s_nop 0
	global_load_dwordx4 v[18:21], v[18:19], off offset:256 sc1
	v_mfma_f32_16x16x32_f16 v[38:41], v[6:9], v[102:105], v[38:41]
	ds_read_b128 v[6:9], v151 offset:192
	ds_read_b128 v[102:105], v151 offset:800
	s_waitcnt vmcnt(24) lgkmcnt(1)
	v_mfma_f32_16x16x32_f16 v[130:133], v[42:45], v[6:9], v[130:133]
	s_waitcnt vmcnt(23)
	v_mfma_f32_16x16x32_f16 v[214:217], v[58:61], v[6:9], v[214:217]
	ds_read_b128 v[6:9], v151 offset:1408
	s_waitcnt lgkmcnt(1)
	v_mfma_f32_16x16x32_f16 v[142:145], v[42:45], v[102:105], v[142:145]
	v_mfma_f32_16x16x32_f16 v[158:161], v[58:61], v[102:105], v[158:161]
	s_waitcnt lgkmcnt(0)
	v_mfma_f32_16x16x32_f16 v[218:221], v[42:45], v[6:9], v[222:225]
	v_mfma_f32_16x16x32_f16 v[178:181], v[58:61], v[6:9], v[178:181]
	v_add_u32_e32 v6, 0x9ddc0, v244
	v_min_u32_e32 v6, v6, v157
	global_load_dwordx4 v[6:9], v6, s[8:9] nt
	s_waitcnt vmcnt(21)
	v_cvt_pk_f16_f32 v5, v4, v5
	v_cvt_pk_f16_f32 v4, v2, v3
	ds_write_b16 v238, v4 offset:4256
	ds_write_b16_d16_hi v239, v4 offset:4256
	ds_write_b16 v240, v5 offset:4256
	ds_write_b16_d16_hi v241, v5 offset:4256
	ds_read_b128 v[2:5], v151 offset:2016
	ds_read_b128 v[102:105], v151 offset:2624
	s_waitcnt lgkmcnt(1)
	v_mfma_f32_16x16x32_f16 v[182:185], v[42:45], v[2:5], v[182:185]
	v_mfma_f32_16x16x32_f16 v[2:5], v[58:61], v[2:5], v[198:201]
	s_waitcnt lgkmcnt(0)
	v_mfma_f32_16x16x32_f16 v[134:137], v[42:45], v[102:105], v[134:137]
	v_mfma_f32_16x16x32_f16 v[146:149], v[58:61], v[102:105], v[146:149]
	ds_read_b128 v[102:105], v151 offset:3232
	ds_read_b128 v[198:201], v151 offset:3840
	s_waitcnt lgkmcnt(1)
	v_mfma_f32_16x16x32_f16 v[206:209], v[42:45], v[102:105], v[206:209]
	v_mfma_f32_16x16x32_f16 v[122:125], v[58:61], v[102:105], v[122:125]
	s_waitcnt lgkmcnt(0)
	v_mfma_f32_16x16x32_f16 v[210:213], v[42:45], v[198:201], v[210:213]
	v_mfma_f32_16x16x32_f16 v[190:193], v[58:61], v[198:201], v[190:193]
	v_add_u32_e32 v102, 0xb4400, v150
	v_min_u32_e32 v102, v102, v157
	global_load_dwordx4 v[102:105], v102, s[8:9] nt
	s_waitcnt vmcnt(21)
	v_cvt_pk_f16_f32 v109, v108, v109
	v_cvt_pk_f16_f32 v108, v106, v107
	ds_write_b16 v234, v108 offset:4864
	ds_write_b16_d16_hi v235, v108 offset:4864
	ds_write_b16 v236, v109 offset:4864
	ds_write_b16_d16_hi v237, v109 offset:4864
	ds_read_b128 v[106:109], v151 offset:4448
	ds_read_b128 v[198:201], v151 offset:6272
	s_waitcnt lgkmcnt(1)
	v_mfma_f32_16x16x32_f16 v[166:169], v[42:45], v[106:109], v[166:169]
	v_mfma_f32_16x16x32_f16 v[162:165], v[58:61], v[106:109], v[162:165]
	ds_read_b128 v[106:109], v151 offset:5056
	ds_read_b128 v[222:225], v151 offset:5664
	s_waitcnt lgkmcnt(1)
	v_mfma_f32_16x16x32_f16 v[98:101], v[42:45], v[106:109], v[98:101]
	v_mfma_f32_16x16x32_f16 v[138:141], v[58:61], v[106:109], v[138:141]
	s_waitcnt lgkmcnt(0)
	v_mfma_f32_16x16x32_f16 v[170:173], v[42:45], v[222:225], v[170:173]
	v_mfma_f32_16x16x32_f16 v[126:129], v[58:61], v[222:225], v[126:129]
	v_mfma_f32_16x16x32_f16 v[174:177], v[42:45], v[198:201], v[174:177]
	v_mfma_f32_16x16x32_f16 v[194:197], v[58:61], v[198:201], v[194:197]
	v_add_u32_e32 v106, 0xcaa40, v244
	v_min_u32_e32 v106, v106, v157
	global_load_dwordx4 v[106:109], v106, s[8:9] nt
	s_waitcnt vmcnt(21)
	v_cvt_pk_f16_f32 v117, v116, v117
	v_cvt_pk_f16_f32 v116, v114, v115
	ds_write_b16 v238, v116 offset:5472
	ds_write_b16_d16_hi v239, v116 offset:5472
	ds_write_b16 v240, v117 offset:5472
	ds_write_b16_d16_hi v241, v117 offset:5472
	ds_read_b128 v[114:117], v151 offset:6880
	ds_read_b128 v[198:201], v151 offset:7488
	s_waitcnt lgkmcnt(1)
	v_mfma_f32_16x16x32_f16 v[186:189], v[42:45], v[114:117], v[186:189]
	v_mfma_f32_16x16x32_f16 v[202:205], v[58:61], v[114:117], v[202:205]
	s_waitcnt lgkmcnt(0)
	v_mfma_f32_16x16x32_f16 v[22:25], v[42:45], v[198:201], v[22:25]
	v_mfma_f32_16x16x32_f16 v[58:61], v[58:61], v[198:201], v[38:41]
	s_nop 2
	ds_read_b128 v[38:41], v151 offset:256
	ds_read_b128 v[42:45], v151 offset:864
	s_waitcnt lgkmcnt(1)
	v_mfma_f32_16x16x32_f16 v[130:133], v[34:37], v[38:41], v[130:133]
	v_mfma_f32_16x16x32_f16 v[198:201], v[14:17], v[38:41], v[214:217]
	s_waitcnt lgkmcnt(0)
	v_mfma_f32_16x16x32_f16 v[142:145], v[34:37], v[42:45], v[142:145]
	v_mfma_f32_16x16x32_f16 v[158:161], v[14:17], v[42:45], v[158:161]
	v_add_u32_e32 v38, 0xe1080, v150
	v_min_u32_e32 v38, v38, v157
	global_load_dwordx4 v[114:117], v38, s[8:9] nt
	s_waitcnt vmcnt(21)
	v_cvt_pk_f16_f32 v39, v112, v113
	v_cvt_pk_f16_f32 v38, v110, v111
	ds_write_b16 v234, v38 offset:6080
	ds_write_b16_d16_hi v235, v38 offset:6080
	ds_write_b16 v236, v39 offset:6080
	ds_write_b16_d16_hi v237, v39 offset:6080
	ds_read_b128 v[38:41], v151 offset:1472
	ds_read_b128 v[42:45], v151 offset:2080
	s_waitcnt lgkmcnt(1)
	v_mfma_f32_16x16x32_f16 v[214:217], v[34:37], v[38:41], v[218:221]
	v_mfma_f32_16x16x32_f16 v[178:181], v[14:17], v[38:41], v[178:181]
	s_waitcnt lgkmcnt(0)
	v_mfma_f32_16x16x32_f16 v[218:221], v[14:17], v[42:45], v[2:5]
	s_nop 2
	ds_read_b128 v[2:5], v151 offset:2688
	ds_read_b128 v[38:41], v151 offset:3296
	v_mfma_f32_16x16x32_f16 v[182:185], v[34:37], v[42:45], v[182:185]
	s_waitcnt lgkmcnt(1)
	v_mfma_f32_16x16x32_f16 v[134:137], v[34:37], v[2:5], v[134:137]
	v_mfma_f32_16x16x32_f16 v[146:149], v[14:17], v[2:5], v[146:149]
	s_waitcnt lgkmcnt(0)
	v_mfma_f32_16x16x32_f16 v[206:209], v[34:37], v[38:41], v[206:209]
	v_mfma_f32_16x16x32_f16 v[122:125], v[14:17], v[38:41], v[122:125]
	v_add_u32_e32 v2, 0xf76c0, v244
	v_min_u32_e32 v2, v2, v157
	global_load_dwordx4 v[110:113], v2, s[8:9] nt
	s_waitcnt vmcnt(21)
	v_cvt_pk_f16_f32 v3, v120, v121
	v_cvt_pk_f16_f32 v2, v118, v119
	ds_write_b16 v238, v2 offset:6688
	ds_write_b16_d16_hi v239, v2 offset:6688
	ds_write_b16 v240, v3 offset:6688
	ds_write_b16_d16_hi v241, v3 offset:6688
	ds_read_b128 v[2:5], v151 offset:3904
	ds_read_b128 v[38:41], v151 offset:4512
	s_waitcnt lgkmcnt(1)
	v_mfma_f32_16x16x32_f16 v[210:213], v[34:37], v[2:5], v[210:213]
	v_mfma_f32_16x16x32_f16 v[190:193], v[14:17], v[2:5], v[190:193]
	s_waitcnt lgkmcnt(0)
	v_mfma_f32_16x16x32_f16 v[166:169], v[34:37], v[38:41], v[166:169]
	v_mfma_f32_16x16x32_f16 v[162:165], v[14:17], v[38:41], v[162:165]
	ds_read_b128 v[2:5], v151 offset:5120
	ds_read_b128 v[38:41], v151 offset:5728
	s_waitcnt lgkmcnt(1)
	v_mfma_f32_16x16x32_f16 v[98:101], v[34:37], v[2:5], v[98:101]
	v_mfma_f32_16x16x32_f16 v[138:141], v[14:17], v[2:5], v[138:141]
	s_waitcnt lgkmcnt(0)
	v_mfma_f32_16x16x32_f16 v[170:173], v[34:37], v[38:41], v[170:173]
	v_mfma_f32_16x16x32_f16 v[126:129], v[14:17], v[38:41], v[126:129]
	v_add_u32_e32 v2, 0x10dd00, v150
	v_min_u32_e32 v2, v2, v157
	v_cndmask_b32_e64 v2, 0, v2, s[0:1]
	global_load_dwordx4 v[118:121], v2, s[8:9] nt
	s_waitcnt vmcnt(21)
	v_cvt_pk_f16_f32 v3, v72, v73
	v_cvt_pk_f16_f32 v2, v70, v71
	ds_write_b16 v234, v2 offset:7296
	ds_write_b16_d16_hi v235, v2 offset:7296
	ds_write_b16 v236, v3 offset:7296
	ds_write_b16_d16_hi v237, v3 offset:7296
	ds_read_b128 v[2:5], v151 offset:6336
	ds_read_b128 v[38:41], v151 offset:6944
	ds_read_b128 v[70:73], v151 offset:7552
	s_mov_b32 s3, 0x90000
	s_waitcnt lgkmcnt(0)
	v_mfma_f32_16x16x32_f16 v[174:177], v[34:37], v[2:5], v[174:177]
	s_barrier
	v_sub_u32_e32 v245, v234, v243
	v_add_u32_e32 v246, 0xfffffdc0, v245
	v_min_u32_e32 v245, v245, v246
	v_add_u32_e32 v234, v242, v245
	v_sub_u32_e32 v245, v235, v243
	v_add_u32_e32 v246, 0xfffffdc0, v245
	v_min_u32_e32 v245, v245, v246
	v_add_u32_e32 v235, v242, v245
	v_sub_u32_e32 v245, v236, v243
	v_add_u32_e32 v246, 0xfffffdc0, v245
	v_min_u32_e32 v245, v245, v246
	v_add_u32_e32 v236, v242, v245
	v_sub_u32_e32 v245, v237, v243
	v_add_u32_e32 v246, 0xfffffdc0, v245
	v_min_u32_e32 v245, v245, v246
	v_add_u32_e32 v237, v242, v245
	v_sub_u32_e32 v245, v238, v243
	v_add_u32_e32 v246, 0xfffffdc0, v245
	v_min_u32_e32 v245, v245, v246
	v_add_u32_e32 v238, v242, v245
	v_sub_u32_e32 v245, v239, v243
	v_add_u32_e32 v246, 0xfffffdc0, v245
	v_min_u32_e32 v245, v245, v246
	v_add_u32_e32 v239, v242, v245
	v_sub_u32_e32 v245, v240, v243
	v_add_u32_e32 v246, 0xfffffdc0, v245
	v_min_u32_e32 v245, v245, v246
	v_add_u32_e32 v240, v242, v245
	v_sub_u32_e32 v245, v241, v243
	v_add_u32_e32 v246, 0xfffffdc0, v245
	v_min_u32_e32 v245, v245, v246
	v_add_u32_e32 v241, v242, v245
	v_mfma_f32_16x16x32_f16 v[194:197], v[14:17], v[2:5], v[194:197]
	v_add_co_u32_e32 v2, vcc, s3, v152
	s_mov_b32 s3, 0x94000
	s_nop 0
	v_addc_co_u32_e32 v3, vcc, 0, v153, vcc
	v_mfma_f32_16x16x32_f16 v[186:189], v[34:37], v[38:41], v[186:189]
	v_mfma_f32_16x16x32_f16 v[202:205], v[14:17], v[38:41], v[202:205]
	global_load_dwordx4 v[38:41], v[2:3], off sc1
	global_load_dwordx4 v[42:45], v[2:3], off offset:256 sc1
	v_add_co_u32_e32 v2, vcc, s3, v152
	v_mfma_f32_16x16x32_f16 v[34:37], v[34:37], v[70:73], v[22:25]
	s_nop 0
	v_addc_co_u32_e32 v3, vcc, 0, v153, vcc
	s_nop 0
	global_load_dwordx4 v[22:25], v[2:3], off sc1
	s_nop 0
	global_load_dwordx4 v[2:5], v[2:3], off offset:256 sc1
	v_mfma_f32_16x16x32_f16 v[14:17], v[14:17], v[70:73], v[58:61]
	v_add_u32_e32 v157, 0x111528dc, v154
	s_nop 1
	ds_read_b128 v[58:61], v151 offset:320
	v_add_u32_e32 v70, 0x1400, v150
	s_waitcnt vmcnt(24) lgkmcnt(0)
	v_mfma_f32_16x16x32_f16 v[130:133], v[46:49], v[58:61], v[130:133]
	s_waitcnt vmcnt(23)
	v_mfma_f32_16x16x32_f16 v[198:201], v[54:57], v[58:61], v[198:201]
	v_min_u32_e32 v58, v70, v157
	global_load_dwordx4 v[58:61], v58, s[8:9] nt
	s_waitcnt vmcnt(21)
	v_cvt_pk_f16_f32 v71, v76, v77
	v_cvt_pk_f16_f32 v70, v74, v75
	ds_write_b16 v234, v70 offset:0
	ds_write_b16_d16_hi v235, v70 offset:0
	ds_write_b16 v236, v71 offset:0
	ds_write_b16_d16_hi v237, v71 offset:0
	ds_read_b128 v[70:73], v151 offset:928
	ds_read_b128 v[74:77], v151 offset:1536
	s_waitcnt lgkmcnt(1)
	v_mfma_f32_16x16x32_f16 v[142:145], v[46:49], v[70:73], v[142:145]
	v_mfma_f32_16x16x32_f16 v[158:161], v[54:57], v[70:73], v[158:161]
	s_waitcnt lgkmcnt(0)
	v_mfma_f32_16x16x32_f16 v[214:217], v[46:49], v[74:77], v[214:217]
	v_mfma_f32_16x16x32_f16 v[178:181], v[54:57], v[74:77], v[178:181]
	ds_read_b128 v[70:73], v151 offset:2144
	ds_read_b128 v[74:77], v151 offset:2752
	s_waitcnt lgkmcnt(1)
	v_mfma_f32_16x16x32_f16 v[182:185], v[46:49], v[70:73], v[182:185]
	v_mfma_f32_16x16x32_f16 v[218:221], v[54:57], v[70:73], v[218:221]
	s_waitcnt lgkmcnt(0)
	v_mfma_f32_16x16x32_f16 v[134:137], v[46:49], v[74:77], v[134:137]
	v_mfma_f32_16x16x32_f16 v[146:149], v[54:57], v[74:77], v[146:149]
	v_add_u32_e32 v70, 0x17a40, v244
	v_min_u32_e32 v70, v70, v157
	global_load_dwordx4 v[70:73], v70, s[8:9] nt
	s_waitcnt vmcnt(21)
	v_cvt_pk_f16_f32 v75, v80, v81
	v_cvt_pk_f16_f32 v74, v78, v79
	ds_write_b16 v238, v74 offset:608
	ds_write_b16_d16_hi v239, v74 offset:608
	ds_write_b16 v240, v75 offset:608
	ds_write_b16_d16_hi v241, v75 offset:608
	ds_read_b128 v[74:77], v151 offset:3360
	ds_read_b128 v[78:81], v151 offset:5184
	s_waitcnt lgkmcnt(1)
	v_mfma_f32_16x16x32_f16 v[206:209], v[46:49], v[74:77], v[206:209]
	v_mfma_f32_16x16x32_f16 v[122:125], v[54:57], v[74:77], v[122:125]
	ds_read_b128 v[74:77], v151 offset:3968
	ds_read_b128 v[222:225], v151 offset:4576
	s_waitcnt lgkmcnt(1)
	v_mfma_f32_16x16x32_f16 v[210:213], v[46:49], v[74:77], v[210:213]
	v_mfma_f32_16x16x32_f16 v[190:193], v[54:57], v[74:77], v[190:193]
	s_waitcnt lgkmcnt(0)
	v_mfma_f32_16x16x32_f16 v[166:169], v[46:49], v[222:225], v[166:169]
	v_mfma_f32_16x16x32_f16 v[162:165], v[54:57], v[222:225], v[162:165]
	v_mfma_f32_16x16x32_f16 v[98:101], v[46:49], v[78:81], v[98:101]
	v_mfma_f32_16x16x32_f16 v[138:141], v[54:57], v[78:81], v[138:141]
	v_add_u32_e32 v74, 0x2e080, v150
	v_min_u32_e32 v74, v74, v157
	global_load_dwordx4 v[74:77], v74, s[8:9] nt
	s_waitcnt vmcnt(21)
	v_cvt_pk_f16_f32 v79, v84, v85
	v_cvt_pk_f16_f32 v78, v82, v83
	ds_write_b16 v234, v78 offset:1216
	ds_write_b16_d16_hi v235, v78 offset:1216
	ds_write_b16 v236, v79 offset:1216
	ds_write_b16_d16_hi v237, v79 offset:1216
	ds_read_b128 v[78:81], v151 offset:5792
	ds_read_b128 v[82:85], v151 offset:6400
	s_waitcnt lgkmcnt(1)
	v_mfma_f32_16x16x32_f16 v[170:173], v[46:49], v[78:81], v[170:173]
	v_mfma_f32_16x16x32_f16 v[126:129], v[54:57], v[78:81], v[126:129]
	s_waitcnt lgkmcnt(0)
	v_mfma_f32_16x16x32_f16 v[174:177], v[46:49], v[82:85], v[174:177]
	v_mfma_f32_16x16x32_f16 v[194:197], v[54:57], v[82:85], v[194:197]
	ds_read_b128 v[78:81], v151 offset:7008
	ds_read_b128 v[82:85], v151 offset:7616
	s_waitcnt lgkmcnt(1)
	v_mfma_f32_16x16x32_f16 v[186:189], v[46:49], v[78:81], v[186:189]
	v_mfma_f32_16x16x32_f16 v[202:205], v[54:57], v[78:81], v[202:205]
	s_waitcnt lgkmcnt(0)
	v_mfma_f32_16x16x32_f16 v[34:37], v[46:49], v[82:85], v[34:37]
	v_mfma_f32_16x16x32_f16 v[46:49], v[54:57], v[82:85], v[14:17]
	s_nop 2
	v_add_u32_e32 v14, 0x446c0, v244
	v_min_u32_e32 v14, v14, v157
	global_load_dwordx4 v[78:81], v14, s[8:9] nt
	s_waitcnt vmcnt(21)
	v_cvt_pk_f16_f32 v15, v52, v53
	v_cvt_pk_f16_f32 v14, v50, v51
	ds_write_b16 v238, v14 offset:1824
	ds_write_b16_d16_hi v239, v14 offset:1824
	ds_write_b16 v240, v15 offset:1824
	ds_write_b16_d16_hi v241, v15 offset:1824
	ds_read_b128 v[14:17], v151 offset:384
	ds_read_b128 v[50:53], v151 offset:992
	s_waitcnt lgkmcnt(1)
	v_mfma_f32_16x16x32_f16 v[130:133], v[26:29], v[14:17], v[130:133]
	v_mfma_f32_16x16x32_f16 v[198:201], v[10:13], v[14:17], v[198:201]
	s_waitcnt lgkmcnt(0)
	v_mfma_f32_16x16x32_f16 v[142:145], v[26:29], v[50:53], v[142:145]
	v_mfma_f32_16x16x32_f16 v[158:161], v[10:13], v[50:53], v[158:161]
	ds_read_b128 v[14:17], v151 offset:1600
	ds_read_b128 v[50:53], v151 offset:2208
	s_waitcnt lgkmcnt(1)
	v_mfma_f32_16x16x32_f16 v[214:217], v[26:29], v[14:17], v[214:217]
	v_mfma_f32_16x16x32_f16 v[178:181], v[10:13], v[14:17], v[178:181]
	s_waitcnt lgkmcnt(0)
	v_mfma_f32_16x16x32_f16 v[182:185], v[26:29], v[50:53], v[182:185]
	v_mfma_f32_16x16x32_f16 v[218:221], v[10:13], v[50:53], v[218:221]
	v_add_u32_e32 v14, 0x5ad00, v150
	v_min_u32_e32 v14, v14, v157
	global_load_dwordx4 v[82:85], v14, s[8:9] nt
	s_waitcnt vmcnt(21)
	v_cvt_pk_f16_f32 v15, v88, v89
	v_cvt_pk_f16_f32 v14, v86, v87
	ds_write_b16 v234, v14 offset:2432
	ds_write_b16_d16_hi v235, v14 offset:2432
	ds_write_b16 v236, v15 offset:2432
	ds_write_b16_d16_hi v237, v15 offset:2432
	ds_read_b128 v[14:17], v151 offset:2816
	ds_read_b128 v[50:53], v151 offset:3424
	s_waitcnt lgkmcnt(1)
	v_mfma_f32_16x16x32_f16 v[134:137], v[26:29], v[14:17], v[134:137]
	v_mfma_f32_16x16x32_f16 v[146:149], v[10:13], v[14:17], v[146:149]
	s_waitcnt lgkmcnt(0)
	v_mfma_f32_16x16x32_f16 v[206:209], v[26:29], v[50:53], v[206:209]
	v_mfma_f32_16x16x32_f16 v[122:125], v[10:13], v[50:53], v[122:125]
	ds_read_b128 v[14:17], v151 offset:4032
	ds_read_b128 v[50:53], v151 offset:4640
	s_waitcnt lgkmcnt(1)
	v_mfma_f32_16x16x32_f16 v[210:213], v[26:29], v[14:17], v[210:213]
	v_mfma_f32_16x16x32_f16 v[190:193], v[10:13], v[14:17], v[190:193]
	s_waitcnt lgkmcnt(0)
	v_mfma_f32_16x16x32_f16 v[166:169], v[26:29], v[50:53], v[166:169]
	v_mfma_f32_16x16x32_f16 v[162:165], v[10:13], v[50:53], v[162:165]
	v_add_u32_e32 v14, 0x71340, v244
	v_min_u32_e32 v14, v14, v157
	global_load_dwordx4 v[86:89], v14, s[8:9] nt
	s_waitcnt vmcnt(21)
	v_cvt_pk_f16_f32 v15, v92, v93
	v_cvt_pk_f16_f32 v14, v90, v91
	ds_write_b16 v238, v14 offset:3040
	ds_write_b16_d16_hi v239, v14 offset:3040
	ds_write_b16 v240, v15 offset:3040
	ds_write_b16_d16_hi v241, v15 offset:3040
	ds_read_b128 v[14:17], v151 offset:5248
	ds_read_b128 v[50:53], v151 offset:5856
	s_waitcnt lgkmcnt(1)
	v_mfma_f32_16x16x32_f16 v[222:225], v[26:29], v[14:17], v[98:101]
	v_mfma_f32_16x16x32_f16 v[138:141], v[10:13], v[14:17], v[138:141]
	s_waitcnt lgkmcnt(0)
	v_mfma_f32_16x16x32_f16 v[170:173], v[26:29], v[50:53], v[170:173]
	v_mfma_f32_16x16x32_f16 v[126:129], v[10:13], v[50:53], v[126:129]
	ds_read_b128 v[14:17], v151 offset:6464
	ds_read_b128 v[50:53], v151 offset:7072
	s_waitcnt lgkmcnt(1)
	v_mfma_f32_16x16x32_f16 v[174:177], v[26:29], v[14:17], v[174:177]
	v_mfma_f32_16x16x32_f16 v[194:197], v[10:13], v[14:17], v[194:197]
	s_waitcnt lgkmcnt(0)
	v_mfma_f32_16x16x32_f16 v[186:189], v[26:29], v[50:53], v[186:189]
	v_mfma_f32_16x16x32_f16 v[202:205], v[10:13], v[50:53], v[202:205]
	v_add_u32_e32 v14, 0x87980, v150
	v_min_u32_e32 v14, v14, v157
	global_load_dwordx4 v[90:93], v14, s[8:9] nt
	s_waitcnt vmcnt(21)
	v_cvt_pk_f16_f32 v15, v96, v97
	v_cvt_pk_f16_f32 v14, v94, v95
	ds_write_b16 v234, v14 offset:3648
	ds_write_b16_d16_hi v235, v14 offset:3648
	ds_write_b16 v236, v15 offset:3648
	ds_write_b16_d16_hi v237, v15 offset:3648
	ds_read_b128 v[94:97], v151 offset:7680
	s_mov_b32 s3, 0x98000
	v_add_co_u32_e32 v14, vcc, s3, v152
	s_mov_b32 s3, 0x9c000
	s_nop 0
	v_addc_co_u32_e32 v15, vcc, 0, v153, vcc
	global_load_dwordx4 v[50:53], v[14:15], off sc1
	global_load_dwordx4 v[54:57], v[14:15], off offset:256 sc1
	v_add_co_u32_e32 v14, vcc, s3, v152
	s_waitcnt lgkmcnt(0)
	v_mfma_f32_16x16x32_f16 v[34:37], v[26:29], v[94:97], v[34:37]
	v_addc_co_u32_e32 v15, vcc, 0, v153, vcc
	global_load_dwordx4 v[26:29], v[14:15], off sc1
	s_nop 0
	global_load_dwordx4 v[14:17], v[14:15], off offset:256 sc1
	v_mfma_f32_16x16x32_f16 v[10:13], v[10:13], v[94:97], v[46:49]
	s_nop 2
	ds_read_b128 v[46:49], v151 offset:448
	ds_read_b128 v[94:97], v151 offset:1056
	s_waitcnt vmcnt(24) lgkmcnt(1)
	v_mfma_f32_16x16x32_f16 v[130:133], v[62:65], v[46:49], v[130:133]
	s_waitcnt lgkmcnt(0)
	v_mfma_f32_16x16x32_f16 v[142:145], v[62:65], v[94:97], v[142:145]
	s_waitcnt vmcnt(23)
	v_mfma_f32_16x16x32_f16 v[158:161], v[66:69], v[94:97], v[158:161]
	ds_read_b128 v[94:97], v151 offset:1664
	v_mfma_f32_16x16x32_f16 v[46:49], v[66:69], v[46:49], v[198:201]
	s_waitcnt lgkmcnt(0)
	v_mfma_f32_16x16x32_f16 v[198:201], v[62:65], v[94:97], v[214:217]
	v_mfma_f32_16x16x32_f16 v[178:181], v[66:69], v[94:97], v[178:181]
	v_add_u32_e32 v94, 0x9dfc0, v244
	v_min_u32_e32 v94, v94, v157
	global_load_dwordx4 v[94:97], v94, s[8:9] nt
	s_waitcnt vmcnt(21)
	v_cvt_pk_f16_f32 v9, v8, v9
	v_cvt_pk_f16_f32 v8, v6, v7
	ds_write_b16 v238, v8 offset:4256
	ds_write_b16_d16_hi v239, v8 offset:4256
	ds_write_b16 v240, v9 offset:4256
	ds_write_b16_d16_hi v241, v9 offset:4256
	ds_read_b128 v[6:9], v151 offset:2272
	ds_read_b128 v[98:101], v151 offset:2880
	s_waitcnt lgkmcnt(1)
	v_mfma_f32_16x16x32_f16 v[182:185], v[62:65], v[6:9], v[182:185]
	s_waitcnt lgkmcnt(0)
	v_mfma_f32_16x16x32_f16 v[134:137], v[62:65], v[98:101], v[134:137]
	v_mfma_f32_16x16x32_f16 v[146:149], v[66:69], v[98:101], v[146:149]
	ds_read_b128 v[98:101], v151 offset:3488
	ds_read_b128 v[214:217], v151 offset:4096
	v_mfma_f32_16x16x32_f16 v[6:9], v[66:69], v[6:9], v[218:221]
	s_waitcnt lgkmcnt(1)
	v_mfma_f32_16x16x32_f16 v[206:209], v[62:65], v[98:101], v[206:209]
	v_mfma_f32_16x16x32_f16 v[122:125], v[66:69], v[98:101], v[122:125]
	s_waitcnt lgkmcnt(0)
	v_mfma_f32_16x16x32_f16 v[210:213], v[62:65], v[214:217], v[210:213]
	v_mfma_f32_16x16x32_f16 v[190:193], v[66:69], v[214:217], v[190:193]
	v_add_u32_e32 v98, 0xb4600, v150
	v_min_u32_e32 v98, v98, v157
	global_load_dwordx4 v[98:101], v98, s[8:9] nt
	s_waitcnt vmcnt(21)
	v_cvt_pk_f16_f32 v105, v104, v105
	v_cvt_pk_f16_f32 v104, v102, v103
	ds_write_b16 v234, v104 offset:4864
	ds_write_b16_d16_hi v235, v104 offset:4864
	ds_write_b16 v236, v105 offset:4864
	ds_write_b16_d16_hi v237, v105 offset:4864
	ds_read_b128 v[102:105], v151 offset:4704
	ds_read_b128 v[214:217], v151 offset:6528
	s_waitcnt lgkmcnt(1)
	v_mfma_f32_16x16x32_f16 v[166:169], v[62:65], v[102:105], v[166:169]
	v_mfma_f32_16x16x32_f16 v[162:165], v[66:69], v[102:105], v[162:165]
	ds_read_b128 v[102:105], v151 offset:5312
	ds_read_b128 v[218:221], v151 offset:5920
	s_waitcnt lgkmcnt(1)
	v_mfma_f32_16x16x32_f16 v[222:225], v[62:65], v[102:105], v[222:225]
	v_mfma_f32_16x16x32_f16 v[138:141], v[66:69], v[102:105], v[138:141]
	s_waitcnt lgkmcnt(0)
	v_mfma_f32_16x16x32_f16 v[170:173], v[62:65], v[218:221], v[170:173]
	v_mfma_f32_16x16x32_f16 v[126:129], v[66:69], v[218:221], v[126:129]
	v_mfma_f32_16x16x32_f16 v[174:177], v[62:65], v[214:217], v[174:177]
	v_mfma_f32_16x16x32_f16 v[194:197], v[66:69], v[214:217], v[194:197]
	v_add_u32_e32 v102, 0xcac40, v244
	v_min_u32_e32 v102, v102, v157
	global_load_dwordx4 v[102:105], v102, s[8:9] nt
	s_waitcnt vmcnt(21)
	v_cvt_pk_f16_f32 v109, v108, v109
	v_cvt_pk_f16_f32 v108, v106, v107
	ds_write_b16 v238, v108 offset:5472
	ds_write_b16_d16_hi v239, v108 offset:5472
	ds_write_b16 v240, v109 offset:5472
	ds_write_b16_d16_hi v241, v109 offset:5472
	ds_read_b128 v[106:109], v151 offset:7136
	ds_read_b128 v[214:217], v151 offset:7744
	s_waitcnt lgkmcnt(1)
	v_mfma_f32_16x16x32_f16 v[186:189], v[62:65], v[106:109], v[186:189]
	s_waitcnt lgkmcnt(0)
	v_mfma_f32_16x16x32_f16 v[218:221], v[62:65], v[214:217], v[34:37]
	v_mfma_f32_16x16x32_f16 v[214:217], v[66:69], v[214:217], v[10:13]
	s_nop 2
	ds_read_b128 v[10:13], v151 offset:512
	ds_read_b128 v[34:37], v151 offset:1120
	v_mfma_f32_16x16x32_f16 v[202:205], v[66:69], v[106:109], v[202:205]
	s_waitcnt lgkmcnt(1)
	v_mfma_f32_16x16x32_f16 v[130:133], v[30:33], v[10:13], v[130:133]
	v_mfma_f32_16x16x32_f16 v[226:229], v[18:21], v[10:13], v[46:49]
	s_waitcnt lgkmcnt(0)
	v_mfma_f32_16x16x32_f16 v[142:145], v[30:33], v[34:37], v[142:145]
	v_mfma_f32_16x16x32_f16 v[158:161], v[18:21], v[34:37], v[158:161]
	v_add_u32_e32 v10, 0xe1280, v150
	v_min_u32_e32 v10, v10, v157
	global_load_dwordx4 v[62:65], v10, s[8:9] nt
	s_waitcnt vmcnt(21)
	v_cvt_pk_f16_f32 v11, v116, v117
	v_cvt_pk_f16_f32 v10, v114, v115
	ds_write_b16 v234, v10 offset:6080
	ds_write_b16_d16_hi v235, v10 offset:6080
	ds_write_b16 v236, v11 offset:6080
	ds_write_b16_d16_hi v237, v11 offset:6080
	ds_read_b128 v[10:13], v151 offset:1728
	ds_read_b128 v[34:37], v151 offset:2336
	s_waitcnt lgkmcnt(1)
	v_mfma_f32_16x16x32_f16 v[114:117], v[30:33], v[10:13], v[198:201]
	v_mfma_f32_16x16x32_f16 v[178:181], v[18:21], v[10:13], v[178:181]
	s_waitcnt lgkmcnt(0)
	v_mfma_f32_16x16x32_f16 v[198:201], v[18:21], v[34:37], v[6:9]
	s_nop 2
	ds_read_b128 v[6:9], v151 offset:2944
	ds_read_b128 v[10:13], v151 offset:3552
	v_mfma_f32_16x16x32_f16 v[182:185], v[30:33], v[34:37], v[182:185]
	s_waitcnt lgkmcnt(1)
	v_mfma_f32_16x16x32_f16 v[134:137], v[30:33], v[6:9], v[134:137]
	v_mfma_f32_16x16x32_f16 v[146:149], v[18:21], v[6:9], v[146:149]
	s_waitcnt lgkmcnt(0)
	v_mfma_f32_16x16x32_f16 v[206:209], v[30:33], v[10:13], v[206:209]
	v_mfma_f32_16x16x32_f16 v[122:125], v[18:21], v[10:13], v[122:125]
	v_add_u32_e32 v6, 0xf78c0, v244
	v_min_u32_e32 v6, v6, v157
	global_load_dwordx4 v[66:69], v6, s[8:9] nt
	s_waitcnt vmcnt(21)
	v_cvt_pk_f16_f32 v7, v112, v113
	v_cvt_pk_f16_f32 v6, v110, v111
	ds_write_b16 v238, v6 offset:6688
	ds_write_b16_d16_hi v239, v6 offset:6688
	ds_write_b16 v240, v7 offset:6688
	ds_write_b16_d16_hi v241, v7 offset:6688
	ds_read_b128 v[6:9], v151 offset:4160
	ds_read_b128 v[10:13], v151 offset:4768
	s_waitcnt lgkmcnt(1)
	v_mfma_f32_16x16x32_f16 v[210:213], v[30:33], v[6:9], v[210:213]
	v_mfma_f32_16x16x32_f16 v[190:193], v[18:21], v[6:9], v[190:193]
	s_waitcnt lgkmcnt(0)
	v_mfma_f32_16x16x32_f16 v[166:169], v[30:33], v[10:13], v[166:169]
	v_mfma_f32_16x16x32_f16 v[162:165], v[18:21], v[10:13], v[162:165]
	ds_read_b128 v[6:9], v151 offset:5376
	ds_read_b128 v[10:13], v151 offset:5984
	s_waitcnt lgkmcnt(1)
	v_mfma_f32_16x16x32_f16 v[222:225], v[30:33], v[6:9], v[222:225]
	v_mfma_f32_16x16x32_f16 v[138:141], v[18:21], v[6:9], v[138:141]
	s_waitcnt lgkmcnt(0)
	v_mfma_f32_16x16x32_f16 v[170:173], v[30:33], v[10:13], v[170:173]
	v_mfma_f32_16x16x32_f16 v[126:129], v[18:21], v[10:13], v[126:129]
	v_add_u32_e32 v6, 0x10df00, v150
	v_min_u32_e32 v6, v6, v157
	v_cndmask_b32_e64 v6, 0, v6, s[0:1]
	global_load_dwordx4 v[106:109], v6, s[8:9] nt
	s_waitcnt vmcnt(21)
	v_cvt_pk_f16_f32 v7, v120, v121
	v_cvt_pk_f16_f32 v6, v118, v119
	ds_write_b16 v234, v6 offset:7296
	ds_write_b16_d16_hi v235, v6 offset:7296
	ds_write_b16 v236, v7 offset:7296
	ds_write_b16_d16_hi v237, v7 offset:7296
	ds_read_b128 v[6:9], v151 offset:6592
	ds_read_b128 v[10:13], v151 offset:7200
	s_mov_b32 s3, 0xa0000
	ds_read_b128 v[110:113], v151 offset:7808
	s_waitcnt lgkmcnt(0)
	v_mfma_f32_16x16x32_f16 v[118:121], v[30:33], v[6:9], v[174:177]
	s_barrier
	v_sub_u32_e32 v245, v234, v243
	v_add_u32_e32 v246, 0xfffffdc0, v245
	v_min_u32_e32 v245, v245, v246
	v_add_u32_e32 v234, v242, v245
	v_sub_u32_e32 v245, v235, v243
	v_add_u32_e32 v246, 0xfffffdc0, v245
	v_min_u32_e32 v245, v245, v246
	v_add_u32_e32 v235, v242, v245
	v_sub_u32_e32 v245, v236, v243
	v_add_u32_e32 v246, 0xfffffdc0, v245
	v_min_u32_e32 v245, v245, v246
	v_add_u32_e32 v236, v242, v245
	v_sub_u32_e32 v245, v237, v243
	v_add_u32_e32 v246, 0xfffffdc0, v245
	v_min_u32_e32 v245, v245, v246
	v_add_u32_e32 v237, v242, v245
	v_sub_u32_e32 v245, v238, v243
	v_add_u32_e32 v246, 0xfffffdc0, v245
	v_min_u32_e32 v245, v245, v246
	v_add_u32_e32 v238, v242, v245
	v_sub_u32_e32 v245, v239, v243
	v_add_u32_e32 v246, 0xfffffdc0, v245
	v_min_u32_e32 v245, v245, v246
	v_add_u32_e32 v239, v242, v245
	v_sub_u32_e32 v245, v240, v243
	v_add_u32_e32 v246, 0xfffffdc0, v245
	v_min_u32_e32 v245, v245, v246
	v_add_u32_e32 v240, v242, v245
	v_sub_u32_e32 v245, v241, v243
	v_add_u32_e32 v246, 0xfffffdc0, v245
	v_min_u32_e32 v245, v245, v246
	v_add_u32_e32 v241, v242, v245
	v_mfma_f32_16x16x32_f16 v[174:177], v[18:21], v[6:9], v[194:197]
	v_add_co_u32_e32 v6, vcc, s3, v152
	s_mov_b32 s3, 0xa4000
	s_nop 0
	v_addc_co_u32_e32 v7, vcc, 0, v153, vcc
	global_load_dwordx4 v[34:37], v[6:7], off sc1
	global_load_dwordx4 v[46:49], v[6:7], off offset:256 sc1
	v_add_co_u32_e32 v6, vcc, s3, v152
	v_mfma_f32_16x16x32_f16 v[186:189], v[30:33], v[10:13], v[186:189]
	s_nop 0
	v_addc_co_u32_e32 v7, vcc, 0, v153, vcc
	v_mfma_f32_16x16x32_f16 v[194:197], v[18:21], v[10:13], v[202:205]
	global_load_dwordx4 v[10:13], v[6:7], off sc1
	s_nop 0
	global_load_dwordx4 v[6:9], v[6:7], off offset:256 sc1
	v_mfma_f32_16x16x32_f16 v[30:33], v[30:33], v[110:113], v[218:221]
	v_mfma_f32_16x16x32_f16 v[18:21], v[18:21], v[110:113], v[214:217]
	v_min_u32_e32 v110, 0x54, v154
	v_add_u32_e32 v154, 0x11152adc, v110
	ds_read_b128 v[110:113], v151 offset:0
	v_add_u32_e32 v157, 0x1600, v250
	s_waitcnt vmcnt(24) lgkmcnt(0)
	v_mfma_f32_16x16x32_f16 v[130:133], v[38:41], v[110:113], v[130:133]
	s_waitcnt vmcnt(23)
	v_mfma_f32_16x16x32_f16 v[202:205], v[42:45], v[110:113], v[226:229]
	v_min_u32_e32 v110, v157, v154
	global_load_dwordx4 v[110:113], v110, s[8:9] nt
	s_waitcnt vmcnt(21)
	v_cvt_pk_f16_f32 v61, v60, v61
	v_cvt_pk_f16_f32 v60, v58, v59
	ds_write_b16 v234, v60 offset:0
	ds_write_b16_d16_hi v235, v60 offset:0
	ds_write_b16 v236, v61 offset:0
	ds_write_b16_d16_hi v237, v61 offset:0
	ds_read_b128 v[58:61], v151 offset:608
	ds_read_b128 v[214:217], v151 offset:1216
	s_waitcnt lgkmcnt(1)
	v_mfma_f32_16x16x32_f16 v[142:145], v[38:41], v[58:61], v[142:145]
	v_mfma_f32_16x16x32_f16 v[158:161], v[42:45], v[58:61], v[158:161]
	s_waitcnt lgkmcnt(0)
	v_mfma_f32_16x16x32_f16 v[114:117], v[38:41], v[214:217], v[114:117]
	v_mfma_f32_16x16x32_f16 v[178:181], v[42:45], v[214:217], v[178:181]
	ds_read_b128 v[58:61], v151 offset:1824
	ds_read_b128 v[214:217], v151 offset:2432
	s_waitcnt lgkmcnt(1)
	v_mfma_f32_16x16x32_f16 v[182:185], v[38:41], v[58:61], v[182:185]
	v_mfma_f32_16x16x32_f16 v[198:201], v[42:45], v[58:61], v[198:201]
	s_waitcnt lgkmcnt(0)
	v_mfma_f32_16x16x32_f16 v[134:137], v[38:41], v[214:217], v[134:137]
	v_mfma_f32_16x16x32_f16 v[146:149], v[42:45], v[214:217], v[146:149]
	v_add_u32_e32 v58, 0x17c40, v251
	v_min_u32_e32 v58, v58, v154
	global_load_dwordx4 v[58:61], v58, s[8:9] nt
	s_waitcnt vmcnt(21)
	v_cvt_pk_f16_f32 v73, v72, v73
	v_cvt_pk_f16_f32 v72, v70, v71
	ds_write_b16 v238, v72 offset:608
	ds_write_b16_d16_hi v239, v72 offset:608
	ds_write_b16 v240, v73 offset:608
	ds_write_b16_d16_hi v241, v73 offset:608
	ds_read_b128 v[70:73], v151 offset:3040
	ds_read_b128 v[214:217], v151 offset:4864
	s_waitcnt lgkmcnt(1)
	v_mfma_f32_16x16x32_f16 v[206:209], v[38:41], v[70:73], v[206:209]
	v_mfma_f32_16x16x32_f16 v[122:125], v[42:45], v[70:73], v[122:125]
	ds_read_b128 v[70:73], v151 offset:3648
	ds_read_b128 v[218:221], v151 offset:4256
	s_waitcnt lgkmcnt(1)
	v_mfma_f32_16x16x32_f16 v[210:213], v[38:41], v[70:73], v[210:213]
	v_mfma_f32_16x16x32_f16 v[190:193], v[42:45], v[70:73], v[190:193]
	s_waitcnt lgkmcnt(0)
	v_mfma_f32_16x16x32_f16 v[166:169], v[38:41], v[218:221], v[166:169]
	v_mfma_f32_16x16x32_f16 v[162:165], v[42:45], v[218:221], v[162:165]
	v_mfma_f32_16x16x32_f16 v[218:221], v[38:41], v[214:217], v[222:225]
	v_mfma_f32_16x16x32_f16 v[138:141], v[42:45], v[214:217], v[138:141]
	v_add_u32_e32 v70, 0x2e280, v250
	v_min_u32_e32 v70, v70, v154
	global_load_dwordx4 v[70:73], v70, s[8:9] nt
	s_waitcnt vmcnt(21)
	v_cvt_pk_f16_f32 v77, v76, v77
	v_cvt_pk_f16_f32 v76, v74, v75
	ds_write_b16 v234, v76 offset:1216
	ds_write_b16_d16_hi v235, v76 offset:1216
	ds_write_b16 v236, v77 offset:1216
	ds_write_b16_d16_hi v237, v77 offset:1216
	ds_read_b128 v[74:77], v151 offset:5472
	ds_read_b128 v[214:217], v151 offset:6080
	s_waitcnt lgkmcnt(1)
	v_mfma_f32_16x16x32_f16 v[170:173], v[38:41], v[74:77], v[170:173]
	v_mfma_f32_16x16x32_f16 v[126:129], v[42:45], v[74:77], v[126:129]
	s_waitcnt lgkmcnt(0)
	v_mfma_f32_16x16x32_f16 v[118:121], v[38:41], v[214:217], v[118:121]
	v_mfma_f32_16x16x32_f16 v[174:177], v[42:45], v[214:217], v[174:177]
	ds_read_b128 v[74:77], v151 offset:6688
	ds_read_b128 v[214:217], v151 offset:7296
	s_waitcnt lgkmcnt(1)
	v_mfma_f32_16x16x32_f16 v[186:189], v[38:41], v[74:77], v[186:189]
	v_mfma_f32_16x16x32_f16 v[194:197], v[42:45], v[74:77], v[194:197]
	s_waitcnt lgkmcnt(0)
	v_mfma_f32_16x16x32_f16 v[30:33], v[38:41], v[214:217], v[30:33]
	v_mfma_f32_16x16x32_f16 v[214:217], v[42:45], v[214:217], v[18:21]
	s_nop 2
	v_add_u32_e32 v18, 0x448c0, v251
	v_min_u32_e32 v18, v18, v154
	global_load_dwordx4 v[42:45], v18, s[8:9] nt
	s_waitcnt vmcnt(21)
	v_cvt_pk_f16_f32 v19, v80, v81
	v_cvt_pk_f16_f32 v18, v78, v79
	ds_write_b16 v238, v18 offset:1824
	ds_write_b16_d16_hi v239, v18 offset:1824
	ds_write_b16 v240, v19 offset:1824
	ds_write_b16_d16_hi v241, v19 offset:1824
	ds_read_b128 v[18:21], v151 offset:64
	ds_read_b128 v[38:41], v151 offset:672
	s_waitcnt lgkmcnt(1)
	v_mfma_f32_16x16x32_f16 v[130:133], v[22:25], v[18:21], v[130:133]
	v_mfma_f32_16x16x32_f16 v[202:205], v[2:5], v[18:21], v[202:205]
	s_waitcnt lgkmcnt(0)
	v_mfma_f32_16x16x32_f16 v[142:145], v[22:25], v[38:41], v[142:145]
	v_mfma_f32_16x16x32_f16 v[158:161], v[2:5], v[38:41], v[158:161]
	ds_read_b128 v[18:21], v151 offset:1280
	ds_read_b128 v[38:41], v151 offset:1888
	s_waitcnt lgkmcnt(1)
	v_mfma_f32_16x16x32_f16 v[114:117], v[22:25], v[18:21], v[114:117]
	v_mfma_f32_16x16x32_f16 v[178:181], v[2:5], v[18:21], v[178:181]
	s_waitcnt lgkmcnt(0)
	v_mfma_f32_16x16x32_f16 v[182:185], v[22:25], v[38:41], v[182:185]
	v_mfma_f32_16x16x32_f16 v[198:201], v[2:5], v[38:41], v[198:201]
	v_add_u32_e32 v18, 0x5af00, v250
	v_min_u32_e32 v18, v18, v154
	global_load_dwordx4 v[74:77], v18, s[8:9] nt
	s_waitcnt vmcnt(21)
	v_cvt_pk_f16_f32 v19, v84, v85
	v_cvt_pk_f16_f32 v18, v82, v83
	ds_write_b16 v234, v18 offset:2432
	ds_write_b16_d16_hi v235, v18 offset:2432
	ds_write_b16 v236, v19 offset:2432
	ds_write_b16_d16_hi v237, v19 offset:2432
	ds_read_b128 v[18:21], v151 offset:2496
	ds_read_b128 v[38:41], v151 offset:3104
	s_waitcnt lgkmcnt(1)
	v_mfma_f32_16x16x32_f16 v[134:137], v[22:25], v[18:21], v[134:137]
	v_mfma_f32_16x16x32_f16 v[146:149], v[2:5], v[18:21], v[146:149]
	s_waitcnt lgkmcnt(0)
	v_mfma_f32_16x16x32_f16 v[206:209], v[22:25], v[38:41], v[206:209]
	v_mfma_f32_16x16x32_f16 v[122:125], v[2:5], v[38:41], v[122:125]
	ds_read_b128 v[18:21], v151 offset:3712
	ds_read_b128 v[38:41], v151 offset:4320
	s_waitcnt lgkmcnt(1)
	v_mfma_f32_16x16x32_f16 v[210:213], v[22:25], v[18:21], v[210:213]
	v_mfma_f32_16x16x32_f16 v[190:193], v[2:5], v[18:21], v[190:193]
	s_waitcnt lgkmcnt(0)
	v_mfma_f32_16x16x32_f16 v[166:169], v[22:25], v[38:41], v[166:169]
	v_mfma_f32_16x16x32_f16 v[162:165], v[2:5], v[38:41], v[162:165]
	v_add_u32_e32 v18, 0x71540, v251
	v_min_u32_e32 v18, v18, v154
	global_load_dwordx4 v[78:81], v18, s[8:9] nt
	s_waitcnt vmcnt(21)
	v_cvt_pk_f16_f32 v19, v88, v89
	v_cvt_pk_f16_f32 v18, v86, v87
	ds_write_b16 v238, v18 offset:3040
	ds_write_b16_d16_hi v239, v18 offset:3040
	ds_write_b16 v240, v19 offset:3040
	ds_write_b16_d16_hi v241, v19 offset:3040
	ds_read_b128 v[18:21], v151 offset:4928
	ds_read_b128 v[38:41], v151 offset:5536
	s_waitcnt lgkmcnt(1)
	v_mfma_f32_16x16x32_f16 v[218:221], v[22:25], v[18:21], v[218:221]
	v_mfma_f32_16x16x32_f16 v[138:141], v[2:5], v[18:21], v[138:141]
	s_waitcnt lgkmcnt(0)
	v_mfma_f32_16x16x32_f16 v[170:173], v[22:25], v[38:41], v[170:173]
	v_mfma_f32_16x16x32_f16 v[126:129], v[2:5], v[38:41], v[126:129]
	ds_read_b128 v[18:21], v151 offset:6144
	ds_read_b128 v[38:41], v151 offset:6752
	s_waitcnt lgkmcnt(1)
	v_mfma_f32_16x16x32_f16 v[118:121], v[22:25], v[18:21], v[118:121]
	v_mfma_f32_16x16x32_f16 v[174:177], v[2:5], v[18:21], v[174:177]
	s_waitcnt lgkmcnt(0)
	v_mfma_f32_16x16x32_f16 v[186:189], v[22:25], v[38:41], v[186:189]
	v_mfma_f32_16x16x32_f16 v[194:197], v[2:5], v[38:41], v[194:197]
	v_add_u32_e32 v18, 0x87b80, v250
	v_min_u32_e32 v18, v18, v154
	global_load_dwordx4 v[82:85], v18, s[8:9] nt
	s_waitcnt vmcnt(21)
	v_cvt_pk_f16_f32 v19, v92, v93
	v_cvt_pk_f16_f32 v18, v90, v91
	ds_write_b16 v234, v18 offset:3648
	ds_write_b16_d16_hi v235, v18 offset:3648
	ds_write_b16 v236, v19 offset:3648
	ds_write_b16_d16_hi v237, v19 offset:3648
	ds_read_b128 v[86:89], v151 offset:7360
	s_mov_b32 s3, 0xa8000
	v_add_co_u32_e32 v18, vcc, s3, v152
	s_mov_b32 s3, 0xac000
	s_nop 0
	v_addc_co_u32_e32 v19, vcc, 0, v153, vcc
	s_waitcnt lgkmcnt(0)
	v_mfma_f32_16x16x32_f16 v[222:225], v[22:25], v[86:89], v[30:33]
	s_nop 2
	global_load_dwordx4 v[30:33], v[18:19], off sc1
	global_load_dwordx4 v[38:41], v[18:19], off offset:256 sc1
	v_add_co_u32_e32 v18, vcc, s3, v152
	v_mfma_f32_16x16x32_f16 v[2:5], v[2:5], v[86:89], v[214:217]
	s_nop 0
	v_addc_co_u32_e32 v19, vcc, 0, v153, vcc
	global_load_dwordx4 v[22:25], v[18:19], off sc1
	s_nop 0
	global_load_dwordx4 v[18:21], v[18:19], off offset:256 sc1
	ds_read_b128 v[86:89], v151 offset:128
	ds_read_b128 v[90:93], v151 offset:736
	s_waitcnt vmcnt(24) lgkmcnt(1)
	v_mfma_f32_16x16x32_f16 v[130:133], v[50:53], v[86:89], v[130:133]
	s_waitcnt vmcnt(23)
	v_mfma_f32_16x16x32_f16 v[202:205], v[54:57], v[86:89], v[202:205]
	ds_read_b128 v[86:89], v151 offset:1344
	s_waitcnt lgkmcnt(0)
	v_mfma_f32_16x16x32_f16 v[114:117], v[50:53], v[86:89], v[114:117]
	v_mfma_f32_16x16x32_f16 v[142:145], v[50:53], v[90:93], v[142:145]
	v_mfma_f32_16x16x32_f16 v[158:161], v[54:57], v[90:93], v[158:161]
	v_mfma_f32_16x16x32_f16 v[178:181], v[54:57], v[86:89], v[178:181]
	v_add_u32_e32 v86, 0x9e1c0, v251
	v_min_u32_e32 v86, v86, v154
	global_load_dwordx4 v[86:89], v86, s[8:9] nt
	s_waitcnt vmcnt(21)
	v_cvt_pk_f16_f32 v91, v96, v97
	v_cvt_pk_f16_f32 v90, v94, v95
	ds_write_b16 v238, v90 offset:4256
	ds_write_b16_d16_hi v239, v90 offset:4256
	ds_write_b16 v240, v91 offset:4256
	ds_write_b16_d16_hi v241, v91 offset:4256
	ds_read_b128 v[90:93], v151 offset:1952
	ds_read_b128 v[94:97], v151 offset:2560
	s_waitcnt lgkmcnt(1)
	v_mfma_f32_16x16x32_f16 v[182:185], v[50:53], v[90:93], v[182:185]
	v_mfma_f32_16x16x32_f16 v[198:201], v[54:57], v[90:93], v[198:201]
	s_waitcnt lgkmcnt(0)
	v_mfma_f32_16x16x32_f16 v[134:137], v[50:53], v[94:97], v[134:137]
	v_mfma_f32_16x16x32_f16 v[146:149], v[54:57], v[94:97], v[146:149]
	ds_read_b128 v[90:93], v151 offset:3168
	ds_read_b128 v[94:97], v151 offset:3776
	s_waitcnt lgkmcnt(1)
	v_mfma_f32_16x16x32_f16 v[206:209], v[50:53], v[90:93], v[206:209]
	v_mfma_f32_16x16x32_f16 v[122:125], v[54:57], v[90:93], v[122:125]
	s_waitcnt lgkmcnt(0)
	v_mfma_f32_16x16x32_f16 v[210:213], v[50:53], v[94:97], v[210:213]
	v_mfma_f32_16x16x32_f16 v[190:193], v[54:57], v[94:97], v[190:193]
	v_add_u32_e32 v90, 0xb4800, v250
	v_min_u32_e32 v90, v90, v154
	global_load_dwordx4 v[90:93], v90, s[8:9] nt
	s_waitcnt vmcnt(21)
	v_cvt_pk_f16_f32 v95, v100, v101
	v_cvt_pk_f16_f32 v94, v98, v99
	ds_write_b16 v234, v94 offset:4864
	ds_write_b16_d16_hi v235, v94 offset:4864
	ds_write_b16 v236, v95 offset:4864
	ds_write_b16_d16_hi v237, v95 offset:4864
	ds_read_b128 v[94:97], v151 offset:4384
	ds_read_b128 v[98:101], v151 offset:6208
	s_waitcnt lgkmcnt(1)
	v_mfma_f32_16x16x32_f16 v[166:169], v[50:53], v[94:97], v[166:169]
	v_mfma_f32_16x16x32_f16 v[162:165], v[54:57], v[94:97], v[162:165]
	ds_read_b128 v[94:97], v151 offset:4992
	ds_read_b128 v[214:217], v151 offset:5600
	s_waitcnt lgkmcnt(1)
	v_mfma_f32_16x16x32_f16 v[218:221], v[50:53], v[94:97], v[218:221]
	v_mfma_f32_16x16x32_f16 v[138:141], v[54:57], v[94:97], v[138:141]
	s_waitcnt lgkmcnt(0)
	v_mfma_f32_16x16x32_f16 v[170:173], v[50:53], v[214:217], v[170:173]
	v_mfma_f32_16x16x32_f16 v[126:129], v[54:57], v[214:217], v[126:129]
	v_mfma_f32_16x16x32_f16 v[118:121], v[50:53], v[98:101], v[118:121]
	v_mfma_f32_16x16x32_f16 v[174:177], v[54:57], v[98:101], v[174:177]
	v_add_u32_e32 v94, 0xcae40, v251
	v_min_u32_e32 v94, v94, v154
	global_load_dwordx4 v[94:97], v94, s[8:9] nt
	s_waitcnt vmcnt(21)
	v_cvt_pk_f16_f32 v99, v104, v105
	v_cvt_pk_f16_f32 v98, v102, v103
	ds_write_b16 v238, v98 offset:5472
	ds_write_b16_d16_hi v239, v98 offset:5472
	ds_write_b16 v240, v99 offset:5472
	ds_write_b16_d16_hi v241, v99 offset:5472
	ds_read_b128 v[98:101], v151 offset:6816
	ds_read_b128 v[102:105], v151 offset:7424
	s_waitcnt lgkmcnt(1)
	v_mfma_f32_16x16x32_f16 v[186:189], v[50:53], v[98:101], v[186:189]
	s_waitcnt lgkmcnt(0)
	v_mfma_f32_16x16x32_f16 v[214:217], v[50:53], v[102:105], v[222:225]
	v_mfma_f32_16x16x32_f16 v[102:105], v[54:57], v[102:105], v[2:5]
	s_nop 2
	ds_read_b128 v[2:5], v151 offset:192
	ds_read_b128 v[50:53], v151 offset:800
	v_mfma_f32_16x16x32_f16 v[194:197], v[54:57], v[98:101], v[194:197]
	s_waitcnt lgkmcnt(1)
	v_mfma_f32_16x16x32_f16 v[130:133], v[26:29], v[2:5], v[130:133]
	v_mfma_f32_16x16x32_f16 v[202:205], v[14:17], v[2:5], v[202:205]
	s_waitcnt lgkmcnt(0)
	v_mfma_f32_16x16x32_f16 v[142:145], v[26:29], v[50:53], v[142:145]
	v_mfma_f32_16x16x32_f16 v[158:161], v[14:17], v[50:53], v[158:161]
	v_add_u32_e32 v2, 0xe1480, v250
	v_min_u32_e32 v2, v2, v154
	global_load_dwordx4 v[98:101], v2, s[8:9] nt
	s_waitcnt vmcnt(21)
	v_cvt_pk_f16_f32 v3, v64, v65
	v_cvt_pk_f16_f32 v2, v62, v63
	ds_write_b16 v234, v2 offset:6080
	ds_write_b16_d16_hi v235, v2 offset:6080
	ds_write_b16 v236, v3 offset:6080
	ds_write_b16_d16_hi v237, v3 offset:6080
	ds_read_b128 v[2:5], v151 offset:1408
	ds_read_b128 v[50:53], v151 offset:2016
	s_waitcnt lgkmcnt(1)
	v_mfma_f32_16x16x32_f16 v[222:225], v[26:29], v[2:5], v[114:117]
	v_mfma_f32_16x16x32_f16 v[178:181], v[14:17], v[2:5], v[178:181]
	s_waitcnt lgkmcnt(0)
	v_mfma_f32_16x16x32_f16 v[182:185], v[26:29], v[50:53], v[182:185]
	v_mfma_f32_16x16x32_f16 v[198:201], v[14:17], v[50:53], v[198:201]
	ds_read_b128 v[2:5], v151 offset:2624
	ds_read_b128 v[50:53], v151 offset:3232
	s_waitcnt lgkmcnt(1)
	v_mfma_f32_16x16x32_f16 v[134:137], v[26:29], v[2:5], v[134:137]
	v_mfma_f32_16x16x32_f16 v[146:149], v[14:17], v[2:5], v[146:149]
	s_waitcnt lgkmcnt(0)
	v_mfma_f32_16x16x32_f16 v[206:209], v[26:29], v[50:53], v[206:209]
	v_mfma_f32_16x16x32_f16 v[122:125], v[14:17], v[50:53], v[122:125]
	v_add_u32_e32 v2, 0xf7ac0, v251
	v_min_u32_e32 v2, v2, v154
	global_load_dwordx4 v[62:65], v2, s[8:9] nt
	s_waitcnt vmcnt(21)
	v_cvt_pk_f16_f32 v3, v68, v69
	v_cvt_pk_f16_f32 v2, v66, v67
	ds_write_b16 v238, v2 offset:6688
	ds_write_b16_d16_hi v239, v2 offset:6688
	ds_write_b16 v240, v3 offset:6688
	ds_write_b16_d16_hi v241, v3 offset:6688
	ds_read_b128 v[2:5], v151 offset:3840
	ds_read_b128 v[50:53], v151 offset:4448
	s_waitcnt lgkmcnt(1)
	v_mfma_f32_16x16x32_f16 v[210:213], v[26:29], v[2:5], v[210:213]
	v_mfma_f32_16x16x32_f16 v[190:193], v[14:17], v[2:5], v[190:193]
	s_waitcnt lgkmcnt(0)
	v_mfma_f32_16x16x32_f16 v[166:169], v[26:29], v[50:53], v[166:169]
	v_mfma_f32_16x16x32_f16 v[162:165], v[14:17], v[50:53], v[162:165]
	ds_read_b128 v[2:5], v151 offset:5056
	ds_read_b128 v[50:53], v151 offset:5664
	s_waitcnt lgkmcnt(1)
	v_mfma_f32_16x16x32_f16 v[218:221], v[26:29], v[2:5], v[218:221]
	v_mfma_f32_16x16x32_f16 v[138:141], v[14:17], v[2:5], v[138:141]
	s_waitcnt lgkmcnt(0)
	v_mfma_f32_16x16x32_f16 v[170:173], v[26:29], v[50:53], v[170:173]
	v_mfma_f32_16x16x32_f16 v[126:129], v[14:17], v[50:53], v[126:129]
	v_add_u32_e32 v2, 0x10e100, v250
	v_min_u32_e32 v2, v2, v154
	v_cndmask_b32_e64 v2, 0, v2, s[0:1]
	global_load_dwordx4 v[66:69], v2, s[8:9] nt
	s_waitcnt vmcnt(21)
	v_cvt_pk_f16_f32 v3, v108, v109
	v_cvt_pk_f16_f32 v2, v106, v107
	ds_write_b16 v234, v2 offset:7296
	ds_write_b16_d16_hi v235, v2 offset:7296
	ds_write_b16 v236, v3 offset:7296
	ds_write_b16_d16_hi v237, v3 offset:7296
	ds_read_b128 v[2:5], v151 offset:6272
	ds_read_b128 v[50:53], v151 offset:6880
	ds_read_b128 v[106:109], v151 offset:7488
	s_mov_b32 s3, 0xb0000
	s_waitcnt lgkmcnt(0)
	v_mfma_f32_16x16x32_f16 v[116:119], v[26:29], v[2:5], v[118:121]
	s_barrier
	v_sub_u32_e32 v245, v234, v243
	v_add_u32_e32 v246, 0xfffffdc0, v245
	v_min_u32_e32 v245, v245, v246
	v_add_u32_e32 v234, v242, v245
	v_sub_u32_e32 v245, v235, v243
	v_add_u32_e32 v246, 0xfffffdc0, v245
	v_min_u32_e32 v245, v245, v246
	v_add_u32_e32 v235, v242, v245
	v_sub_u32_e32 v245, v236, v243
	v_add_u32_e32 v246, 0xfffffdc0, v245
	v_min_u32_e32 v245, v245, v246
	v_add_u32_e32 v236, v242, v245
	v_sub_u32_e32 v245, v237, v243
	v_add_u32_e32 v246, 0xfffffdc0, v245
	v_min_u32_e32 v245, v245, v246
	v_add_u32_e32 v237, v242, v245
	v_sub_u32_e32 v245, v238, v243
	v_add_u32_e32 v246, 0xfffffdc0, v245
	v_min_u32_e32 v245, v245, v246
	v_add_u32_e32 v238, v242, v245
	v_sub_u32_e32 v245, v239, v243
	v_add_u32_e32 v246, 0xfffffdc0, v245
	v_min_u32_e32 v245, v245, v246
	v_add_u32_e32 v239, v242, v245
	v_sub_u32_e32 v245, v240, v243
	v_add_u32_e32 v246, 0xfffffdc0, v245
	v_min_u32_e32 v245, v245, v246
	v_add_u32_e32 v240, v242, v245
	v_sub_u32_e32 v245, v241, v243
	v_add_u32_e32 v246, 0xfffffdc0, v245
	v_min_u32_e32 v245, v245, v246
	v_add_u32_e32 v241, v242, v245
	v_mfma_f32_16x16x32_f16 v[174:177], v[14:17], v[2:5], v[174:177]
	v_add_co_u32_e32 v2, vcc, s3, v152
	s_nop 1
	v_addc_co_u32_e32 v3, vcc, 0, v153, vcc
	v_mfma_f32_16x16x32_f16 v[186:189], v[26:29], v[50:53], v[186:189]
	v_mfma_f32_16x16x32_f16 v[214:217], v[26:29], v[106:109], v[214:217]
	v_add_co_u32_e32 v26, vcc, s2, v152
	s_nop 1
	v_addc_co_u32_e32 v27, vcc, 0, v153, vcc
	v_mfma_f32_16x16x32_f16 v[194:197], v[14:17], v[50:53], v[194:197]
	global_load_dwordx4 v[50:53], v[2:3], off sc1
	global_load_dwordx4 v[54:57], v[2:3], off offset:256 sc1
	s_nop 0
	global_load_dwordx4 v[2:5], v[26:27], off sc1
	s_nop 0
	global_load_dwordx4 v[26:29], v[26:27], off offset:256 sc1
	v_mfma_f32_16x16x32_f16 v[14:17], v[14:17], v[106:109], v[102:105]
	v_mov_b32_e32 v114, 0
	s_nop 1
	ds_read_b128 v[102:105], v151 offset:256
	v_mov_b32_e32 v115, 0
	v_add_u32_e32 v106, 0x1800, v150
	s_waitcnt vmcnt(24) lgkmcnt(0)
	v_mfma_f32_16x16x32_f16 v[130:133], v[34:37], v[102:105], v[130:133]
	s_waitcnt vmcnt(23)
	v_mfma_f32_16x16x32_f16 v[202:205], v[46:49], v[102:105], v[202:205]
	v_min_u32_e32 v102, v106, v114
	global_load_dwordx4 v[102:105], v102, s[8:9] nt
	s_waitcnt vmcnt(21)
	v_cvt_pk_f16_f32 v107, v112, v113
	v_cvt_pk_f16_f32 v106, v110, v111
	ds_write_b16 v234, v106 offset:0
	ds_write_b16_d16_hi v235, v106 offset:0
	ds_write_b16 v236, v107 offset:0
	ds_write_b16_d16_hi v237, v107 offset:0
	ds_read_b128 v[106:109], v151 offset:864
	ds_read_b128 v[110:113], v151 offset:1472
	s_waitcnt lgkmcnt(1)
	v_mfma_f32_16x16x32_f16 v[142:145], v[34:37], v[106:109], v[142:145]
	v_mfma_f32_16x16x32_f16 v[158:161], v[46:49], v[106:109], v[158:161]
	s_waitcnt lgkmcnt(0)
	v_mfma_f32_16x16x32_f16 v[222:225], v[34:37], v[110:113], v[222:225]
	v_mfma_f32_16x16x32_f16 v[110:113], v[46:49], v[110:113], v[178:181]
	ds_read_b128 v[106:109], v151 offset:2080
	s_nop 1
	ds_read_b128 v[178:181], v151 offset:2688
	s_waitcnt lgkmcnt(1)
	v_mfma_f32_16x16x32_f16 v[182:185], v[34:37], v[106:109], v[182:185]
	v_mfma_f32_16x16x32_f16 v[198:201], v[46:49], v[106:109], v[198:201]
	s_waitcnt lgkmcnt(0)
	v_mfma_f32_16x16x32_f16 v[134:137], v[34:37], v[178:181], v[134:137]
	v_mfma_f32_16x16x32_f16 v[146:149], v[46:49], v[178:181], v[146:149]
	v_add_u32_e32 v106, 0x17e40, v244
	v_min_u32_e32 v106, v106, v114
	global_load_dwordx4 v[106:109], v106, s[8:9] nt
	s_waitcnt vmcnt(21)
	v_cvt_pk_f16_f32 v61, v60, v61
	v_cvt_pk_f16_f32 v60, v58, v59
	ds_write_b16 v238, v60 offset:608
	ds_write_b16_d16_hi v239, v60 offset:608
	ds_write_b16 v240, v61 offset:608
	ds_write_b16_d16_hi v241, v61 offset:608
	ds_read_b128 v[58:61], v151 offset:3296
	ds_read_b128 v[178:181], v151 offset:5120
	s_waitcnt lgkmcnt(1)
	v_mfma_f32_16x16x32_f16 v[206:209], v[34:37], v[58:61], v[206:209]
	v_mfma_f32_16x16x32_f16 v[120:123], v[46:49], v[58:61], v[122:125]
	ds_read_b128 v[58:61], v151 offset:3904
	ds_read_b128 v[226:229], v151 offset:4512
	s_waitcnt lgkmcnt(1)
	v_mfma_f32_16x16x32_f16 v[210:213], v[34:37], v[58:61], v[210:213]
	v_mfma_f32_16x16x32_f16 v[190:193], v[46:49], v[58:61], v[190:193]
	s_waitcnt lgkmcnt(0)
	v_mfma_f32_16x16x32_f16 v[166:169], v[34:37], v[226:229], v[166:169]
	v_mfma_f32_16x16x32_f16 v[162:165], v[46:49], v[226:229], v[162:165]
	v_mfma_f32_16x16x32_f16 v[218:221], v[34:37], v[178:181], v[218:221]
	v_mfma_f32_16x16x32_f16 v[138:141], v[46:49], v[178:181], v[138:141]
	v_add_u32_e32 v58, 0x2e480, v150
	v_min_u32_e32 v58, v58, v114
	global_load_dwordx4 v[58:61], v58, s[8:9] nt
	s_waitcnt vmcnt(21)
	v_cvt_pk_f16_f32 v73, v72, v73
	v_cvt_pk_f16_f32 v72, v70, v71
	ds_write_b16 v234, v72 offset:1216
	ds_write_b16_d16_hi v235, v72 offset:1216
	ds_write_b16 v236, v73 offset:1216
	ds_write_b16_d16_hi v237, v73 offset:1216
	ds_read_b128 v[70:73], v151 offset:5728
	ds_read_b128 v[178:181], v151 offset:6336
	s_waitcnt lgkmcnt(1)
	v_mfma_f32_16x16x32_f16 v[170:173], v[34:37], v[70:73], v[170:173]
	v_mfma_f32_16x16x32_f16 v[124:127], v[46:49], v[70:73], v[126:129]
	s_waitcnt lgkmcnt(0)
	v_mfma_f32_16x16x32_f16 v[116:119], v[34:37], v[178:181], v[116:119]
	v_mfma_f32_16x16x32_f16 v[174:177], v[46:49], v[178:181], v[174:177]
	ds_read_b128 v[70:73], v151 offset:6944
	ds_read_b128 v[178:181], v151 offset:7552
	s_waitcnt lgkmcnt(1)
	v_mfma_f32_16x16x32_f16 v[186:189], v[34:37], v[70:73], v[186:189]
	v_mfma_f32_16x16x32_f16 v[194:197], v[46:49], v[70:73], v[194:197]
	s_waitcnt lgkmcnt(0)
	v_mfma_f32_16x16x32_f16 v[214:217], v[34:37], v[178:181], v[214:217]
	v_mfma_f32_16x16x32_f16 v[178:181], v[46:49], v[178:181], v[14:17]
	s_nop 2
	v_add_u32_e32 v14, 0x44ac0, v244
	v_min_u32_e32 v14, v14, v114
	global_load_dwordx4 v[34:37], v14, s[8:9] nt
	s_waitcnt vmcnt(21)
	v_cvt_pk_f16_f32 v15, v44, v45
	v_cvt_pk_f16_f32 v14, v42, v43
	ds_write_b16 v238, v14 offset:1824
	ds_write_b16_d16_hi v239, v14 offset:1824
	ds_write_b16 v240, v15 offset:1824
	ds_write_b16_d16_hi v241, v15 offset:1824
	ds_read_b128 v[14:17], v151 offset:320
	ds_read_b128 v[42:45], v151 offset:928
	s_waitcnt lgkmcnt(1)
	v_mfma_f32_16x16x32_f16 v[128:131], v[10:13], v[14:17], v[130:133]
	v_mfma_f32_16x16x32_f16 v[202:205], v[6:9], v[14:17], v[202:205]
	s_waitcnt lgkmcnt(0)
	v_mfma_f32_16x16x32_f16 v[142:145], v[10:13], v[42:45], v[142:145]
	v_mfma_f32_16x16x32_f16 v[158:161], v[6:9], v[42:45], v[158:161]
	ds_read_b128 v[14:17], v151 offset:1536
	ds_read_b128 v[42:45], v151 offset:2144
	s_waitcnt lgkmcnt(1)
	v_mfma_f32_16x16x32_f16 v[222:225], v[10:13], v[14:17], v[222:225]
	v_mfma_f32_16x16x32_f16 v[110:113], v[6:9], v[14:17], v[110:113]
	s_waitcnt lgkmcnt(0)
	v_mfma_f32_16x16x32_f16 v[182:185], v[10:13], v[42:45], v[182:185]
	v_mfma_f32_16x16x32_f16 v[198:201], v[6:9], v[42:45], v[198:201]
	v_add_u32_e32 v14, 0x5b100, v150
	v_min_u32_e32 v14, v14, v114
	global_load_dwordx4 v[70:73], v14, s[8:9] nt
	s_waitcnt vmcnt(21)
	v_cvt_pk_f16_f32 v15, v76, v77
	v_cvt_pk_f16_f32 v14, v74, v75
	ds_write_b16 v234, v14 offset:2432
	ds_write_b16_d16_hi v235, v14 offset:2432
	ds_write_b16 v236, v15 offset:2432
	ds_write_b16_d16_hi v237, v15 offset:2432
	ds_read_b128 v[14:17], v151 offset:2752
	ds_read_b128 v[42:45], v151 offset:3360
	s_waitcnt lgkmcnt(1)
	v_mfma_f32_16x16x32_f16 v[132:135], v[10:13], v[14:17], v[134:137]
	v_mfma_f32_16x16x32_f16 v[146:149], v[6:9], v[14:17], v[146:149]
	s_waitcnt lgkmcnt(0)
	v_mfma_f32_16x16x32_f16 v[206:209], v[10:13], v[42:45], v[206:209]
	v_mfma_f32_16x16x32_f16 v[120:123], v[6:9], v[42:45], v[120:123]
	ds_read_b128 v[14:17], v151 offset:3968
	ds_read_b128 v[42:45], v151 offset:4576
	s_waitcnt lgkmcnt(1)
	v_mfma_f32_16x16x32_f16 v[210:213], v[10:13], v[14:17], v[210:213]
	v_mfma_f32_16x16x32_f16 v[190:193], v[6:9], v[14:17], v[190:193]
	s_waitcnt lgkmcnt(0)
	v_mfma_f32_16x16x32_f16 v[166:169], v[10:13], v[42:45], v[166:169]
	v_mfma_f32_16x16x32_f16 v[162:165], v[6:9], v[42:45], v[162:165]
	v_add_u32_e32 v14, 0x71740, v244
	v_min_u32_e32 v14, v14, v114
	global_load_dwordx4 v[74:77], v14, s[8:9] nt
	s_waitcnt vmcnt(21)
	v_cvt_pk_f16_f32 v15, v80, v81
	v_cvt_pk_f16_f32 v14, v78, v79
	ds_write_b16 v238, v14 offset:3040
	ds_write_b16_d16_hi v239, v14 offset:3040
	ds_write_b16 v240, v15 offset:3040
	ds_write_b16_d16_hi v241, v15 offset:3040
	ds_read_b128 v[14:17], v151 offset:5184
	ds_read_b128 v[42:45], v151 offset:5792
	s_waitcnt lgkmcnt(1)
	v_mfma_f32_16x16x32_f16 v[218:221], v[10:13], v[14:17], v[218:221]
	v_mfma_f32_16x16x32_f16 v[136:139], v[6:9], v[14:17], v[138:141]
	s_waitcnt lgkmcnt(0)
	v_mfma_f32_16x16x32_f16 v[170:173], v[10:13], v[42:45], v[170:173]
	v_mfma_f32_16x16x32_f16 v[124:127], v[6:9], v[42:45], v[124:127]
	ds_read_b128 v[14:17], v151 offset:6400
	ds_read_b128 v[42:45], v151 offset:7008
	s_waitcnt lgkmcnt(1)
	v_mfma_f32_16x16x32_f16 v[116:119], v[10:13], v[14:17], v[116:119]
	v_mfma_f32_16x16x32_f16 v[174:177], v[6:9], v[14:17], v[174:177]
	s_waitcnt lgkmcnt(0)
	v_mfma_f32_16x16x32_f16 v[186:189], v[10:13], v[42:45], v[186:189]
	v_mfma_f32_16x16x32_f16 v[194:197], v[6:9], v[42:45], v[194:197]
	v_add_u32_e32 v14, 0x87d80, v150
	v_min_u32_e32 v14, v14, v114
	global_load_dwordx4 v[78:81], v14, s[8:9] nt
	s_waitcnt vmcnt(21)
	v_cvt_pk_f16_f32 v15, v84, v85
	v_cvt_pk_f16_f32 v14, v82, v83
	ds_write_b16 v234, v14 offset:3648
	ds_write_b16_d16_hi v235, v14 offset:3648
	ds_write_b16 v236, v15 offset:3648
	ds_write_b16_d16_hi v237, v15 offset:3648
	ds_read_b128 v[82:85], v151 offset:7616
	s_mov_b32 s2, 0xb8000
	v_add_co_u32_e32 v14, vcc, s2, v152
	s_mov_b32 s2, 0xbc000
	s_nop 0
	v_addc_co_u32_e32 v15, vcc, 0, v153, vcc
	v_add_co_u32_e32 v42, vcc, s2, v152
	s_waitcnt lgkmcnt(0)
	v_mfma_f32_16x16x32_f16 v[214:217], v[10:13], v[82:85], v[214:217]
	v_addc_co_u32_e32 v43, vcc, 0, v153, vcc
	global_load_dwordx4 v[10:13], v[14:15], off sc1
	s_nop 0
	global_load_dwordx4 v[14:17], v[14:15], off offset:256 sc1
	s_nop 0
	global_load_dwordx4 v[46:49], v[42:43], off sc1
	s_nop 0
	global_load_dwordx4 v[42:45], v[42:43], off offset:256 sc1
	v_mfma_f32_16x16x32_f16 v[178:181], v[6:9], v[82:85], v[178:181]
	ds_read_b128 v[6:9], v151 offset:384
	ds_read_b128 v[82:85], v151 offset:992
	s_waitcnt vmcnt(24) lgkmcnt(1)
	v_mfma_f32_16x16x32_f16 v[128:131], v[30:33], v[6:9], v[128:131]
	s_waitcnt vmcnt(23)
	v_mfma_f32_16x16x32_f16 v[202:205], v[38:41], v[6:9], v[202:205]
	ds_read_b128 v[6:9], v151 offset:1600
	s_waitcnt lgkmcnt(1)
	v_mfma_f32_16x16x32_f16 v[140:143], v[30:33], v[82:85], v[142:145]
	v_mfma_f32_16x16x32_f16 v[158:161], v[38:41], v[82:85], v[158:161]
	s_waitcnt lgkmcnt(0)
	v_mfma_f32_16x16x32_f16 v[222:225], v[30:33], v[6:9], v[222:225]
	v_mfma_f32_16x16x32_f16 v[110:113], v[38:41], v[6:9], v[110:113]
	v_add_u32_e32 v6, 0x9e3c0, v244
	v_min_u32_e32 v6, v6, v114
	global_load_dwordx4 v[6:9], v6, s[8:9] nt
	s_waitcnt vmcnt(21)
	v_cvt_pk_f16_f32 v83, v88, v89
	v_cvt_pk_f16_f32 v82, v86, v87
	ds_write_b16 v238, v82 offset:4256
	ds_write_b16_d16_hi v239, v82 offset:4256
	ds_write_b16 v240, v83 offset:4256
	ds_write_b16_d16_hi v241, v83 offset:4256
	ds_read_b128 v[82:85], v151 offset:2208
	ds_read_b128 v[86:89], v151 offset:2816
	s_waitcnt lgkmcnt(1)
	v_mfma_f32_16x16x32_f16 v[182:185], v[30:33], v[82:85], v[182:185]
	v_mfma_f32_16x16x32_f16 v[198:201], v[38:41], v[82:85], v[198:201]
	s_waitcnt lgkmcnt(0)
	v_mfma_f32_16x16x32_f16 v[132:135], v[30:33], v[86:89], v[132:135]
	v_mfma_f32_16x16x32_f16 v[144:147], v[38:41], v[86:89], v[146:149]
	ds_read_b128 v[82:85], v151 offset:3424
	ds_read_b128 v[86:89], v151 offset:4032
	s_waitcnt lgkmcnt(1)
	v_mfma_f32_16x16x32_f16 v[206:209], v[30:33], v[82:85], v[206:209]
	v_mfma_f32_16x16x32_f16 v[120:123], v[38:41], v[82:85], v[120:123]
	s_waitcnt lgkmcnt(0)
	v_mfma_f32_16x16x32_f16 v[210:213], v[30:33], v[86:89], v[210:213]
	v_mfma_f32_16x16x32_f16 v[190:193], v[38:41], v[86:89], v[190:193]
	v_add_u32_e32 v82, 0xb4a00, v150
	v_min_u32_e32 v82, v82, v114
	global_load_dwordx4 v[82:85], v82, s[8:9] nt
	s_waitcnt vmcnt(21)
	v_cvt_pk_f16_f32 v87, v92, v93
	v_cvt_pk_f16_f32 v86, v90, v91
	ds_write_b16 v234, v86 offset:4864
	ds_write_b16_d16_hi v235, v86 offset:4864
	ds_write_b16 v236, v87 offset:4864
	ds_write_b16_d16_hi v237, v87 offset:4864
	ds_read_b128 v[86:89], v151 offset:4640
	ds_read_b128 v[90:93], v151 offset:6464
	s_waitcnt lgkmcnt(1)
	v_mfma_f32_16x16x32_f16 v[166:169], v[30:33], v[86:89], v[166:169]
	v_mfma_f32_16x16x32_f16 v[162:165], v[38:41], v[86:89], v[162:165]
	ds_read_b128 v[86:89], v151 offset:5248
	ds_read_b128 v[226:229], v151 offset:5856
	s_waitcnt lgkmcnt(1)
	v_mfma_f32_16x16x32_f16 v[218:221], v[30:33], v[86:89], v[218:221]
	v_mfma_f32_16x16x32_f16 v[136:139], v[38:41], v[86:89], v[136:139]
	s_waitcnt lgkmcnt(0)
	v_mfma_f32_16x16x32_f16 v[170:173], v[30:33], v[226:229], v[170:173]
	v_mfma_f32_16x16x32_f16 v[124:127], v[38:41], v[226:229], v[124:127]
	v_mfma_f32_16x16x32_f16 v[116:119], v[30:33], v[90:93], v[116:119]
	v_mfma_f32_16x16x32_f16 v[90:93], v[38:41], v[90:93], v[174:177]
	v_add_u32_e32 v86, 0xcb040, v244
	v_min_u32_e32 v86, v86, v114
	global_load_dwordx4 v[86:89], v86, s[8:9] nt
	s_waitcnt vmcnt(21)
	v_cvt_pk_f16_f32 v97, v96, v97
	v_cvt_pk_f16_f32 v96, v94, v95
	ds_write_b16 v238, v96 offset:5472
	ds_write_b16_d16_hi v239, v96 offset:5472
	ds_write_b16 v240, v97 offset:5472
	ds_write_b16_d16_hi v241, v97 offset:5472
	ds_read_b128 v[94:97], v151 offset:7072
	ds_read_b128 v[174:177], v151 offset:7680
	s_waitcnt lgkmcnt(1)
	v_mfma_f32_16x16x32_f16 v[186:189], v[30:33], v[94:97], v[186:189]
	v_mfma_f32_16x16x32_f16 v[94:97], v[38:41], v[94:97], v[194:197]
	s_waitcnt lgkmcnt(0)
	v_mfma_f32_16x16x32_f16 v[194:197], v[30:33], v[174:177], v[214:217]
	v_mfma_f32_16x16x32_f16 v[174:177], v[38:41], v[174:177], v[178:181]
	ds_read_b128 v[30:33], v151 offset:448
	ds_read_b128 v[38:41], v151 offset:1056
	s_waitcnt lgkmcnt(1)
	v_mfma_f32_16x16x32_f16 v[128:131], v[22:25], v[30:33], v[128:131]
	v_mfma_f32_16x16x32_f16 v[178:181], v[18:21], v[30:33], v[202:205]
	s_waitcnt lgkmcnt(0)
	v_mfma_f32_16x16x32_f16 v[140:143], v[22:25], v[38:41], v[140:143]
	v_mfma_f32_16x16x32_f16 v[158:161], v[18:21], v[38:41], v[158:161]
	v_add_u32_e32 v30, 0xe1680, v150
	v_min_u32_e32 v30, v30, v114
	global_load_dwordx4 v[30:33], v30, s[8:9] nt
	s_waitcnt vmcnt(21)
	v_cvt_pk_f16_f32 v39, v100, v101
	v_cvt_pk_f16_f32 v38, v98, v99
	ds_write_b16 v234, v38 offset:6080
	ds_write_b16_d16_hi v235, v38 offset:6080
	ds_write_b16 v236, v39 offset:6080
	ds_write_b16_d16_hi v237, v39 offset:6080
	ds_read_b128 v[38:41], v151 offset:1664
	ds_read_b128 v[98:101], v151 offset:2272
	s_waitcnt lgkmcnt(1)
	v_mfma_f32_16x16x32_f16 v[202:205], v[22:25], v[38:41], v[222:225]
	v_mfma_f32_16x16x32_f16 v[214:217], v[18:21], v[38:41], v[110:113]
	ds_read_b128 v[38:41], v151 offset:2880
	s_nop 1
	ds_read_b128 v[110:113], v151 offset:3488
	s_waitcnt lgkmcnt(2)
	v_mfma_f32_16x16x32_f16 v[182:185], v[22:25], v[98:101], v[182:185]
	v_mfma_f32_16x16x32_f16 v[98:101], v[18:21], v[98:101], v[198:201]
	s_waitcnt lgkmcnt(1)
	v_mfma_f32_16x16x32_f16 v[132:135], v[22:25], v[38:41], v[132:135]
	v_mfma_f32_16x16x32_f16 v[144:147], v[18:21], v[38:41], v[144:147]
	s_waitcnt lgkmcnt(0)
	v_mfma_f32_16x16x32_f16 v[198:201], v[22:25], v[110:113], v[206:209]
	v_mfma_f32_16x16x32_f16 v[120:123], v[18:21], v[110:113], v[120:123]
	v_add_u32_e32 v38, 0xf7cc0, v244
	v_min_u32_e32 v38, v38, v114
	global_load_dwordx4 v[38:41], v38, s[8:9] nt
	s_waitcnt vmcnt(21)
	v_cvt_pk_f16_f32 v65, v64, v65
	v_cvt_pk_f16_f32 v64, v62, v63
	ds_write_b16 v238, v64 offset:6688
	ds_write_b16_d16_hi v239, v64 offset:6688
	ds_write_b16 v240, v65 offset:6688
	ds_write_b16_d16_hi v241, v65 offset:6688
	ds_read_b128 v[62:65], v151 offset:4096
	ds_read_b128 v[110:113], v151 offset:4704
	s_waitcnt lgkmcnt(1)
	v_mfma_f32_16x16x32_f16 v[206:209], v[22:25], v[62:65], v[210:213]
	v_mfma_f32_16x16x32_f16 v[62:65], v[18:21], v[62:65], v[190:193]
	s_waitcnt lgkmcnt(0)
	v_mfma_f32_16x16x32_f16 v[166:169], v[22:25], v[110:113], v[166:169]
	v_mfma_f32_16x16x32_f16 v[162:165], v[18:21], v[110:113], v[162:165]
	ds_read_b128 v[110:113], v151 offset:5312
	ds_read_b128 v[190:193], v151 offset:5920
	s_waitcnt lgkmcnt(1)
	v_mfma_f32_16x16x32_f16 v[210:213], v[22:25], v[110:113], v[218:221]
	v_mfma_f32_16x16x32_f16 v[136:139], v[18:21], v[110:113], v[136:139]
	s_waitcnt lgkmcnt(0)
	v_mfma_f32_16x16x32_f16 v[170:173], v[22:25], v[190:193], v[170:173]
	v_mfma_f32_16x16x32_f16 v[124:127], v[18:21], v[190:193], v[124:127]
	v_add_u32_e32 v110, 0x10e300, v150
	v_min_u32_e32 v110, v110, v114
	v_cndmask_b32_e64 v110, 0, v110, s[0:1]
	global_load_dwordx4 v[110:113], v110, s[8:9] nt
	s_waitcnt vmcnt(21)
	v_cvt_pk_f16_f32 v69, v68, v69
	v_cvt_pk_f16_f32 v68, v66, v67
	ds_write_b16 v234, v68 offset:7296
	ds_write_b16_d16_hi v235, v68 offset:7296
	ds_write_b16 v236, v69 offset:7296
	ds_write_b16_d16_hi v237, v69 offset:7296
	ds_read_b128 v[66:69], v151 offset:6528
	ds_read_b128 v[152:155], v151 offset:7136
	s_waitcnt lgkmcnt(1)
	v_mfma_f32_16x16x32_f16 v[116:119], v[22:25], v[66:69], v[116:119]
	v_mfma_f32_16x16x32_f16 v[66:69], v[18:21], v[66:69], v[90:93]
	s_waitcnt lgkmcnt(0)
	v_mfma_f32_16x16x32_f16 v[90:93], v[22:25], v[152:155], v[186:189]
	v_mfma_f32_16x16x32_f16 v[94:97], v[18:21], v[152:155], v[94:97]
	ds_read_b128 v[152:155], v151 offset:7744
	s_waitcnt lgkmcnt(0)
	s_barrier
	v_sub_u32_e32 v245, v234, v243
	v_add_u32_e32 v246, 0xfffffdc0, v245
	v_min_u32_e32 v245, v245, v246
	v_add_u32_e32 v234, v242, v245
	v_sub_u32_e32 v245, v235, v243
	v_add_u32_e32 v246, 0xfffffdc0, v245
	v_min_u32_e32 v245, v245, v246
	v_add_u32_e32 v235, v242, v245
	v_sub_u32_e32 v245, v236, v243
	v_add_u32_e32 v246, 0xfffffdc0, v245
	v_min_u32_e32 v245, v245, v246
	v_add_u32_e32 v236, v242, v245
	v_sub_u32_e32 v245, v237, v243
	v_add_u32_e32 v246, 0xfffffdc0, v245
	v_min_u32_e32 v245, v245, v246
	v_add_u32_e32 v237, v242, v245
	v_sub_u32_e32 v245, v238, v243
	v_add_u32_e32 v246, 0xfffffdc0, v245
	v_min_u32_e32 v245, v245, v246
	v_add_u32_e32 v238, v242, v245
	v_sub_u32_e32 v245, v239, v243
	v_add_u32_e32 v246, 0xfffffdc0, v245
	v_min_u32_e32 v245, v245, v246
	v_add_u32_e32 v239, v242, v245
	v_sub_u32_e32 v245, v240, v243
	v_add_u32_e32 v246, 0xfffffdc0, v245
	v_min_u32_e32 v245, v245, v246
	v_add_u32_e32 v240, v242, v245
	v_sub_u32_e32 v245, v241, v243
	v_add_u32_e32 v246, 0xfffffdc0, v245
	v_min_u32_e32 v245, v245, v246
	v_add_u32_e32 v241, v242, v245
	v_mfma_f32_16x16x32_f16 v[22:25], v[22:25], v[152:155], v[194:197]
	v_mfma_f32_16x16x32_f16 v[18:21], v[18:21], v[152:155], v[174:177]
	v_mov_b32_e32 v114, 0
	ds_read_b128 v[152:155], v151 offset:512
	s_waitcnt vmcnt(20) lgkmcnt(0)
	v_mfma_f32_16x16x32_f16 v[128:131], v[50:53], v[152:155], v[128:131]
	s_waitcnt vmcnt(19)
	v_mfma_f32_16x16x32_f16 v[152:155], v[54:57], v[152:155], v[178:181]
	s_waitcnt vmcnt(16)
	v_cvt_pk_f16_f32 v105, v104, v105
	v_cvt_pk_f16_f32 v104, v102, v103
	ds_write_b16 v234, v104 offset:0
	ds_write_b16_d16_hi v235, v104 offset:0
	ds_write_b16 v236, v105 offset:0
	ds_write_b16_d16_hi v237, v105 offset:0
	ds_read_b128 v[102:105], v151 offset:1120
	ds_read_b128 v[174:177], v151 offset:1728
	ds_read_b128 v[178:181], v151 offset:2336
	ds_read_b128 v[186:189], v151 offset:2944
	s_waitcnt lgkmcnt(3)
	v_mfma_f32_16x16x32_f16 v[140:143], v[50:53], v[102:105], v[140:143]
	v_mfma_f32_16x16x32_f16 v[102:105], v[54:57], v[102:105], v[158:161]
	s_waitcnt lgkmcnt(2)
	v_mfma_f32_16x16x32_f16 v[158:161], v[50:53], v[174:177], v[202:205]
	v_mfma_f32_16x16x32_f16 v[174:177], v[54:57], v[174:177], v[214:217]
	s_waitcnt lgkmcnt(1)
	v_mfma_f32_16x16x32_f16 v[182:185], v[50:53], v[178:181], v[182:185]
	v_mfma_f32_16x16x32_f16 v[98:101], v[54:57], v[178:181], v[98:101]
	s_waitcnt lgkmcnt(0)
	v_mfma_f32_16x16x32_f16 v[132:135], v[50:53], v[186:189], v[132:135]
	v_mfma_f32_16x16x32_f16 v[144:147], v[54:57], v[186:189], v[144:147]
	s_waitcnt vmcnt(15)
	v_cvt_pk_f16_f32 v109, v108, v109
	v_cvt_pk_f16_f32 v108, v106, v107
	ds_write_b16 v238, v108 offset:608
	ds_write_b16_d16_hi v239, v108 offset:608
	ds_write_b16 v240, v109 offset:608
	ds_write_b16_d16_hi v241, v109 offset:608
	ds_read_b128 v[106:109], v151 offset:3552
	ds_read_b128 v[178:181], v151 offset:5376
	s_waitcnt lgkmcnt(1)
	v_mfma_f32_16x16x32_f16 v[186:189], v[50:53], v[106:109], v[198:201]
	v_mfma_f32_16x16x32_f16 v[106:109], v[54:57], v[106:109], v[120:123]
	s_nop 2
	ds_read_b128 v[120:123], v151 offset:4160
	ds_read_b128 v[190:193], v151 offset:4768
	s_waitcnt lgkmcnt(1)
	v_mfma_f32_16x16x32_f16 v[194:197], v[50:53], v[120:123], v[206:209]
	v_mfma_f32_16x16x32_f16 v[62:65], v[54:57], v[120:123], v[62:65]
	s_waitcnt lgkmcnt(0)
	v_mfma_f32_16x16x32_f16 v[120:123], v[50:53], v[190:193], v[166:169]
	v_mfma_f32_16x16x32_f16 v[162:165], v[54:57], v[190:193], v[162:165]
	v_mfma_f32_16x16x32_f16 v[166:169], v[50:53], v[178:181], v[210:213]
	v_mfma_f32_16x16x32_f16 v[136:139], v[54:57], v[178:181], v[136:139]
	s_waitcnt vmcnt(14)
	v_cvt_pk_f16_f32 v61, v60, v61
	v_cvt_pk_f16_f32 v60, v58, v59
	ds_write_b16 v234, v60 offset:1216
	ds_write_b16_d16_hi v235, v60 offset:1216
	ds_write_b16 v236, v61 offset:1216
	ds_write_b16_d16_hi v237, v61 offset:1216
	ds_read_b128 v[58:61], v151 offset:5984
	ds_read_b128 v[178:181], v151 offset:6592
	s_waitcnt lgkmcnt(1)
	v_mfma_f32_16x16x32_f16 v[170:173], v[50:53], v[58:61], v[170:173]
	v_mfma_f32_16x16x32_f16 v[58:61], v[54:57], v[58:61], v[124:127]
	s_waitcnt lgkmcnt(0)
	v_mfma_f32_16x16x32_f16 v[116:119], v[50:53], v[178:181], v[116:119]
	v_mfma_f32_16x16x32_f16 v[66:69], v[54:57], v[178:181], v[66:69]
	ds_read_b128 v[124:127], v151 offset:7200
	ds_read_b128 v[178:181], v151 offset:7808
	s_waitcnt lgkmcnt(1)
	v_mfma_f32_16x16x32_f16 v[90:93], v[50:53], v[124:127], v[90:93]
	v_mfma_f32_16x16x32_f16 v[94:97], v[54:57], v[124:127], v[94:97]
	s_waitcnt lgkmcnt(0)
	v_mfma_f32_16x16x32_f16 v[22:25], v[50:53], v[178:181], v[22:25]
	v_mfma_f32_16x16x32_f16 v[18:21], v[54:57], v[178:181], v[18:21]
	s_waitcnt vmcnt(13)
	v_cvt_pk_f16_f32 v37, v36, v37
	v_cvt_pk_f16_f32 v36, v34, v35
	ds_write_b16 v238, v36 offset:1824
	ds_write_b16_d16_hi v239, v36 offset:1824
	ds_write_b16 v240, v37 offset:1824
	ds_write_b16_d16_hi v241, v37 offset:1824
	ds_read_b128 v[34:37], v151 offset:0
	ds_read_b128 v[50:53], v151 offset:608
	s_waitcnt lgkmcnt(1)
	v_mfma_f32_16x16x32_f16 v[54:57], v[2:5], v[34:37], v[128:131]
	s_waitcnt lgkmcnt(0)
	v_mfma_f32_16x16x32_f16 v[124:127], v[2:5], v[50:53], v[140:143]
	v_mfma_f32_16x16x32_f16 v[50:53], v[26:29], v[50:53], v[102:105]
	s_nop 2
	ds_read_b128 v[102:105], v151 offset:1216
	ds_read_b128 v[128:131], v151 offset:1824
	v_mfma_f32_16x16x32_f16 v[34:37], v[26:29], v[34:37], v[152:155]
	s_waitcnt lgkmcnt(1)
	v_mfma_f32_16x16x32_f16 v[140:143], v[2:5], v[102:105], v[158:161]
	v_mfma_f32_16x16x32_f16 v[102:105], v[26:29], v[102:105], v[174:177]
	s_waitcnt lgkmcnt(0)
	v_mfma_f32_16x16x32_f16 v[152:155], v[2:5], v[128:131], v[182:185]
	v_mfma_f32_16x16x32_f16 v[98:101], v[26:29], v[128:131], v[98:101]
	s_waitcnt vmcnt(12)
	v_cvt_pk_f16_f32 v73, v72, v73
	v_cvt_pk_f16_f32 v72, v70, v71
	ds_write_b16 v234, v72 offset:2432
	ds_write_b16_d16_hi v235, v72 offset:2432
	ds_write_b16 v236, v73 offset:2432
	ds_write_b16_d16_hi v237, v73 offset:2432
	ds_read_b128 v[70:73], v151 offset:2432
	ds_read_b128 v[128:131], v151 offset:3040
	s_waitcnt lgkmcnt(1)
	v_mfma_f32_16x16x32_f16 v[132:135], v[2:5], v[70:73], v[132:135]
	v_mfma_f32_16x16x32_f16 v[70:73], v[26:29], v[70:73], v[144:147]
	s_waitcnt lgkmcnt(0)
	v_mfma_f32_16x16x32_f16 v[144:147], v[2:5], v[128:131], v[186:189]
	v_mfma_f32_16x16x32_f16 v[106:109], v[26:29], v[128:131], v[106:109]
	ds_read_b128 v[128:131], v151 offset:3648
	ds_read_b128 v[158:161], v151 offset:4256
	s_waitcnt lgkmcnt(1)
	v_mfma_f32_16x16x32_f16 v[174:177], v[2:5], v[128:131], v[194:197]
	v_mfma_f32_16x16x32_f16 v[62:65], v[26:29], v[128:131], v[62:65]
	s_waitcnt lgkmcnt(0)
	v_mfma_f32_16x16x32_f16 v[120:123], v[2:5], v[158:161], v[120:123]
	v_mfma_f32_16x16x32_f16 v[128:131], v[26:29], v[158:161], v[162:165]
	s_waitcnt vmcnt(11)
	v_cvt_pk_f16_f32 v77, v76, v77
	v_cvt_pk_f16_f32 v76, v74, v75
	ds_write_b16 v238, v76 offset:3040
	ds_write_b16_d16_hi v239, v76 offset:3040
	ds_write_b16 v240, v77 offset:3040
	ds_write_b16_d16_hi v241, v77 offset:3040
	ds_read_b128 v[74:77], v151 offset:4864
	ds_read_b128 v[158:161], v151 offset:5472
	s_waitcnt lgkmcnt(1)
	v_mfma_f32_16x16x32_f16 v[162:165], v[2:5], v[74:77], v[166:169]
	v_mfma_f32_16x16x32_f16 v[74:77], v[26:29], v[74:77], v[136:139]
	s_waitcnt lgkmcnt(0)
	v_mfma_f32_16x16x32_f16 v[136:139], v[2:5], v[158:161], v[170:173]
	v_mfma_f32_16x16x32_f16 v[58:61], v[26:29], v[158:161], v[58:61]
	ds_read_b128 v[158:161], v151 offset:6080
	ds_read_b128 v[166:169], v151 offset:6688
	s_waitcnt lgkmcnt(1)
	v_mfma_f32_16x16x32_f16 v[116:119], v[2:5], v[158:161], v[116:119]
	v_mfma_f32_16x16x32_f16 v[66:69], v[26:29], v[158:161], v[66:69]
	s_waitcnt lgkmcnt(0)
	v_mfma_f32_16x16x32_f16 v[90:93], v[2:5], v[166:169], v[90:93]
	v_mfma_f32_16x16x32_f16 v[94:97], v[26:29], v[166:169], v[94:97]
	s_waitcnt vmcnt(10)
	v_cvt_pk_f16_f32 v81, v80, v81
	v_cvt_pk_f16_f32 v80, v78, v79
	ds_write_b16 v234, v80 offset:3648
	ds_write_b16_d16_hi v235, v80 offset:3648
	ds_write_b16 v236, v81 offset:3648
	ds_write_b16_d16_hi v237, v81 offset:3648
	ds_read_b128 v[78:81], v151 offset:7296
	s_waitcnt lgkmcnt(0)
	v_mfma_f32_16x16x32_f16 v[2:5], v[2:5], v[78:81], v[22:25]
	v_mfma_f32_16x16x32_f16 v[18:21], v[26:29], v[78:81], v[18:21]
	s_nop 1
	ds_read_b128 v[22:25], v151 offset:64
	ds_read_b128 v[26:29], v151 offset:672
	s_waitcnt vmcnt(9) lgkmcnt(1)
	v_mfma_f32_16x16x32_f16 v[54:57], v[10:13], v[22:25], v[54:57]
	s_waitcnt vmcnt(8)
	v_mfma_f32_16x16x32_f16 v[22:25], v[14:17], v[22:25], v[34:37]
	s_waitcnt lgkmcnt(0)
	v_mfma_f32_16x16x32_f16 v[34:37], v[10:13], v[26:29], v[124:127]
	v_mfma_f32_16x16x32_f16 v[26:29], v[14:17], v[26:29], v[50:53]
	s_nop 2
	ds_read_b128 v[50:53], v151 offset:1280
	s_waitcnt lgkmcnt(0)
	v_mfma_f32_16x16x32_f16 v[78:81], v[10:13], v[50:53], v[140:143]
	v_mfma_f32_16x16x32_f16 v[50:53], v[14:17], v[50:53], v[102:105]
	s_waitcnt vmcnt(5)
	v_cvt_pk_f16_f32 v9, v8, v9
	v_cvt_pk_f16_f32 v8, v6, v7
	ds_write_b16 v238, v8 offset:4256
	ds_write_b16_d16_hi v239, v8 offset:4256
	ds_write_b16 v240, v9 offset:4256
	ds_write_b16_d16_hi v241, v9 offset:4256
	ds_read_b128 v[6:9], v151 offset:1888
	ds_read_b128 v[102:105], v151 offset:2496
	s_waitcnt lgkmcnt(1)
	v_mfma_f32_16x16x32_f16 v[124:127], v[10:13], v[6:9], v[152:155]
	v_mfma_f32_16x16x32_f16 v[6:9], v[14:17], v[6:9], v[98:101]
	s_waitcnt lgkmcnt(0)
	v_mfma_f32_16x16x32_f16 v[132:135], v[10:13], v[102:105], v[132:135]
	v_mfma_f32_16x16x32_f16 v[70:73], v[14:17], v[102:105], v[70:73]
	ds_read_b128 v[98:101], v151 offset:3104
	ds_read_b128 v[102:105], v151 offset:3712
	s_waitcnt lgkmcnt(1)
	v_mfma_f32_16x16x32_f16 v[140:143], v[10:13], v[98:101], v[144:147]
	v_mfma_f32_16x16x32_f16 v[144:147], v[14:17], v[98:101], v[106:109]
	s_waitcnt lgkmcnt(0)
	v_mfma_f32_16x16x32_f16 v[152:155], v[10:13], v[102:105], v[174:177]
	v_mfma_f32_16x16x32_f16 v[158:161], v[14:17], v[102:105], v[62:65]
	s_waitcnt vmcnt(4)
	s_nop 1
	v_cvt_pk_f16_f32 v63, v84, v85
	v_cvt_pk_f16_f32 v62, v82, v83
	ds_write_b16 v234, v62 offset:4864
	ds_write_b16_d16_hi v235, v62 offset:4864
	ds_write_b16 v236, v63 offset:4864
	ds_write_b16_d16_hi v237, v63 offset:4864
	ds_read_b128 v[62:65], v151 offset:4320
	ds_read_b128 v[82:85], v151 offset:6144
	s_waitcnt lgkmcnt(1)
	v_mfma_f32_16x16x32_f16 v[120:123], v[10:13], v[62:65], v[120:123]
	v_mfma_f32_16x16x32_f16 v[128:131], v[14:17], v[62:65], v[128:131]
	ds_read_b128 v[62:65], v151 offset:4928
	ds_read_b128 v[98:101], v151 offset:5536
	s_waitcnt lgkmcnt(1)
	v_mfma_f32_16x16x32_f16 v[162:165], v[10:13], v[62:65], v[162:165]
	v_mfma_f32_16x16x32_f16 v[166:169], v[14:17], v[62:65], v[74:77]
	s_waitcnt lgkmcnt(0)
	v_mfma_f32_16x16x32_f16 v[136:139], v[10:13], v[98:101], v[136:139]
	v_mfma_f32_16x16x32_f16 v[170:173], v[14:17], v[98:101], v[58:61]
	v_mfma_f32_16x16x32_f16 v[116:119], v[10:13], v[82:85], v[116:119]
	v_mfma_f32_16x16x32_f16 v[174:177], v[14:17], v[82:85], v[66:69]
	s_waitcnt vmcnt(3)
	v_cvt_pk_f16_f32 v59, v88, v89
	v_cvt_pk_f16_f32 v58, v86, v87
	ds_write_b16 v238, v58 offset:5472
	ds_write_b16_d16_hi v239, v58 offset:5472
	ds_write_b16 v240, v59 offset:5472
	ds_write_b16_d16_hi v241, v59 offset:5472
	ds_read_b128 v[58:61], v151 offset:6752
	ds_read_b128 v[62:65], v151 offset:7360
	s_waitcnt lgkmcnt(1)
	v_mfma_f32_16x16x32_f16 v[178:181], v[10:13], v[58:61], v[90:93]
	v_mfma_f32_16x16x32_f16 v[182:185], v[14:17], v[58:61], v[94:97]
	s_waitcnt lgkmcnt(0)
	v_mfma_f32_16x16x32_f16 v[2:5], v[10:13], v[62:65], v[2:5]
	v_mfma_f32_16x16x32_f16 v[186:189], v[14:17], v[62:65], v[18:21]
	ds_read_b128 v[10:13], v151 offset:128
	ds_read_b128 v[14:17], v151 offset:736
	s_waitcnt lgkmcnt(1)
	v_mfma_f32_16x16x32_f16 v[148:151], v[46:49], v[10:13], v[54:57]
	v_mfma_f32_16x16x32_f16 v[106:109], v[42:45], v[10:13], v[22:25]
	s_waitcnt lgkmcnt(0)
	v_mfma_f32_16x16x32_f16 v[102:105], v[46:49], v[14:17], v[34:37]
	v_mfma_f32_16x16x32_f16 v[94:97], v[42:45], v[14:17], v[26:29]
	s_waitcnt vmcnt(2)
	v_cvt_pk_f16_f32 v11, v32, v33
	v_cvt_pk_f16_f32 v10, v30, v31
	ds_write_b16 v234, v10 offset:6080
	ds_write_b16_d16_hi v235, v10 offset:6080
	ds_write_b16 v236, v11 offset:6080
	ds_write_b16_d16_hi v237, v11 offset:6080
	ds_read_b128 v[10:13], v151 offset:1344
	ds_read_b128 v[14:17], v151 offset:1952
	s_waitcnt lgkmcnt(1)
	v_mfma_f32_16x16x32_f16 v[98:101], v[46:49], v[10:13], v[78:81]
	v_mfma_f32_16x16x32_f16 v[90:93], v[42:45], v[10:13], v[50:53]
	s_waitcnt lgkmcnt(0)
	v_mfma_f32_16x16x32_f16 v[82:85], v[42:45], v[14:17], v[6:9]
	s_nop 2
	ds_read_b128 v[6:9], v151 offset:2560
	ds_read_b128 v[10:13], v151 offset:3168
	v_mfma_f32_16x16x32_f16 v[86:89], v[46:49], v[14:17], v[124:127]
	s_waitcnt lgkmcnt(1)
	v_mfma_f32_16x16x32_f16 v[78:81], v[46:49], v[6:9], v[132:135]
	v_mfma_f32_16x16x32_f16 v[74:77], v[42:45], v[6:9], v[70:73]
	s_waitcnt lgkmcnt(0)
	v_mfma_f32_16x16x32_f16 v[70:73], v[46:49], v[10:13], v[140:143]
	v_mfma_f32_16x16x32_f16 v[62:65], v[42:45], v[10:13], v[144:147]
	s_waitcnt vmcnt(1)
	v_cvt_pk_f16_f32 v7, v40, v41
	v_cvt_pk_f16_f32 v6, v38, v39
	ds_write_b16 v238, v6 offset:6688
	ds_write_b16_d16_hi v239, v6 offset:6688
	ds_write_b16 v240, v7 offset:6688
	ds_write_b16_d16_hi v241, v7 offset:6688
	ds_read_b128 v[6:9], v151 offset:3776
	ds_read_b128 v[10:13], v151 offset:4384
	s_waitcnt lgkmcnt(1)
	v_mfma_f32_16x16x32_f16 v[66:69], v[46:49], v[6:9], v[152:155]
	v_mfma_f32_16x16x32_f16 v[58:61], v[42:45], v[6:9], v[158:161]
	s_waitcnt lgkmcnt(0)
	v_mfma_f32_16x16x32_f16 v[54:57], v[46:49], v[10:13], v[120:123]
	v_mfma_f32_16x16x32_f16 v[50:53], v[42:45], v[10:13], v[128:131]
	ds_read_b128 v[6:9], v151 offset:4992
	ds_read_b128 v[10:13], v151 offset:5600
	s_waitcnt lgkmcnt(1)
	v_mfma_f32_16x16x32_f16 v[38:41], v[46:49], v[6:9], v[162:165]
	v_mfma_f32_16x16x32_f16 v[34:37], v[42:45], v[6:9], v[166:169]
	s_waitcnt lgkmcnt(0)
	v_mfma_f32_16x16x32_f16 v[30:33], v[46:49], v[10:13], v[136:139]
	v_mfma_f32_16x16x32_f16 v[18:21], v[42:45], v[10:13], v[170:173]
	s_waitcnt vmcnt(0)
	v_cvt_pk_f16_f32 v7, v112, v113
	v_cvt_pk_f16_f32 v6, v110, v111
	ds_write_b16 v234, v6 offset:7296
	ds_write_b16_d16_hi v235, v6 offset:7296
	ds_write_b16 v236, v7 offset:7296
	ds_write_b16_d16_hi v237, v7 offset:7296
	ds_read_b128 v[6:9], v151 offset:6208
	ds_read_b128 v[10:13], v151 offset:6816
	ds_read_b128 v[110:113], v151 offset:7424
	s_waitcnt lgkmcnt(0)
	s_barrier
	v_mfma_f32_16x16x32_f16 v[22:25], v[46:49], v[6:9], v[116:119]
	s_barrier
	v_mfma_f32_16x16x32_f16 v[26:29], v[42:45], v[6:9], v[174:177]
	s_movk_i32 s0, 0xffe0
	v_lshrrev_b32_e32 v6, 2, v0
	v_and_b32_e32 v1, 15, v0
	v_ashrrev_i32_e32 v114, 1, v0
	v_and_b32_e32 v116, 12, v6
	v_mfma_f32_16x16x32_f16 v[14:17], v[46:49], v[10:13], v[178:181]
	v_and_or_b32 v120, v114, s0, v116
	v_lshlrev_b32_e32 v114, 3, v1
	v_lshlrev_b32_e32 v129, 1, v120
	v_mfma_f32_16x16x32_f16 v[6:9], v[46:49], v[110:113], v[2:5]
	v_mov_b32_e32 v46, 0x1f480
	v_lshl_add_u32 v128, v120, 2, v46
	v_or_b32_e32 v46, 0x1ee00, v114
	v_or_b32_e32 v47, 0x1ee80, v114
	v_or_b32_e32 v48, 0x1ef00, v114
	v_or_b32_e32 v49, 0x1ef80, v114
	v_mfma_f32_16x16x32_f16 v[10:13], v[42:45], v[10:13], v[182:185]
	s_movk_i32 s4, 0x210
	s_movk_i32 s0, 0x1880
	v_cmp_gt_i32_e32 vcc, s0, v0
	v_mfma_f32_16x16x32_f16 v[2:5], v[42:45], v[110:113], v[186:189]
	ds_read_b128 v[42:45], v128
	ds_read_b64 v[124:125], v46
	ds_read_b64 v[126:127], v47
	ds_read_b64 v[118:119], v48
	ds_read_b64 v[116:117], v49
	ds_read_b128 v[46:49], v128
	ds_read_b128 v[120:123], v128 offset:64
	s_waitcnt lgkmcnt(4)
	v_pk_fma_f32 v[104:105], v[126:127], v[44:45], v[104:105] op_sel_hi:[0,1,1]
	v_pk_fma_f32 v[102:103], v[126:127], v[42:43], v[102:103] op_sel_hi:[0,1,1]
	s_waitcnt lgkmcnt(0)
	v_pk_fma_f32 v[108:109], v[124:125], v[122:123], v[108:109] op_sel_hi:[0,1,1]
	v_pk_fma_f32 v[106:107], v[124:125], v[120:121], v[106:107] op_sel_hi:[0,1,1]
	v_pk_mul_f32 v[108:109], v[124:125], v[108:109] op_sel:[1,0]
	v_pk_mul_f32 v[106:107], v[124:125], v[106:107] op_sel:[1,0]
	v_cvt_pk_f16_f32 v109, v108, v109
	v_cvt_pk_f16_f32 v108, v106, v107
	v_or_b32_e32 v106, 32, v129
	v_mad_u32_u24 v107, v1, s4, v106
	ds_write_b64 v107, v[108:109]
	v_mov_b32_e32 v107, 0x2100
	v_pk_fma_f32 v[96:97], v[126:127], v[122:123], v[96:97] op_sel_hi:[0,1,1]
	v_pk_fma_f32 v[94:95], v[126:127], v[120:121], v[94:95] op_sel_hi:[0,1,1]
	v_mad_u32_u24 v107, v1, s4, v107
	v_pk_mul_f32 v[96:97], v[126:127], v[96:97] op_sel:[1,0]
	v_pk_mul_f32 v[94:95], v[126:127], v[94:95] op_sel:[1,0]
	v_pk_mul_f32 v[104:105], v[126:127], v[104:105] op_sel:[1,0]
	v_pk_mul_f32 v[102:103], v[126:127], v[102:103] op_sel:[1,0]
	v_cvt_pk_f16_f32 v97, v96, v97
	v_cvt_pk_f16_f32 v96, v94, v95
	v_add_u32_e32 v94, v107, v106
	v_cvt_pk_f16_f32 v105, v104, v105
	v_cvt_pk_f16_f32 v104, v102, v103
	v_add_u32_e32 v102, v107, v129
	ds_write_b64 v94, v[96:97]
	v_mov_b32_e32 v94, 0x4200
	v_pk_fma_f32 v[92:93], v[118:119], v[122:123], v[92:93] op_sel_hi:[0,1,1]
	v_pk_fma_f32 v[90:91], v[118:119], v[120:121], v[90:91] op_sel_hi:[0,1,1]
	ds_write_b64 v102, v[104:105]
	v_mad_u32_u24 v102, v1, s4, v94
	v_pk_mul_f32 v[92:93], v[118:119], v[92:93] op_sel:[1,0]
	v_pk_mul_f32 v[90:91], v[118:119], v[90:91] op_sel:[1,0]
	v_cvt_pk_f16_f32 v93, v92, v93
	v_cvt_pk_f16_f32 v92, v90, v91
	v_add_u32_e32 v90, v102, v106
	ds_write_b64 v90, v[92:93]
	v_mov_b32_e32 v90, 0x6300
	v_pk_fma_f32 v[84:85], v[116:117], v[122:123], v[84:85] op_sel_hi:[0,1,1]
	v_pk_fma_f32 v[82:83], v[116:117], v[120:121], v[82:83] op_sel_hi:[0,1,1]
	v_pk_fma_f32 v[110:111], v[124:125], v[44:45], v[150:151] op_sel_hi:[0,1,1]
	v_pk_fma_f32 v[112:113], v[124:125], v[42:43], v[148:149] op_sel_hi:[0,1,1]
	v_mad_u32_u24 v90, v1, s4, v90
	v_pk_mul_f32 v[84:85], v[116:117], v[84:85] op_sel:[1,0]
	v_pk_mul_f32 v[82:83], v[116:117], v[82:83] op_sel:[1,0]
	v_pk_mul_f32 v[110:111], v[124:125], v[110:111] op_sel:[1,0]
	v_pk_mul_f32 v[112:113], v[124:125], v[112:113] op_sel:[1,0]
	v_cvt_pk_f16_f32 v85, v84, v85
	v_cvt_pk_f16_f32 v84, v82, v83
	v_add_u32_e32 v82, v90, v106
	v_cvt_pk_f16_f32 v111, v110, v111
	v_cvt_pk_f16_f32 v110, v112, v113
	v_mad_u32_u24 v112, v1, s4, v129
	ds_write_b64 v82, v[84:85]
	v_or_b32_e32 v82, 0x1f000, v114
	ds_write_b64 v112, v[110:111]
	ds_read_b128 v[110:113], v128
	ds_read_b64 v[82:83], v82
	v_pk_fma_f32 v[94:95], v[118:119], v[44:45], v[100:101] op_sel_hi:[0,1,1]
	v_pk_fma_f32 v[96:97], v[118:119], v[42:43], v[98:99] op_sel_hi:[0,1,1]
	v_pk_fma_f32 v[88:89], v[116:117], v[44:45], v[88:89] op_sel_hi:[0,1,1]
	v_pk_fma_f32 v[86:87], v[116:117], v[42:43], v[86:87] op_sel_hi:[0,1,1]
	v_pk_mul_f32 v[94:95], v[118:119], v[94:95] op_sel:[1,0]
	v_pk_mul_f32 v[96:97], v[118:119], v[96:97] op_sel:[1,0]
	v_pk_mul_f32 v[88:89], v[116:117], v[88:89] op_sel:[1,0]
	v_pk_mul_f32 v[86:87], v[116:117], v[86:87] op_sel:[1,0]
	v_mov_b32_e32 v84, 0x8400
	s_waitcnt lgkmcnt(0)
	v_pk_fma_f32 v[44:45], v[82:83], v[44:45], v[80:81] op_sel_hi:[0,1,1]
	v_pk_fma_f32 v[42:43], v[82:83], v[42:43], v[78:79] op_sel_hi:[0,1,1]
	v_cvt_pk_f16_f32 v95, v94, v95
	v_cvt_pk_f16_f32 v94, v96, v97
	v_add_u32_e32 v96, v102, v129
	v_cvt_pk_f16_f32 v89, v88, v89
	v_cvt_pk_f16_f32 v88, v86, v87
	v_add_u32_e32 v86, v90, v129
	v_mad_u32_u24 v90, v1, s4, v84
	v_pk_mul_f32 v[44:45], v[82:83], v[44:45] op_sel:[1,0]
	v_pk_mul_f32 v[42:43], v[82:83], v[42:43] op_sel:[1,0]
	ds_write_b64 v96, v[94:95]
	ds_write_b64 v86, v[88:89]
	v_or_b32_e32 v84, 0x1f080, v114
	v_or_b32_e32 v86, 0x1f100, v114
	v_or_b32_e32 v88, 0x1f180, v114
	v_cvt_pk_f16_f32 v45, v44, v45
	v_cvt_pk_f16_f32 v44, v42, v43
	v_add_u32_e32 v42, v90, v129
	ds_read_b64 v[84:85], v84
	ds_read_b64 v[86:87], v86
	ds_read_b64 v[88:89], v88
	ds_write_b64 v42, v[44:45]
	v_pk_fma_f32 v[42:43], v[82:83], v[122:123], v[76:77] op_sel_hi:[0,1,1]
	v_pk_fma_f32 v[44:45], v[82:83], v[120:121], v[74:75] op_sel_hi:[0,1,1]
	v_pk_mul_f32 v[42:43], v[82:83], v[42:43] op_sel:[1,0]
	v_pk_mul_f32 v[44:45], v[82:83], v[44:45] op_sel:[1,0]
	v_cvt_pk_f16_f32 v43, v42, v43
	v_cvt_pk_f16_f32 v42, v44, v45
	v_add_u32_e32 v44, v90, v106
	ds_write_b64 v44, v[42:43]
	v_mov_b32_e32 v42, 0xa500
	v_mad_u32_u24 v74, v1, s4, v42
	s_waitcnt lgkmcnt(4)
	v_pk_fma_f32 v[42:43], v[84:85], v[48:49], v[72:73] op_sel_hi:[0,1,1]
	v_pk_fma_f32 v[44:45], v[84:85], v[46:47], v[70:71] op_sel_hi:[0,1,1]
	v_pk_mul_f32 v[42:43], v[84:85], v[42:43] op_sel:[1,0]
	v_pk_mul_f32 v[70:71], v[84:85], v[44:45] op_sel:[1,0]
	v_cvt_pk_f16_f32 v73, v42, v43
	ds_read_b128 v[42:45], v128 offset:64
	v_cvt_pk_f16_f32 v72, v70, v71
	v_add_u32_e32 v70, v74, v129
	ds_write_b64 v70, v[72:73]
	ds_read_b128 v[70:73], v128 offset:64
	s_waitcnt lgkmcnt(2)
	v_pk_fma_f32 v[64:65], v[84:85], v[44:45], v[64:65] op_sel_hi:[0,1,1]
	v_pk_fma_f32 v[62:63], v[84:85], v[42:43], v[62:63] op_sel_hi:[0,1,1]
	v_pk_mul_f32 v[64:65], v[84:85], v[64:65] op_sel:[1,0]
	v_pk_mul_f32 v[62:63], v[84:85], v[62:63] op_sel:[1,0]
	v_cvt_pk_f16_f32 v65, v64, v65
	v_cvt_pk_f16_f32 v64, v62, v63
	v_add_u32_e32 v62, v74, v106
	ds_write_b64 v62, v[64:65]
	v_mov_b32_e32 v62, 0xc600
	v_pk_fma_f32 v[60:61], v[86:87], v[44:45], v[60:61] op_sel_hi:[0,1,1]
	v_pk_fma_f32 v[58:59], v[86:87], v[42:43], v[58:59] op_sel_hi:[0,1,1]
	v_mad_u32_u24 v74, v1, s4, v62
	v_pk_mul_f32 v[60:61], v[86:87], v[60:61] op_sel:[1,0]
	v_pk_mul_f32 v[58:59], v[86:87], v[58:59] op_sel:[1,0]
	v_cvt_pk_f16_f32 v61, v60, v61
	v_cvt_pk_f16_f32 v60, v58, v59
	v_add_u32_e32 v58, v74, v106
	ds_write_b64 v58, v[60:61]
	v_mov_b32_e32 v58, 0xe700
	v_pk_fma_f32 v[52:53], v[88:89], v[44:45], v[52:53] op_sel_hi:[0,1,1]
	v_pk_fma_f32 v[50:51], v[88:89], v[42:43], v[50:51] op_sel_hi:[0,1,1]
	v_mad_u32_u24 v58, v1, s4, v58
	v_pk_mul_f32 v[52:53], v[88:89], v[52:53] op_sel:[1,0]
	v_pk_mul_f32 v[50:51], v[88:89], v[50:51] op_sel:[1,0]
	v_cvt_pk_f16_f32 v53, v52, v53
	v_cvt_pk_f16_f32 v52, v50, v51
	v_add_u32_e32 v50, v58, v106
	ds_write_b64 v50, v[52:53]
	v_or_b32_e32 v50, 0x1f200, v114
	ds_read_b64 v[50:51], v50
	v_pk_fma_f32 v[62:63], v[86:87], v[48:49], v[68:69] op_sel_hi:[0,1,1]
	v_pk_fma_f32 v[64:65], v[86:87], v[46:47], v[66:67] op_sel_hi:[0,1,1]
	v_pk_fma_f32 v[56:57], v[88:89], v[48:49], v[56:57] op_sel_hi:[0,1,1]
	v_pk_fma_f32 v[54:55], v[88:89], v[46:47], v[54:55] op_sel_hi:[0,1,1]
	v_pk_mul_f32 v[62:63], v[86:87], v[62:63] op_sel:[1,0]
	v_pk_mul_f32 v[64:65], v[86:87], v[64:65] op_sel:[1,0]
	v_pk_mul_f32 v[56:57], v[88:89], v[56:57] op_sel:[1,0]
	v_pk_mul_f32 v[54:55], v[88:89], v[54:55] op_sel:[1,0]
	v_cvt_pk_f16_f32 v63, v62, v63
	v_cvt_pk_f16_f32 v62, v64, v65
	v_add_u32_e32 v64, v74, v129
	v_cvt_pk_f16_f32 v57, v56, v57
	v_cvt_pk_f16_f32 v56, v54, v55
	v_add_u32_e32 v54, v58, v129
	v_mov_b32_e32 v52, 0x10800
	ds_write_b64 v64, v[62:63]
	ds_write_b64 v54, v[56:57]
	v_mad_u32_u24 v58, v1, s4, v52
	v_or_b32_e32 v52, 0x1f280, v114
	v_or_b32_e32 v54, 0x1f300, v114
	v_or_b32_e32 v56, 0x1f380, v114
	ds_read_b64 v[52:53], v52
	ds_read_b64 v[54:55], v54
	ds_read_b64 v[56:57], v56
	s_waitcnt lgkmcnt(5)
	v_pk_fma_f32 v[36:37], v[50:51], v[44:45], v[36:37] op_sel_hi:[0,1,1]
	v_pk_fma_f32 v[34:35], v[50:51], v[42:43], v[34:35] op_sel_hi:[0,1,1]
	v_pk_mul_f32 v[36:37], v[50:51], v[36:37] op_sel:[1,0]
	v_pk_mul_f32 v[34:35], v[50:51], v[34:35] op_sel:[1,0]
	v_cvt_pk_f16_f32 v37, v36, v37
	v_cvt_pk_f16_f32 v36, v34, v35
	v_add_u32_e32 v34, v58, v106
	v_pk_fma_f32 v[40:41], v[50:51], v[48:49], v[40:41] op_sel_hi:[0,1,1]
	v_pk_fma_f32 v[38:39], v[50:51], v[46:47], v[38:39] op_sel_hi:[0,1,1]
	ds_write_b64 v34, v[36:37]
	v_mov_b32_e32 v34, 0x12900
	s_waitcnt lgkmcnt(3)
	v_pk_fma_f32 v[20:21], v[52:53], v[44:45], v[20:21] op_sel_hi:[0,1,1]
	v_pk_fma_f32 v[18:19], v[52:53], v[42:43], v[18:19] op_sel_hi:[0,1,1]
	v_pk_mul_f32 v[40:41], v[50:51], v[40:41] op_sel:[1,0]
	v_pk_mul_f32 v[38:39], v[50:51], v[38:39] op_sel:[1,0]
	v_mad_u32_u24 v34, v1, s4, v34
	v_pk_fma_f32 v[32:33], v[52:53], v[48:49], v[32:33] op_sel_hi:[0,1,1]
	v_pk_fma_f32 v[30:31], v[52:53], v[46:47], v[30:31] op_sel_hi:[0,1,1]
	v_pk_mul_f32 v[20:21], v[52:53], v[20:21] op_sel:[1,0]
	v_pk_mul_f32 v[18:19], v[52:53], v[18:19] op_sel:[1,0]
	v_cvt_pk_f16_f32 v41, v40, v41
	v_cvt_pk_f16_f32 v40, v38, v39
	v_add_u32_e32 v38, v58, v129
	v_pk_mul_f32 v[32:33], v[52:53], v[32:33] op_sel:[1,0]
	v_pk_mul_f32 v[30:31], v[52:53], v[30:31] op_sel:[1,0]
	v_cvt_pk_f16_f32 v21, v20, v21
	v_cvt_pk_f16_f32 v20, v18, v19
	v_add_u32_e32 v18, v34, v106
	ds_write_b64 v38, v[40:41]
	v_cvt_pk_f16_f32 v33, v32, v33
	v_cvt_pk_f16_f32 v32, v30, v31
	v_add_u32_e32 v30, v34, v129
	ds_write_b64 v18, v[20:21]
	v_mov_b32_e32 v18, 0x14a00
	ds_write_b64 v30, v[32:33]
	v_mad_u32_u24 v30, v1, s4, v18
	s_waitcnt lgkmcnt(5)
	v_pk_fma_f32 v[18:19], v[54:55], v[112:113], v[24:25] op_sel_hi:[0,1,1]
	v_pk_fma_f32 v[20:21], v[54:55], v[110:111], v[22:23] op_sel_hi:[0,1,1]
	v_pk_mul_f32 v[18:19], v[54:55], v[18:19] op_sel:[1,0]
	v_pk_mul_f32 v[20:21], v[54:55], v[20:21] op_sel:[1,0]
	v_cvt_pk_f16_f32 v19, v18, v19
	v_cvt_pk_f16_f32 v18, v20, v21
	v_add_u32_e32 v20, v30, v129
	s_waitcnt lgkmcnt(4)
	v_pk_fma_f32 v[12:13], v[56:57], v[72:73], v[12:13] op_sel_hi:[0,1,1]
	v_pk_fma_f32 v[10:11], v[56:57], v[70:71], v[10:11] op_sel_hi:[0,1,1]
	ds_write_b64 v20, v[18:19]
	v_pk_fma_f32 v[18:19], v[54:55], v[72:73], v[28:29] op_sel_hi:[0,1,1]
	v_pk_fma_f32 v[20:21], v[54:55], v[70:71], v[26:27] op_sel_hi:[0,1,1]
	v_pk_mul_f32 v[12:13], v[56:57], v[12:13] op_sel:[1,0]
	v_pk_mul_f32 v[10:11], v[56:57], v[10:11] op_sel:[1,0]
	v_pk_mul_f32 v[18:19], v[54:55], v[18:19] op_sel:[1,0]
	v_pk_mul_f32 v[20:21], v[54:55], v[20:21] op_sel:[1,0]
	v_cvt_pk_f16_f32 v13, v12, v13
	v_cvt_pk_f16_f32 v12, v10, v11
	v_or_b32_e32 v10, 0x1f400, v114
	v_cvt_pk_f16_f32 v19, v18, v19
	v_cvt_pk_f16_f32 v18, v20, v21
	v_add_u32_e32 v20, v30, v106
	ds_read_b64 v[10:11], v10
	ds_write_b64 v20, v[18:19]
	v_mov_b32_e32 v18, 0x16b00
	v_pk_fma_f32 v[16:17], v[56:57], v[112:113], v[16:17] op_sel_hi:[0,1,1]
	v_pk_fma_f32 v[14:15], v[56:57], v[110:111], v[14:15] op_sel_hi:[0,1,1]
	v_mad_u32_u24 v18, v1, s4, v18
	v_pk_mul_f32 v[16:17], v[56:57], v[16:17] op_sel:[1,0]
	v_pk_mul_f32 v[14:15], v[56:57], v[14:15] op_sel:[1,0]
	v_cvt_pk_f16_f32 v17, v16, v17
	v_cvt_pk_f16_f32 v16, v14, v15
	v_add_u32_e32 v14, v18, v129
	ds_write_b64 v14, v[16:17]
	v_add_u32_e32 v14, v18, v106
	ds_write_b64 v14, v[12:13]
	v_mov_b32_e32 v12, 0x18c00
	s_waitcnt lgkmcnt(3)
	v_pk_fma_f32 v[8:9], v[10:11], v[112:113], v[8:9] op_sel_hi:[0,1,1]
	v_pk_fma_f32 v[6:7], v[10:11], v[110:111], v[6:7] op_sel_hi:[0,1,1]
	v_pk_fma_f32 v[4:5], v[10:11], v[72:73], v[4:5] op_sel_hi:[0,1,1]
	v_pk_fma_f32 v[2:3], v[10:11], v[70:71], v[2:3] op_sel_hi:[0,1,1]
	v_mad_u32_u24 v1, v1, s4, v12
	v_pk_mul_f32 v[8:9], v[10:11], v[8:9] op_sel:[1,0]
	v_pk_mul_f32 v[6:7], v[10:11], v[6:7] op_sel:[1,0]
	v_pk_mul_f32 v[4:5], v[10:11], v[4:5] op_sel:[1,0]
	v_pk_mul_f32 v[2:3], v[10:11], v[2:3] op_sel:[1,0]
	v_cvt_pk_f16_f32 v9, v8, v9
	v_cvt_pk_f16_f32 v8, v6, v7
	v_add_u32_e32 v6, v1, v129
	v_cvt_pk_f16_f32 v5, v4, v5
	v_cvt_pk_f16_f32 v4, v2, v3
	v_add_u32_e32 v1, v1, v106
	ds_write_b64 v6, v[8:9]
	ds_write_b64 v1, v[4:5]
	s_waitcnt lgkmcnt(0)
	s_barrier
	s_and_saveexec_b64 s[0:1], vcc
	s_cbranch_execz .LBB2_12
	v_lshlrev_b32_e32 v1, 4, v0
	v_and_b32_e32 v114, 0x70, v1
	v_lshl_add_u64 v[2:3], s[6:7], 0, v[114:115]
	s_mov_b64 s[0:1], 0
	s_mov_b32 s5, 0x5397829d
	s_movk_i32 s6, 0xf9e0
	s_mov_b32 s7, 0xc350
	s_movk_i32 s8, 0x167f
	s_branch .LBB2_10

	.amdhsa_kernel _Z6k_gemmPKfPKDv8_DF16_S0_S0_PDF16_
		.amdhsa_group_segment_fixed_size 129152
		.amdhsa_private_segment_fixed_size 0
		.amdhsa_kernarg_size 40
		.amdhsa_user_sgpr_count 2
		.amdhsa_user_sgpr_dispatch_ptr 0
		.amdhsa_user_sgpr_queue_ptr 0
		.amdhsa_user_sgpr_kernarg_segment_ptr 1
		.amdhsa_user_sgpr_dispatch_id 0
		.amdhsa_user_sgpr_kernarg_preload_length 0
		.amdhsa_user_sgpr_kernarg_preload_offset 0
		.amdhsa_user_sgpr_private_segment_size 0
		.amdhsa_uses_dynamic_stack 0
		.amdhsa_enable_private_segment 0
		.amdhsa_system_sgpr_workgroup_id_x 1
		.amdhsa_system_sgpr_workgroup_id_y 0
		.amdhsa_system_sgpr_workgroup_id_z 0
		.amdhsa_system_sgpr_workgroup_info 0
		.amdhsa_system_vgpr_workitem_id 0
		.amdhsa_next_free_vgpr 252
		.amdhsa_next_free_sgpr 96
		.amdhsa_accum_offset 252
		.amdhsa_reserve_vcc 1
		.amdhsa_float_round_mode_32 0
		.amdhsa_float_round_mode_16_64 0
		.amdhsa_float_denorm_mode_32 3
		.amdhsa_float_denorm_mode_16_64 3
		.amdhsa_dx10_clamp 1
		.amdhsa_ieee_mode 1
		.amdhsa_fp16_overflow 0
		.amdhsa_tg_split 0
		.amdhsa_exception_fp_ieee_invalid_op 0
		.amdhsa_exception_fp_denorm_src 0
		.amdhsa_exception_fp_ieee_div_zero 0
		.amdhsa_exception_fp_ieee_overflow 0
		.amdhsa_exception_fp_ieee_underflow 0
		.amdhsa_exception_fp_ieee_inexact 0
		.amdhsa_exception_int_div_zero 0
	.end_amdhsa_kernel

amdhsa.kernels:
  - .agpr_count:     0
    .args:
      - .actual_access:  read_only
        .address_space:  global
        .offset:         0
        .size:           8
        .value_kind:     global_buffer
      - .actual_access:  write_only
        .address_space:  global
        .offset:         8
        .size:           8
        .value_kind:     global_buffer
      - .actual_access:  write_only
        .address_space:  global
        .offset:         16
        .size:           8
        .value_kind:     global_buffer
      - .actual_access:  read_only
        .address_space:  global
        .offset:         24
        .size:           8
        .value_kind:     global_buffer
      - .actual_access:  write_only
        .address_space:  global
        .offset:         32
        .size:           8
        .value_kind:     global_buffer
      - .actual_access:  write_only
        .address_space:  global
        .offset:         40
        .size:           8
        .value_kind:     global_buffer
    .group_segment_fixed_size: 14576
    .kernarg_segment_align: 8
    .kernarg_segment_size: 48
    .language:       OpenCL C
    .language_version:
      - 2
      - 0
    .max_flat_workgroup_size: 256
    .name:           _Z5k_binPKiPiPjPKfPDv8_DF16_PDF16_
    .private_segment_fixed_size: 0
    .sgpr_count:     22
    .sgpr_spill_count: 0
    .symbol:         _Z5k_binPKiPiPjPKfPDv8_DF16_PDF16_.kd
    .uniform_work_group_size: 1
    .uses_dynamic_stack: false
    .vgpr_count:     75
    .vgpr_spill_count: 0
    .wavefront_size: 64
  - .agpr_count:     0
    .args:
      - .actual_access:  read_only
        .address_space:  global
        .offset:         0
        .size:           8
        .value_kind:     global_buffer
      - .actual_access:  read_only
        .address_space:  global
        .offset:         8
        .size:           8
        .value_kind:     global_buffer
      - .actual_access:  write_only
        .address_space:  global
        .offset:         16
        .size:           8
        .value_kind:     global_buffer
      - .actual_access:  write_only
        .address_space:  global
        .offset:         24
        .size:           8
        .value_kind:     global_buffer
      - .actual_access:  write_only
        .address_space:  global
        .offset:         32
        .size:           8
        .value_kind:     global_buffer
      - .actual_access:  write_only
        .address_space:  global
        .offset:         40
        .size:           8
        .value_kind:     global_buffer
    .group_segment_fixed_size: 18452
    .kernarg_segment_align: 8
    .kernarg_segment_size: 48
    .language:       OpenCL C
    .language_version:
      - 2
      - 0
    .max_flat_workgroup_size: 256
    .name:           _Z5k_csrPKiPKjP15HIP_vector_typeIiLj2EEPfPtS6_
    .private_segment_fixed_size: 0
    .sgpr_count:     94
    .sgpr_spill_count: 0
    .symbol:         _Z5k_csrPKiPKjP15HIP_vector_typeIiLj2EEPfPtS6_.kd
    .uniform_work_group_size: 1
    .uses_dynamic_stack: false
    .vgpr_count:     65
    .vgpr_spill_count: 0
    .wavefront_size: 64
  - .agpr_count:     0
    .args:
      - .actual_access:  read_only
        .address_space:  global
        .offset:         0
        .size:           8
        .value_kind:     global_buffer
      - .actual_access:  read_only
        .address_space:  global
        .offset:         8
        .size:           8
        .value_kind:     global_buffer
      - .actual_access:  read_only
        .address_space:  global
        .offset:         16
        .size:           8
        .value_kind:     global_buffer
      - .actual_access:  read_only
        .address_space:  global
        .offset:         24
        .size:           8
        .value_kind:     global_buffer
      - .actual_access:  write_only
        .address_space:  global
        .offset:         32
        .size:           8
        .value_kind:     global_buffer
    .group_segment_fixed_size: 129152
    .kernarg_segment_align: 8
    .kernarg_segment_size: 40
    .language:       OpenCL C
    .language_version:
      - 2
      - 0
    .max_flat_workgroup_size: 512
    .name:           _Z6k_gemmPKfPKDv8_DF16_S0_S0_PDF16_
    .private_segment_fixed_size: 0
    .sgpr_count:     22
    .sgpr_spill_count: 0
    .symbol:         _Z6k_gemmPKfPKDv8_DF16_S0_S0_PDF16_.kd
    .uniform_work_group_size: 1
    .uses_dynamic_stack: false
    .vgpr_count:     252
    .vgpr_spill_count: 0
    .wavefront_size: 64
  - .agpr_count:     0
    .args:
      - .actual_access:  read_only
        .address_space:  global
        .offset:         0
        .size:           8
        .value_kind:     global_buffer
      - .actual_access:  read_only
        .address_space:  global
        .offset:         8
        .size:           8
        .value_kind:     global_buffer
      - .actual_access:  read_only
        .address_space:  global
        .offset:         16
        .size:           8
        .value_kind:     global_buffer
      - .actual_access:  read_only
        .address_space:  global
        .offset:         24
        .size:           8
        .value_kind:     global_buffer
      - .actual_access:  read_only
        .address_space:  global
        .offset:         32
        .size:           8
        .value_kind:     global_buffer
      - .actual_access:  read_only
        .address_space:  global
        .offset:         40
        .size:           8
        .value_kind:     global_buffer
      - .address_space:  global
        .offset:         48
        .size:           8
        .value_kind:     global_buffer
    .group_segment_fixed_size: 2304
    .kernarg_segment_align: 8
    .kernarg_segment_size: 56
    .language:       OpenCL C
    .language_version:
      - 2
      - 0
    .max_flat_workgroup_size: 320
    .name:           _Z6k_agg1PKDF16_PK15HIP_vector_typeIiLj2EEPKtPKfS8_S8_Pf
    .private_segment_fixed_size: 0
    .sgpr_count:     40
    .sgpr_spill_count: 0
    .symbol:         _Z6k_agg1PKDF16_PK15HIP_vector_typeIiLj2EEPKtPKfS8_S8_Pf.kd
    .uniform_work_group_size: 1
    .uses_dynamic_stack: false
    .vgpr_count:     62
    .vgpr_spill_count: 0
    .wavefront_size: 64
  - .agpr_count:     0
    .args:
      - .actual_access:  read_only
        .address_space:  global
        .offset:         0
        .size:           8
        .value_kind:     global_buffer
      - .actual_access:  read_only
        .address_space:  global
        .offset:         8
        .size:           8
        .value_kind:     global_buffer
      - .actual_access:  read_only
        .address_space:  global
        .offset:         16
        .size:           8
        .value_kind:     global_buffer
      - .actual_access:  read_only
        .address_space:  global
        .offset:         24
        .size:           8
        .value_kind:     global_buffer
      - .actual_access:  read_only
        .address_space:  global
        .offset:         32
        .size:           8
        .value_kind:     global_buffer
      - .actual_access:  write_only
        .address_space:  global
        .offset:         40
        .size:           8
        .value_kind:     global_buffer
    .group_segment_fixed_size: 0
    .kernarg_segment_align: 8
    .kernarg_segment_size: 48
    .language:       OpenCL C
    .language_version:
      - 2
      - 0
    .max_flat_workgroup_size: 256
    .name:           _Z5k_outPKfPK15HIP_vector_typeIiLj2EEPKtS0_S0_Pf
    .private_segment_fixed_size: 0
    .sgpr_count:     18
    .sgpr_spill_count: 0
    .symbol:         _Z5k_outPKfPK15HIP_vector_typeIiLj2EEPKtS0_S0_Pf.kd
    .uniform_work_group_size: 1
    .uses_dynamic_stack: false
    .vgpr_count:     27
    .vgpr_spill_count: 0
    .wavefront_size: 64
